# baseline (speedup 1.0000x reference)
_Z11jacobi_mainPKfS0_S0_PyPf:
	s_lshl_b32 s3, s2, 3
	s_load_dwordx4 s[12:15], s[0:1], 0x0
	s_load_dwordx2 s[4:5], s[0:1], 0x10
	s_and_b32 s3, s3, 56
	s_ashr_i32 s33, s2, 5
	v_readfirstlane_b32 s40, v0
	s_add_i32 s18, s3, s33
	s_bfe_u32 s3, s2, 0x20003
	s_lshl_b32 s7, s3, 8
	s_and_b32 s10, s40, 0xffffffc0
	s_ashr_i32 s19, s18, 31
	s_lshr_b32 s34, s2, 3
	s_add_i32 s11, s10, s7
	s_lshl_b64 s[8:9], s[18:19], 22
	v_and_b32_e32 v206, 63, v0
	s_waitcnt lgkmcnt(0)
	s_add_u32 s8, s12, s8
	s_addc_u32 s9, s13, s9
	v_or_b32_e32 v154, s11, v206
	s_lshl_b32 s6, s18, 10
	v_add_u32_e32 v2, s6, v154
	v_ashrrev_i32_e32 v3, 31, v2
	v_lshlrev_b64 v[2:3], 2, v[2:3]
	v_lshl_add_u64 v[4:5], s[14:15], 0, v[2:3]
	global_load_dword v1, v[4:5], off
	s_movk_i32 s12, 0x1004
	v_mov_b64_e32 v[4:5], s[8:9]
	v_mad_i64_i32 v[4:5], s[12:13], v154, s12, v[4:5]
	v_lshl_add_u64 v[2:3], s[4:5], 0, v[2:3]
	global_load_dword v207, v[4:5], off
	global_load_dword v66, v[2:3], off
	s_lshl_b32 s76, s6, 2
	s_add_u32 s76, s4, s76
	s_addc_u32 s77, s5, 0
	v_lshlrev_b32_e32 v220, 4, v0
	global_load_dwordx4 v[224:227], v220, s[76:77]
	s_load_dwordx2 s[16:17], s[0:1], 0x20
	v_ashrrev_i32_e32 v155, 31, v154
	s_mov_b32 s21, 0
	s_lshr_b32 s35, s40, 6
	v_cmp_eq_u32_e64 s[12:13], 0, v206
	s_load_dwordx2 s[0:1], s[0:1], 0x18
	v_lshrrev_b32_e32 v67, 5, v206
	v_or_b32_e32 v132, s11, v67
	s_lshl_b64 s[14:15], s[18:19], 14
	v_ashrrev_i32_e32 v133, 31, v132
	v_and_b32_e32 v124, 31, v0
	s_waitcnt lgkmcnt(0)
	s_add_u32 s14, s0, s14
	v_lshlrev_b64 v[2:3], 12, v[132:133]
	s_addc_u32 s15, s1, s15
	s_add_i32 s0, s7, 0x100
	v_lshl_add_u64 v[2:3], s[8:9], 0, v[2:3]
	v_lshlrev_b32_e32 v190, 4, v124
	v_mov_b32_e32 v191, 0
	s_and_b32 s26, s0, 0x300
	v_lshl_add_u64 v[130:131], v[2:3], 0, v[190:191]
	s_mov_b64 s[0:1], 0x30000
	v_lshl_add_u64 v[126:127], v[130:131], 0, s[0:1]
	s_mov_b64 s[0:1], 0x32000
	v_lshl_add_u64 v[128:129], v[130:131], 0, s[0:1]
	s_mov_b64 s[0:1], 0x34000
	v_lshl_add_u64 v[134:135], v[130:131], 0, s[0:1]
	s_mov_b64 s[0:1], 0x36000
	v_lshl_add_u64 v[136:137], v[130:131], 0, s[0:1]
	s_mov_b64 s[0:1], 0x38000
	v_lshl_add_u64 v[138:139], v[130:131], 0, s[0:1]
	s_mov_b64 s[0:1], 0x3a000
	v_lshl_add_u64 v[140:141], v[130:131], 0, s[0:1]
	s_mov_b64 s[0:1], 0x3c000
	s_or_b32 s24, s7, 0x80
	v_lshl_add_u64 v[142:143], v[130:131], 0, s[0:1]
	s_mov_b64 s[0:1], 0x3e000
	s_lshl_b32 s20, s7, 2
	v_lshl_add_u64 v[144:145], v[130:131], 0, s[0:1]
	s_lshl_b32 s8, s24, 2
	s_mov_b32 s9, s21
	v_lshl_add_u64 v[2:3], v[126:127], 0, s[20:21]
	v_lshl_add_u64 v[4:5], v[128:129], 0, s[20:21]
	v_lshl_add_u64 v[6:7], v[134:135], 0, s[20:21]
	v_lshl_add_u64 v[8:9], v[136:137], 0, s[20:21]
	v_lshl_add_u64 v[10:11], v[138:139], 0, s[20:21]
	v_lshl_add_u64 v[12:13], v[140:141], 0, s[20:21]
	v_lshl_add_u64 v[14:15], v[142:143], 0, s[20:21]
	v_lshl_add_u64 v[16:17], v[144:145], 0, s[20:21]
	v_lshl_add_u64 v[18:19], v[126:127], 0, s[8:9]
	v_lshl_add_u64 v[20:21], v[128:129], 0, s[8:9]
	v_lshl_add_u64 v[22:23], v[134:135], 0, s[8:9]
	v_lshl_add_u64 v[24:25], v[136:137], 0, s[8:9]
	s_lshl_b32 s0, s26, 2
	s_mov_b32 s1, s21
	v_lshl_add_u64 v[72:73], v[138:139], 0, s[8:9]
	v_lshl_add_u64 v[102:103], v[140:141], 0, s[8:9]
	v_lshl_add_u64 v[104:105], v[142:143], 0, s[8:9]
	v_lshl_add_u64 v[106:107], v[144:145], 0, s[8:9]
	v_lshl_add_u64 v[108:109], v[126:127], 0, s[0:1]
	v_lshl_add_u64 v[110:111], v[128:129], 0, s[0:1]
	v_lshl_add_u64 v[112:113], v[134:135], 0, s[0:1]
	v_lshl_add_u64 v[114:115], v[136:137], 0, s[0:1]
	v_lshl_add_u64 v[116:117], v[138:139], 0, s[0:1]
	v_lshl_add_u64 v[118:119], v[140:141], 0, s[0:1]
	v_lshl_add_u64 v[120:121], v[142:143], 0, s[0:1]
	v_lshl_add_u64 v[122:123], v[144:145], 0, s[0:1]
	global_load_dwordx4 v[68:71], v[2:3], off nt
	global_load_dwordx4 v[78:81], v[4:5], off nt
	global_load_dwordx4 v[82:85], v[6:7], off nt
	global_load_dwordx4 v[90:93], v[8:9], off nt
	global_load_dwordx4 v[98:101], v[10:11], off nt
	global_load_dwordx4 v[62:65], v[12:13], off nt
	global_load_dwordx4 v[54:57], v[14:15], off nt
	global_load_dwordx4 v[46:49], v[16:17], off nt
	global_load_dwordx4 v[94:97], v[18:19], off nt
	global_load_dwordx4 v[86:89], v[20:21], off nt
	global_load_dwordx4 v[74:77], v[22:23], off nt
	global_load_dwordx4 v[58:61], v[24:25], off nt
	global_load_dwordx4 v[50:53], v[72:73], off nt
	global_load_dwordx4 v[42:45], v[102:103], off nt
	global_load_dwordx4 v[38:41], v[104:105], off nt
	global_load_dwordx4 v[34:37], v[106:107], off nt
	global_load_dwordx4 v[30:33], v[108:109], off nt
	global_load_dwordx4 v[26:29], v[110:111], off nt
	s_nop 0
	global_load_dwordx4 v[22:25], v[112:113], off nt
	global_load_dwordx4 v[18:21], v[114:115], off nt
	global_load_dwordx4 v[14:17], v[116:117], off nt
	global_load_dwordx4 v[10:13], v[118:119], off nt
	global_load_dwordx4 v[6:9], v[120:121], off nt
	global_load_dwordx4 v[2:5], v[122:123], off nt
	s_waitcnt vmcnt(25)
	v_div_scale_f32 v72, s[22:23], v207, v207, 1.0
	v_rcp_f32_e32 v73, v72
	s_lshl_b32 s11, s10, 2
	s_mul_i32 s19, s35, 0x1100
	s_add_i32 s22, s11, 0x26600
	v_fma_f32 v103, -v72, v73, 1.0
	v_fmac_f32_e32 v73, v103, v73
	v_div_scale_f32 v103, vcc, 1.0, v207, 1.0
	v_mul_f32_e32 v104, v103, v73
	v_fma_f32 v105, -v72, v104, v103
	v_fmac_f32_e32 v104, v105, v73
	v_fma_f32 v72, -v72, v104, v103
	v_div_fmas_f32 v72, v72, v73, v104
	v_div_fixup_f32 v72, v72, v207, 1.0
	s_waitcnt vmcnt(24)
	v_fma_f32 v208, v72, v1, -v66
	v_mbcnt_lo_u32_b32 v244, -1, 0
	v_mbcnt_hi_u32_b32 v244, -1, v244
	v_and_b32_e32 v245, 64, v244
	v_xor_b32_e32 v246, 32, v244
	v_add_u32_e32 v245, 64, v245
	v_cmp_lt_i32_e32 vcc, v246, v245
	v_xor_b32_e32 v248, 8, v244
	s_nop 0
	v_cndmask_b32_e32 v246, v244, v246, vcc
	v_lshlrev_b32_e32 v246, 2, v246
	v_mul_f32_e32 v247, v1, v1
	ds_bpermute_b32 v246, v246, v247
	v_xor_b32_e32 v247, 16, v244
	v_cmp_lt_i32_e32 vcc, v247, v245
	s_waitcnt lgkmcnt(0)
	v_fmac_f32_e32 v246, v1, v1
	v_cndmask_b32_e32 v247, v244, v247, vcc
	v_lshlrev_b32_e32 v247, 2, v247
	ds_bpermute_b32 v247, v247, v246
	v_cmp_lt_i32_e32 vcc, v248, v245
	s_waitcnt lgkmcnt(0)
	v_add_f32_e32 v246, v246, v247
	v_cndmask_b32_e32 v248, v244, v248, vcc
	v_lshlrev_b32_e32 v248, 2, v248
	ds_bpermute_b32 v247, v248, v246
	v_xor_b32_e32 v248, 4, v244
	v_cmp_lt_i32_e32 vcc, v248, v245
	s_waitcnt lgkmcnt(0)
	v_add_f32_e32 v246, v246, v247
	v_cndmask_b32_e32 v248, v244, v248, vcc
	v_lshlrev_b32_e32 v248, 2, v248
	ds_bpermute_b32 v247, v248, v246
	v_xor_b32_e32 v248, 2, v244
	v_cmp_lt_i32_e32 vcc, v248, v245
	s_waitcnt lgkmcnt(0)
	v_add_f32_e32 v246, v246, v247
	v_cndmask_b32_e32 v248, v244, v248, vcc
	v_lshlrev_b32_e32 v248, 2, v248
	ds_bpermute_b32 v247, v248, v246
	v_xor_b32_e32 v248, 1, v244
	v_cmp_lt_i32_e32 vcc, v248, v245
	s_nop 1
	v_cndmask_b32_e32 v245, v244, v248, vcc
	s_waitcnt lgkmcnt(0)
	v_add_f32_e32 v244, v246, v247
	v_lshlrev_b32_e32 v245, 2, v245
	ds_bpermute_b32 v245, v245, v244
	s_and_saveexec_b64 s[80:81], s[12:13]
	s_cbranch_execz .LBB0_2
	s_lshl_b32 s82, s35, 2
	s_add_i32 s82, s82, 0x26a00
	s_waitcnt lgkmcnt(0)
	v_add_f32_e32 v244, v244, v245
	v_mov_b32_e32 v245, s82
	ds_write_b32 v245, v244
.LBB0_2:
	s_or_b64 exec, exec, s[80:81]
	v_lshl_add_u32 v1, v206, 2, s22
	s_add_i32 s19, s19, 0x22200
	ds_write_b32 v1, v72
	v_lshl_or_b32 v1, v124, 3, s19
	v_lshl_add_u32 v187, v67, 2, s22
	s_movk_i32 s22, 0x110
	v_mad_u32_u24 v186, v67, s22, v1
	s_add_i32 s22, s7, 0x180
	v_and_b32_e32 v102, 15, v0
	s_lshl_b32 s27, s34, 8
	s_and_b32 s25, s22, 0x380
	s_add_i32 s22, s7, 0x280
	v_lshlrev_b32_e32 v66, 2, v124
	v_mul_u32_u24_e32 v1, 0x110, v102
	v_and_b32_e32 v209, 48, v0
	s_and_b32 s23, s22, 0x380
	s_add_i32 s22, s7, 0x300
	v_mov_b32_e32 v67, 0x200
	s_addk_i32 s27, 0x380
	v_or_b32_e32 v133, s7, v66
	v_add3_u32 v1, s19, v1, v209
	s_lshl_b32 s19, s35, 15
	v_lshlrev_b32_e32 v210, 4, v206
	v_or_b32_e32 v189, s24, v66
	s_xor_b32 s24, s7, 0x200
	s_and_b32 s22, s22, 0x300
	v_bitop3_b32 v197, s7, v66, v67 bitop3:0xde
	s_and_b32 s7, s27, 0x380
	v_lshrrev_b32_e32 v185, 4, v206
	s_ashr_i32 s11, s10, 31
	v_or_b32_e32 v184, s19, v210
	v_or_b32_e32 v188, s26, v66
	v_or_b32_e32 v198, s25, v66
	v_or_b32_e32 v196, s23, v66
	v_or_b32_e32 v195, s22, v66
	v_or_b32_e32 v194, s7, v66
	v_mov_b32_e32 v102, v133
	v_and_b32_e32 v248, 2, v206
	v_cmp_ne_u32_e32 vcc, 0, v248
	v_mov_b32_e32 v249, 0x44444444
	v_mov_b32_e32 v250, 0xeeeeeeee
	s_nop 1
	v_cndmask_b32_e32 v223, v249, v250, vcc
	v_lshrrev_b32_e32 v248, 4, v206
	v_lshl_add_u32 v248, v248, 4, 1
	v_add_u32_e32 v249, 0, v248
	v_cvt_f32_u32_e32 v249, v249
	v_add_u32_e32 v250, 1, v248
	v_cvt_f32_u32_e32 v250, v250
	v_cvt_pk_bf16_f32 v232, v249, v250
	v_add_u32_e32 v249, 2, v248
	v_cvt_f32_u32_e32 v249, v249
	v_add_u32_e32 v250, 3, v248
	v_cvt_f32_u32_e32 v250, v250
	v_cvt_pk_bf16_f32 v233, v249, v250
	v_add_u32_e32 v249, 4, v248
	v_cvt_f32_u32_e32 v249, v249
	v_add_u32_e32 v250, 5, v248
	v_cvt_f32_u32_e32 v250, v250
	v_cvt_pk_bf16_f32 v234, v249, v250
	v_add_u32_e32 v249, 6, v248
	v_cvt_f32_u32_e32 v249, v249
	v_add_u32_e32 v250, 7, v248
	v_cvt_f32_u32_e32 v250, v250
	v_cvt_pk_bf16_f32 v235, v249, v250
	v_add_u32_e32 v249, 8, v248
	v_cvt_f32_u32_e32 v249, v249
	v_add_u32_e32 v250, 9, v248
	v_cvt_f32_u32_e32 v250, v250
	v_cvt_pk_bf16_f32 v236, v249, v250
	v_add_u32_e32 v249, 10, v248
	v_cvt_f32_u32_e32 v249, v249
	v_add_u32_e32 v250, 11, v248
	v_cvt_f32_u32_e32 v250, v250
	v_cvt_pk_bf16_f32 v237, v249, v250
	v_add_u32_e32 v249, 12, v248
	v_cvt_f32_u32_e32 v249, v249
	v_add_u32_e32 v250, 13, v248
	v_cvt_f32_u32_e32 v250, v250
	v_cvt_pk_bf16_f32 v238, v249, v250
	v_add_u32_e32 v249, 14, v248
	v_cvt_f32_u32_e32 v249, v249
	v_add_u32_e32 v250, 15, v248
	v_cvt_f32_u32_e32 v250, v250
	v_cvt_pk_bf16_f32 v239, v249, v250
	v_and_b32_e32 v248, 15, v206
	v_lshrrev_b32_e32 v249, 2, v248
	v_and_b32_e32 v250, 1, v248
	v_lshl_add_u32 v249, v249, 1, v250
	v_and_b32_e32 v250, 3, v249
	v_lshrrev_b32_e32 v251, 4, v206
	v_cmp_eq_u32_e32 vcc, v250, v251
	v_lshrrev_b32_e32 v249, 2, v249
	v_cmp_ne_u32_e64 s[78:79], 0, v249
	v_mov_b32_e32 v250, 0x3f80
	v_mov_b32_e32 v251, 0x3f800000
	s_nop 1
	v_cndmask_b32_e64 v250, v250, v251, s[78:79]
	v_cndmask_b32_e32 v252, 0, v250, vcc
	s_lshr_b32 s77, s19, 15
	s_mulk_i32 s77, 0x1100
	s_add_i32 s77, s77, 0x22200
	v_lshrrev_b32_e32 v248, 4, v206
	v_and_b32_e32 v249, 1, v248
	v_lshrrev_b32_e32 v250, 1, v248
	v_lshlrev_b32_e32 v249, 6, v249
	v_lshl_add_u32 v253, v250, 1, v249
	v_and_b32_e32 v248, 15, v206
	v_cmp_eq_u32_e64 s[78:79], 0, v248
	v_mov_b32_e32 v244, v252
	v_mov_b32_e32 v245, 0
	v_mov_b32_e32 v246, 0
	v_mov_b32_e32 v247, 0
	v_mov_b64_e32 v[240:241], 0
	v_mov_b64_e32 v[242:243], 0
	s_nop 1
	v_smfmac_f32_16x16x64_bf16 v[240:243], v[244:247], v[232:239], v223
	s_nop 15
	s_nop 3
	s_and_saveexec_b64 s[80:81], s[78:79]
	v_cvt_u32_f32_e32 v248, v240
	v_add_u32_e32 v248, -1, v248
	v_lshl_add_u32 v248, v248, 2, s77
	v_add_u32_e32 v249, 0, v253
	ds_write_b32 v248, v249
	v_cvt_u32_f32_e32 v248, v241
	v_add_u32_e32 v248, -1, v248
	v_lshl_add_u32 v248, v248, 2, s77
	v_add_u32_e32 v249, 32, v253
	ds_write_b32 v248, v249
	v_cvt_u32_f32_e32 v248, v242
	v_add_u32_e32 v248, -1, v248
	v_lshl_add_u32 v248, v248, 2, s77
	v_add_u32_e32 v249, 16, v253
	ds_write_b32 v248, v249
	v_cvt_u32_f32_e32 v248, v243
	v_add_u32_e32 v248, -1, v248
	v_lshl_add_u32 v248, v248, 2, s77
	v_add_u32_e32 v249, 48, v253
	ds_write_b32 v248, v249
	s_or_b64 exec, exec, s[80:81]
	v_mov_b32_e32 v244, 0
	v_mov_b32_e32 v245, v252
	v_mov_b32_e32 v246, 0
	v_mov_b32_e32 v247, 0
	v_mov_b64_e32 v[240:241], 0
	v_mov_b64_e32 v[242:243], 0
	s_nop 1
	v_smfmac_f32_16x16x64_bf16 v[240:243], v[244:247], v[232:239], v223
	s_nop 15
	s_nop 3
	s_and_saveexec_b64 s[80:81], s[78:79]
	v_cvt_u32_f32_e32 v248, v240
	v_add_u32_e32 v248, -1, v248
	v_lshl_add_u32 v248, v248, 2, s77
	v_add_u32_e32 v249, 4, v253
	ds_write_b32 v248, v249
	v_cvt_u32_f32_e32 v248, v241
	v_add_u32_e32 v248, -1, v248
	v_lshl_add_u32 v248, v248, 2, s77
	v_add_u32_e32 v249, 36, v253
	ds_write_b32 v248, v249
	v_cvt_u32_f32_e32 v248, v242
	v_add_u32_e32 v248, -1, v248
	v_lshl_add_u32 v248, v248, 2, s77
	v_add_u32_e32 v249, 20, v253
	ds_write_b32 v248, v249
	v_cvt_u32_f32_e32 v248, v243
	v_add_u32_e32 v248, -1, v248
	v_lshl_add_u32 v248, v248, 2, s77
	v_add_u32_e32 v249, 52, v253
	ds_write_b32 v248, v249
	s_or_b64 exec, exec, s[80:81]
	v_mov_b32_e32 v244, 0
	v_mov_b32_e32 v245, 0
	v_mov_b32_e32 v246, v252
	v_mov_b32_e32 v247, 0
	v_mov_b64_e32 v[240:241], 0
	v_mov_b64_e32 v[242:243], 0
	s_nop 1
	v_smfmac_f32_16x16x64_bf16 v[240:243], v[244:247], v[232:239], v223
	s_nop 15
	s_nop 3
	s_and_saveexec_b64 s[80:81], s[78:79]
	v_cvt_u32_f32_e32 v248, v240
	v_add_u32_e32 v248, -1, v248
	v_lshl_add_u32 v248, v248, 2, s77
	v_add_u32_e32 v249, 8, v253
	ds_write_b32 v248, v249
	v_cvt_u32_f32_e32 v248, v241
	v_add_u32_e32 v248, -1, v248
	v_lshl_add_u32 v248, v248, 2, s77
	v_add_u32_e32 v249, 40, v253
	ds_write_b32 v248, v249
	v_cvt_u32_f32_e32 v248, v242
	v_add_u32_e32 v248, -1, v248
	v_lshl_add_u32 v248, v248, 2, s77
	v_add_u32_e32 v249, 24, v253
	ds_write_b32 v248, v249
	v_cvt_u32_f32_e32 v248, v243
	v_add_u32_e32 v248, -1, v248
	v_lshl_add_u32 v248, v248, 2, s77
	v_add_u32_e32 v249, 56, v253
	ds_write_b32 v248, v249
	s_or_b64 exec, exec, s[80:81]
	v_mov_b32_e32 v244, 0
	v_mov_b32_e32 v245, 0
	v_mov_b32_e32 v246, 0
	v_mov_b32_e32 v247, v252
	v_mov_b64_e32 v[240:241], 0
	v_mov_b64_e32 v[242:243], 0
	s_nop 1
	v_smfmac_f32_16x16x64_bf16 v[240:243], v[244:247], v[232:239], v223
	s_nop 15
	s_nop 3
	s_and_saveexec_b64 s[80:81], s[78:79]
	v_cvt_u32_f32_e32 v248, v240
	v_add_u32_e32 v248, -1, v248
	v_lshl_add_u32 v248, v248, 2, s77
	v_add_u32_e32 v249, 12, v253
	ds_write_b32 v248, v249
	v_cvt_u32_f32_e32 v248, v241
	v_add_u32_e32 v248, -1, v248
	v_lshl_add_u32 v248, v248, 2, s77
	v_add_u32_e32 v249, 44, v253
	ds_write_b32 v248, v249
	v_cvt_u32_f32_e32 v248, v242
	v_add_u32_e32 v248, -1, v248
	v_lshl_add_u32 v248, v248, 2, s77
	v_add_u32_e32 v249, 28, v253
	ds_write_b32 v248, v249
	v_cvt_u32_f32_e32 v248, v243
	v_add_u32_e32 v248, -1, v248
	v_lshl_add_u32 v248, v248, 2, s77
	v_add_u32_e32 v249, 60, v253
	ds_write_b32 v248, v249
	s_or_b64 exec, exec, s[80:81]
	v_bfe_u32 v248, v206, 3, 2
	v_lshrrev_b32_e32 v249, 5, v206
	v_lshlrev_b32_e32 v248, 4, v248
	v_lshl_or_b32 v248, v249, 3, v248
	v_and_b32_e32 v249, 7, v206
	v_or_b32_e32 v248, v248, v249
	v_lshl_add_u32 v248, v248, 2, s77
	s_waitcnt lgkmcnt(0)
	ds_read_b32 v254, v248
	v_and_b32_e32 v248, 15, v206
	v_bfe_u32 v249, v248, 1, 2
	v_lshrrev_b32_e32 v250, 3, v248
	v_lshlrev_b32_e32 v249, 4, v249
	v_lshl_or_b32 v249, v250, 3, v249
	v_and_b32_e32 v250, 1, v248
	v_lshl_or_b32 v249, v250, 2, v249
	v_lshl_add_u32 v249, v249, 2, s77
	ds_read_b128 v[248:251], v249
	s_lshr_b32 s76, s19, 6
	s_add_i32 s76, s76, 0x20000
	v_lshrrev_b32_e32 v252, 4, v206
	v_lshl_add_u32 v252, v252, 7, s76
	s_waitcnt lgkmcnt(0)
	v_add_u32_e32 v248, v252, v248
	v_add_u32_e32 v249, v252, v249
	v_add_u32_e32 v250, v252, v250
	v_add_u32_e32 v251, v252, v251
	v_cvt_pk_bf16_f32 v236, v224, v225
	v_cvt_pk_bf16_f32 v237, v226, v227
	v_lshlrev_b32_e32 v238, 16, v236
	v_and_b32_e32 v239, 0xffff0000, v236
	v_lshlrev_b32_e32 v240, 16, v237
	v_and_b32_e32 v241, 0xffff0000, v237
	v_sub_f32_e32 v238, v224, v238
	v_sub_f32_e32 v239, v225, v239
	v_sub_f32_e32 v240, v226, v240
	v_sub_f32_e32 v241, v227, v241
	v_cvt_pk_bf16_f32 v238, v238, v239
	v_cvt_pk_bf16_f32 v239, v240, v241
	ds_write_b16 v248, v236
	ds_write_b16_d16_hi v249, v236
	ds_write_b16 v250, v237
	ds_write_b16_d16_hi v251, v237
	ds_write_b16 v248, v238 offset:2176
	ds_write_b16_d16_hi v249, v238 offset:2176
	ds_write_b16 v250, v239 offset:2176
	ds_write_b16_d16_hi v251, v239 offset:2176
	s_waitcnt vmcnt(23)
	s_waitcnt vmcnt(22)
	s_waitcnt vmcnt(21)
	s_waitcnt vmcnt(20)
	s_waitcnt vmcnt(19)
	s_waitcnt vmcnt(18)
	s_waitcnt vmcnt(17)
	s_waitcnt vmcnt(16)
	ds_read_b32 v66, v187 offset:192
	v_or_b32_e32 v103, 48, v132
	v_add_u32_e32 v104, 1, v102
	v_cmp_eq_u32_e32 vcc, v102, v103
	v_add_u32_e32 v105, 3, v102
	v_add_u32_e32 v106, 2, v102
	v_cndmask_b32_e64 v72, 0, 1.0, vcc
	v_cmp_eq_u32_e32 vcc, v104, v103
	v_or_b32_e32 v107, 50, v132
	v_or_b32_e32 v108, 52, v132
	v_cndmask_b32_e64 v73, 0, 1.0, vcc
	v_cmp_eq_u32_e32 vcc, v105, v103
	s_waitcnt lgkmcnt(0)
	v_pk_fma_f32 v[68:69], v[66:67], v[68:69], v[72:73] op_sel_hi:[0,1,1] neg_lo:[1,0,0] neg_hi:[1,0,0]
	v_cvt_pk_bf16_f32 v68, v68, v69
	v_cndmask_b32_e64 v73, 0, 1.0, vcc
	v_cmp_eq_u32_e32 vcc, v106, v103
	v_or_b32_e32 v109, 54, v132
	v_or_b32_e32 v110, 56, v132
	v_cndmask_b32_e64 v72, 0, 1.0, vcc
	v_pk_fma_f32 v[66:67], v[66:67], v[70:71], v[72:73] op_sel_hi:[0,1,1] neg_lo:[1,0,0] neg_hi:[1,0,0]
	v_cvt_pk_bf16_f32 v69, v66, v67
	ds_write_b64 v186, v[68:69]
	ds_read_b32 v66, v187 offset:200
	v_cmp_eq_u32_e32 vcc, v102, v107
	v_or_b32_e32 v111, 58, v132
	v_or_b32_e32 v112, 60, v132
	v_cndmask_b32_e64 v68, 0, 1.0, vcc
	v_cmp_eq_u32_e32 vcc, v104, v107
	v_or_b32_e32 v113, 62, v132
	v_or_b32_e32 v193, 2, v132
	v_cndmask_b32_e64 v69, 0, 1.0, vcc
	v_cmp_eq_u32_e32 vcc, v105, v107
	s_waitcnt lgkmcnt(0)
	v_pk_fma_f32 v[68:69], v[66:67], v[78:79], v[68:69] op_sel_hi:[0,1,1] neg_lo:[1,0,0] neg_hi:[1,0,0]
	v_cvt_pk_bf16_f32 v68, v68, v69
	v_cndmask_b32_e64 v71, 0, 1.0, vcc
	v_cmp_eq_u32_e32 vcc, v106, v107
	v_or_b32_e32 v192, 4, v132
	v_or_b32_e32 v190, 6, v132
	v_cndmask_b32_e64 v70, 0, 1.0, vcc
	v_pk_fma_f32 v[66:67], v[66:67], v[80:81], v[70:71] op_sel_hi:[0,1,1] neg_lo:[1,0,0] neg_hi:[1,0,0]
	v_cvt_pk_bf16_f32 v69, v66, v67
	ds_write_b64 v186, v[68:69] offset:544
	ds_read_b32 v66, v187 offset:208
	v_cmp_eq_u32_e32 vcc, v102, v108
	v_or_b32_e32 v149, 8, v132
	v_or_b32_e32 v148, 10, v132
	v_cndmask_b32_e64 v68, 0, 1.0, vcc
	v_cmp_eq_u32_e32 vcc, v104, v108
	v_or_b32_e32 v147, 12, v132
	v_or_b32_e32 v146, 14, v132
	v_cndmask_b32_e64 v69, 0, 1.0, vcc
	v_cmp_eq_u32_e32 vcc, v105, v108
	s_waitcnt lgkmcnt(0)
	v_pk_fma_f32 v[68:69], v[66:67], v[82:83], v[68:69] op_sel_hi:[0,1,1] neg_lo:[1,0,0] neg_hi:[1,0,0]
	v_cvt_pk_bf16_f32 v68, v68, v69
	v_cndmask_b32_e64 v71, 0, 1.0, vcc
	v_cmp_eq_u32_e32 vcc, v106, v108
	s_nop 1
	v_cndmask_b32_e64 v70, 0, 1.0, vcc
	v_pk_fma_f32 v[66:67], v[66:67], v[84:85], v[70:71] op_sel_hi:[0,1,1] neg_lo:[1,0,0] neg_hi:[1,0,0]
	v_cvt_pk_bf16_f32 v69, v66, v67
	ds_write_b64 v186, v[68:69] offset:1088
	ds_read_b32 v66, v187 offset:216
	v_cmp_eq_u32_e32 vcc, v102, v109
	s_nop 1
	v_cndmask_b32_e64 v68, 0, 1.0, vcc
	v_cmp_eq_u32_e32 vcc, v104, v109
	s_nop 1
	v_cndmask_b32_e64 v69, 0, 1.0, vcc
	v_cmp_eq_u32_e32 vcc, v105, v109
	s_waitcnt lgkmcnt(0)
	v_pk_fma_f32 v[68:69], v[66:67], v[90:91], v[68:69] op_sel_hi:[0,1,1] neg_lo:[1,0,0] neg_hi:[1,0,0]
	v_cvt_pk_bf16_f32 v68, v68, v69
	v_cndmask_b32_e64 v71, 0, 1.0, vcc
	v_cmp_eq_u32_e32 vcc, v106, v109
	s_nop 1
	v_cndmask_b32_e64 v70, 0, 1.0, vcc
	v_pk_fma_f32 v[66:67], v[66:67], v[92:93], v[70:71] op_sel_hi:[0,1,1] neg_lo:[1,0,0] neg_hi:[1,0,0]
	v_cvt_pk_bf16_f32 v69, v66, v67
	ds_write_b64 v186, v[68:69] offset:1632
	ds_read_b32 v66, v187 offset:224
	v_cmp_eq_u32_e32 vcc, v102, v110
	s_nop 1
	v_cndmask_b32_e64 v68, 0, 1.0, vcc
	v_cmp_eq_u32_e32 vcc, v104, v110
	s_nop 1
	v_cndmask_b32_e64 v69, 0, 1.0, vcc
	v_cmp_eq_u32_e32 vcc, v105, v110
	s_waitcnt lgkmcnt(0)
	v_pk_fma_f32 v[68:69], v[66:67], v[98:99], v[68:69] op_sel_hi:[0,1,1] neg_lo:[1,0,0] neg_hi:[1,0,0]
	v_cvt_pk_bf16_f32 v68, v68, v69
	v_cndmask_b32_e64 v71, 0, 1.0, vcc
	v_cmp_eq_u32_e32 vcc, v106, v110
	s_nop 1
	v_cndmask_b32_e64 v70, 0, 1.0, vcc
	v_pk_fma_f32 v[66:67], v[66:67], v[100:101], v[70:71] op_sel_hi:[0,1,1] neg_lo:[1,0,0] neg_hi:[1,0,0]
	v_cvt_pk_bf16_f32 v69, v66, v67
	ds_write_b64 v186, v[68:69] offset:2176
	ds_read_b32 v66, v187 offset:232
	v_cmp_eq_u32_e32 vcc, v102, v111
	s_nop 1
	v_cndmask_b32_e64 v68, 0, 1.0, vcc
	v_cmp_eq_u32_e32 vcc, v104, v111
	s_nop 1
	v_cndmask_b32_e64 v69, 0, 1.0, vcc
	v_cmp_eq_u32_e32 vcc, v105, v111
	s_waitcnt lgkmcnt(0)
	v_pk_fma_f32 v[62:63], v[66:67], v[62:63], v[68:69] op_sel_hi:[0,1,1] neg_lo:[1,0,0] neg_hi:[1,0,0]
	v_cvt_pk_bf16_f32 v62, v62, v63
	v_cndmask_b32_e64 v69, 0, 1.0, vcc
	v_cmp_eq_u32_e32 vcc, v106, v111
	s_nop 1
	v_cndmask_b32_e64 v68, 0, 1.0, vcc
	v_pk_fma_f32 v[64:65], v[66:67], v[64:65], v[68:69] op_sel_hi:[0,1,1] neg_lo:[1,0,0] neg_hi:[1,0,0]
	v_cvt_pk_bf16_f32 v63, v64, v65
	ds_write_b64 v186, v[62:63] offset:2720
	ds_read_b32 v62, v187 offset:240
	v_cmp_eq_u32_e32 vcc, v102, v112
	s_nop 1
	v_cndmask_b32_e64 v64, 0, 1.0, vcc
	v_cmp_eq_u32_e32 vcc, v104, v112
	s_nop 1
	v_cndmask_b32_e64 v65, 0, 1.0, vcc
	v_cmp_eq_u32_e32 vcc, v105, v112
	s_waitcnt lgkmcnt(0)
	v_pk_fma_f32 v[54:55], v[62:63], v[54:55], v[64:65] op_sel_hi:[0,1,1] neg_lo:[1,0,0] neg_hi:[1,0,0]
	v_cvt_pk_bf16_f32 v54, v54, v55
	v_cndmask_b32_e64 v65, 0, 1.0, vcc
	v_cmp_eq_u32_e32 vcc, v106, v112
	s_nop 1
	v_cndmask_b32_e64 v64, 0, 1.0, vcc
	v_pk_fma_f32 v[56:57], v[62:63], v[56:57], v[64:65] op_sel_hi:[0,1,1] neg_lo:[1,0,0] neg_hi:[1,0,0]
	v_cvt_pk_bf16_f32 v55, v56, v57
	ds_write_b64 v186, v[54:55] offset:3264
	ds_read_b32 v54, v187 offset:248
	v_cmp_eq_u32_e32 vcc, v102, v113
	s_nop 1
	v_cndmask_b32_e64 v56, 0, 1.0, vcc
	v_cmp_eq_u32_e32 vcc, v104, v113
	s_nop 1
	v_cndmask_b32_e64 v57, 0, 1.0, vcc
	v_cmp_eq_u32_e32 vcc, v105, v113
	s_waitcnt lgkmcnt(0)
	v_pk_fma_f32 v[46:47], v[54:55], v[46:47], v[56:57] op_sel_hi:[0,1,1] neg_lo:[1,0,0] neg_hi:[1,0,0]
	v_cvt_pk_bf16_f32 v46, v46, v47
	v_cndmask_b32_e64 v57, 0, 1.0, vcc
	v_cmp_eq_u32_e32 vcc, v106, v113
	s_nop 1
	v_cndmask_b32_e64 v56, 0, 1.0, vcc
	v_pk_fma_f32 v[48:49], v[54:55], v[48:49], v[56:57] op_sel_hi:[0,1,1] neg_lo:[1,0,0] neg_hi:[1,0,0]
	v_cvt_pk_bf16_f32 v47, v48, v49
	ds_write_b64 v186, v[46:47] offset:3808
	ds_read_b128 v[46:49], v1
	s_waitcnt lgkmcnt(0)
	ds_write_b128 v184, v[46:49]
	ds_read_b128 v[46:49], v1 offset:64
	s_waitcnt lgkmcnt(0)
	ds_write_b128 v184, v[46:49] offset:1024
	ds_read_b128 v[46:49], v1 offset:128
	s_waitcnt lgkmcnt(0)
	ds_write_b128 v184, v[46:49] offset:2048
	ds_read_b128 v[46:49], v1 offset:192
	s_waitcnt lgkmcnt(0)
	ds_write_b128 v184, v[46:49] offset:3072
	s_lshl_b32 s30, s25, 2
	s_mov_b32 s31, s21
	v_lshl_add_u64 v[46:47], v[126:127], 0, s[30:31]
	v_lshl_add_u64 v[48:49], v[128:129], 0, s[30:31]
	v_lshl_add_u64 v[54:55], v[134:135], 0, s[30:31]
	v_lshl_add_u64 v[56:57], v[136:137], 0, s[30:31]
	v_lshl_add_u64 v[62:63], v[138:139], 0, s[30:31]
	v_lshl_add_u64 v[64:65], v[140:141], 0, s[30:31]
	v_lshl_add_u64 v[98:99], v[142:143], 0, s[30:31]
	v_lshl_add_u64 v[100:101], v[144:145], 0, s[30:31]
	global_load_dwordx4 v[90:93], v[46:47], off nt
	global_load_dwordx4 v[82:85], v[48:49], off nt
	global_load_dwordx4 v[78:81], v[54:55], off nt
	global_load_dwordx4 v[70:73], v[56:57], off nt
	global_load_dwordx4 v[66:69], v[62:63], off nt
	s_nop 0
	global_load_dwordx4 v[62:65], v[64:65], off nt
	s_nop 0
	global_load_dwordx4 v[54:57], v[98:99], off nt
	global_load_dwordx4 v[46:49], v[100:101], off nt
	v_mov_b32_e32 v99, v189
	s_waitcnt vmcnt(23)
	s_waitcnt vmcnt(22)
	s_waitcnt vmcnt(21)
	s_waitcnt vmcnt(20)
	s_waitcnt vmcnt(19)
	s_waitcnt vmcnt(18)
	s_waitcnt vmcnt(17)
	s_waitcnt vmcnt(16)
	ds_read_b32 v98, v187 offset:192
	v_add_u32_e32 v102, 1, v99
	v_cmp_eq_u32_e32 vcc, v99, v103
	v_add_u32_e32 v104, 3, v99
	v_add_u32_e32 v105, 2, v99
	v_cndmask_b32_e64 v100, 0, 1.0, vcc
	v_cmp_eq_u32_e32 vcc, v102, v103
	s_nop 1
	v_cndmask_b32_e64 v101, 0, 1.0, vcc
	v_cmp_eq_u32_e32 vcc, v104, v103
	s_waitcnt lgkmcnt(0)
	v_pk_fma_f32 v[94:95], v[98:99], v[94:95], v[100:101] op_sel_hi:[0,1,1] neg_lo:[1,0,0] neg_hi:[1,0,0]
	v_cvt_pk_bf16_f32 v94, v94, v95
	v_cndmask_b32_e64 v101, 0, 1.0, vcc
	v_cmp_eq_u32_e32 vcc, v105, v103
	s_nop 1
	v_cndmask_b32_e64 v100, 0, 1.0, vcc
	v_pk_fma_f32 v[96:97], v[98:99], v[96:97], v[100:101] op_sel_hi:[0,1,1] neg_lo:[1,0,0] neg_hi:[1,0,0]
	v_cvt_pk_bf16_f32 v95, v96, v97
	ds_write_b64 v186, v[94:95]
	ds_read_b32 v94, v187 offset:200
	v_cmp_eq_u32_e32 vcc, v99, v107
	s_nop 1
	v_cndmask_b32_e64 v96, 0, 1.0, vcc
	v_cmp_eq_u32_e32 vcc, v102, v107
	s_nop 1
	v_cndmask_b32_e64 v97, 0, 1.0, vcc
	v_cmp_eq_u32_e32 vcc, v104, v107
	s_waitcnt lgkmcnt(0)
	v_pk_fma_f32 v[86:87], v[94:95], v[86:87], v[96:97] op_sel_hi:[0,1,1] neg_lo:[1,0,0] neg_hi:[1,0,0]
	v_cvt_pk_bf16_f32 v86, v86, v87
	v_cndmask_b32_e64 v97, 0, 1.0, vcc
	v_cmp_eq_u32_e32 vcc, v105, v107
	s_nop 1
	v_cndmask_b32_e64 v96, 0, 1.0, vcc
	v_pk_fma_f32 v[88:89], v[94:95], v[88:89], v[96:97] op_sel_hi:[0,1,1] neg_lo:[1,0,0] neg_hi:[1,0,0]
	v_cvt_pk_bf16_f32 v87, v88, v89
	ds_write_b64 v186, v[86:87] offset:544
	ds_read_b32 v86, v187 offset:208
	v_cmp_eq_u32_e32 vcc, v99, v108
	s_nop 1
	v_cndmask_b32_e64 v88, 0, 1.0, vcc
	v_cmp_eq_u32_e32 vcc, v102, v108
	s_nop 1
	v_cndmask_b32_e64 v89, 0, 1.0, vcc
	v_cmp_eq_u32_e32 vcc, v104, v108
	s_waitcnt lgkmcnt(0)
	v_pk_fma_f32 v[74:75], v[86:87], v[74:75], v[88:89] op_sel_hi:[0,1,1] neg_lo:[1,0,0] neg_hi:[1,0,0]
	v_cvt_pk_bf16_f32 v74, v74, v75
	v_cndmask_b32_e64 v89, 0, 1.0, vcc
	v_cmp_eq_u32_e32 vcc, v105, v108
	s_nop 1
	v_cndmask_b32_e64 v88, 0, 1.0, vcc
	v_pk_fma_f32 v[76:77], v[86:87], v[76:77], v[88:89] op_sel_hi:[0,1,1] neg_lo:[1,0,0] neg_hi:[1,0,0]
	v_cvt_pk_bf16_f32 v75, v76, v77
	ds_write_b64 v186, v[74:75] offset:1088
	ds_read_b32 v74, v187 offset:216
	v_cmp_eq_u32_e32 vcc, v99, v109
	s_nop 1
	v_cndmask_b32_e64 v76, 0, 1.0, vcc
	v_cmp_eq_u32_e32 vcc, v102, v109
	s_nop 1
	v_cndmask_b32_e64 v77, 0, 1.0, vcc
	v_cmp_eq_u32_e32 vcc, v104, v109
	s_waitcnt lgkmcnt(0)
	v_pk_fma_f32 v[58:59], v[74:75], v[58:59], v[76:77] op_sel_hi:[0,1,1] neg_lo:[1,0,0] neg_hi:[1,0,0]
	v_cvt_pk_bf16_f32 v58, v58, v59
	v_cndmask_b32_e64 v77, 0, 1.0, vcc
	v_cmp_eq_u32_e32 vcc, v105, v109
	s_nop 1
	v_cndmask_b32_e64 v76, 0, 1.0, vcc
	v_pk_fma_f32 v[60:61], v[74:75], v[60:61], v[76:77] op_sel_hi:[0,1,1] neg_lo:[1,0,0] neg_hi:[1,0,0]
	v_cvt_pk_bf16_f32 v59, v60, v61
	ds_write_b64 v186, v[58:59] offset:1632
	ds_read_b32 v58, v187 offset:224
	v_cmp_eq_u32_e32 vcc, v99, v110
	s_nop 1
	v_cndmask_b32_e64 v60, 0, 1.0, vcc
	v_cmp_eq_u32_e32 vcc, v102, v110
	s_nop 1
	v_cndmask_b32_e64 v61, 0, 1.0, vcc
	v_cmp_eq_u32_e32 vcc, v104, v110
	s_waitcnt lgkmcnt(0)
	v_pk_fma_f32 v[50:51], v[58:59], v[50:51], v[60:61] op_sel_hi:[0,1,1] neg_lo:[1,0,0] neg_hi:[1,0,0]
	v_cvt_pk_bf16_f32 v50, v50, v51
	v_cndmask_b32_e64 v61, 0, 1.0, vcc
	v_cmp_eq_u32_e32 vcc, v105, v110
	s_nop 1
	v_cndmask_b32_e64 v60, 0, 1.0, vcc
	v_pk_fma_f32 v[52:53], v[58:59], v[52:53], v[60:61] op_sel_hi:[0,1,1] neg_lo:[1,0,0] neg_hi:[1,0,0]
	v_cvt_pk_bf16_f32 v51, v52, v53
	ds_write_b64 v186, v[50:51] offset:2176
	ds_read_b32 v50, v187 offset:232
	v_cmp_eq_u32_e32 vcc, v99, v111
	s_nop 1
	v_cndmask_b32_e64 v52, 0, 1.0, vcc
	v_cmp_eq_u32_e32 vcc, v102, v111
	s_nop 1
	v_cndmask_b32_e64 v53, 0, 1.0, vcc
	v_cmp_eq_u32_e32 vcc, v104, v111
	s_waitcnt lgkmcnt(0)
	v_pk_fma_f32 v[42:43], v[50:51], v[42:43], v[52:53] op_sel_hi:[0,1,1] neg_lo:[1,0,0] neg_hi:[1,0,0]
	v_cvt_pk_bf16_f32 v42, v42, v43
	v_cndmask_b32_e64 v53, 0, 1.0, vcc
	v_cmp_eq_u32_e32 vcc, v105, v111
	s_nop 1
	v_cndmask_b32_e64 v52, 0, 1.0, vcc
	v_pk_fma_f32 v[44:45], v[50:51], v[44:45], v[52:53] op_sel_hi:[0,1,1] neg_lo:[1,0,0] neg_hi:[1,0,0]
	v_cvt_pk_bf16_f32 v43, v44, v45
	ds_write_b64 v186, v[42:43] offset:2720
	ds_read_b32 v42, v187 offset:240
	v_cmp_eq_u32_e32 vcc, v99, v112
	s_nop 1
	v_cndmask_b32_e64 v44, 0, 1.0, vcc
	v_cmp_eq_u32_e32 vcc, v102, v112
	s_nop 1
	v_cndmask_b32_e64 v45, 0, 1.0, vcc
	v_cmp_eq_u32_e32 vcc, v104, v112
	s_waitcnt lgkmcnt(0)
	v_pk_fma_f32 v[38:39], v[42:43], v[38:39], v[44:45] op_sel_hi:[0,1,1] neg_lo:[1,0,0] neg_hi:[1,0,0]
	v_cvt_pk_bf16_f32 v38, v38, v39
	v_cndmask_b32_e64 v45, 0, 1.0, vcc
	v_cmp_eq_u32_e32 vcc, v105, v112
	s_nop 1
	v_cndmask_b32_e64 v44, 0, 1.0, vcc
	v_pk_fma_f32 v[40:41], v[42:43], v[40:41], v[44:45] op_sel_hi:[0,1,1] neg_lo:[1,0,0] neg_hi:[1,0,0]
	v_cvt_pk_bf16_f32 v39, v40, v41
	ds_write_b64 v186, v[38:39] offset:3264
	ds_read_b32 v38, v187 offset:248
	v_cmp_eq_u32_e32 vcc, v99, v113
	s_nop 1
	v_cndmask_b32_e64 v40, 0, 1.0, vcc
	v_cmp_eq_u32_e32 vcc, v102, v113
	s_nop 1
	v_cndmask_b32_e64 v41, 0, 1.0, vcc
	v_cmp_eq_u32_e32 vcc, v104, v113
	s_waitcnt lgkmcnt(0)
	v_pk_fma_f32 v[34:35], v[38:39], v[34:35], v[40:41] op_sel_hi:[0,1,1] neg_lo:[1,0,0] neg_hi:[1,0,0]
	v_cvt_pk_bf16_f32 v34, v34, v35
	v_cndmask_b32_e64 v41, 0, 1.0, vcc
	v_cmp_eq_u32_e32 vcc, v105, v113
	s_nop 1
	v_cndmask_b32_e64 v40, 0, 1.0, vcc
	v_pk_fma_f32 v[36:37], v[38:39], v[36:37], v[40:41] op_sel_hi:[0,1,1] neg_lo:[1,0,0] neg_hi:[1,0,0]
	v_cvt_pk_bf16_f32 v35, v36, v37
	ds_write_b64 v186, v[34:35] offset:3808
	ds_read_b128 v[34:37], v1
	s_waitcnt lgkmcnt(0)
	ds_write_b128 v184, v[34:37] offset:4096
	ds_read_b128 v[34:37], v1 offset:64
	s_waitcnt lgkmcnt(0)
	ds_write_b128 v184, v[34:37] offset:5120
	ds_read_b128 v[34:37], v1 offset:128
	s_waitcnt lgkmcnt(0)
	ds_write_b128 v184, v[34:37] offset:6144
	ds_read_b128 v[34:37], v1 offset:192
	s_waitcnt lgkmcnt(0)
	ds_write_b128 v184, v[34:37] offset:7168
	s_lshl_b32 s28, s24, 2
	s_mov_b32 s29, s21
	v_lshl_add_u64 v[34:35], v[126:127], 0, s[28:29]
	v_lshl_add_u64 v[36:37], v[128:129], 0, s[28:29]
	v_lshl_add_u64 v[38:39], v[134:135], 0, s[28:29]
	v_lshl_add_u64 v[40:41], v[136:137], 0, s[28:29]
	v_lshl_add_u64 v[42:43], v[138:139], 0, s[28:29]
	v_lshl_add_u64 v[44:45], v[140:141], 0, s[28:29]
	v_lshl_add_u64 v[50:51], v[142:143], 0, s[28:29]
	v_lshl_add_u64 v[52:53], v[144:145], 0, s[28:29]
	global_load_dwordx4 v[122:125], v[34:35], off nt
	global_load_dwordx4 v[114:117], v[36:37], off nt
	global_load_dwordx4 v[106:109], v[38:39], off nt
	global_load_dwordx4 v[86:89], v[40:41], off nt
	global_load_dwordx4 v[74:77], v[42:43], off nt
	s_nop 0
	global_load_dwordx4 v[42:45], v[44:45], off nt
	s_nop 0
	global_load_dwordx4 v[38:41], v[50:51], off nt
	global_load_dwordx4 v[34:37], v[52:53], off nt
	v_mov_b32_e32 v50, v188
	s_waitcnt vmcnt(23)
	s_waitcnt vmcnt(22)
	s_waitcnt vmcnt(21)
	s_waitcnt vmcnt(20)
	s_waitcnt vmcnt(19)
	s_waitcnt vmcnt(18)
	s_waitcnt vmcnt(17)
	s_waitcnt vmcnt(16)
	ds_read_b32 v50, v187 offset:192
	s_waitcnt lgkmcnt(0)
	v_pk_fma_f32 v[30:31], v[50:51], v[30:31], 0 op_sel_hi:[0,1,0] neg_lo:[1,0,0] neg_hi:[1,0,0]
	v_pk_fma_f32 v[32:33], v[50:51], v[32:33], 0 op_sel_hi:[0,1,0] neg_lo:[1,0,0] neg_hi:[1,0,0]
	v_cvt_pk_bf16_f32 v30, v30, v31
	v_cvt_pk_bf16_f32 v31, v32, v33
	ds_write_b64 v186, v[30:31]
	ds_read_b32 v30, v187 offset:200
	s_waitcnt lgkmcnt(0)
	v_pk_fma_f32 v[26:27], v[30:31], v[26:27], 0 op_sel_hi:[0,1,0] neg_lo:[1,0,0] neg_hi:[1,0,0]
	v_pk_fma_f32 v[28:29], v[30:31], v[28:29], 0 op_sel_hi:[0,1,0] neg_lo:[1,0,0] neg_hi:[1,0,0]
	v_cvt_pk_bf16_f32 v26, v26, v27
	v_cvt_pk_bf16_f32 v27, v28, v29
	ds_write_b64 v186, v[26:27] offset:544
	ds_read_b32 v26, v187 offset:208
	s_waitcnt lgkmcnt(0)
	v_pk_fma_f32 v[22:23], v[26:27], v[22:23], 0 op_sel_hi:[0,1,0] neg_lo:[1,0,0] neg_hi:[1,0,0]
	v_pk_fma_f32 v[24:25], v[26:27], v[24:25], 0 op_sel_hi:[0,1,0] neg_lo:[1,0,0] neg_hi:[1,0,0]
	v_cvt_pk_bf16_f32 v22, v22, v23
	v_cvt_pk_bf16_f32 v23, v24, v25
	ds_write_b64 v186, v[22:23] offset:1088
	ds_read_b32 v22, v187 offset:216
	s_waitcnt lgkmcnt(0)
	v_pk_fma_f32 v[18:19], v[22:23], v[18:19], 0 op_sel_hi:[0,1,0] neg_lo:[1,0,0] neg_hi:[1,0,0]
	v_pk_fma_f32 v[20:21], v[22:23], v[20:21], 0 op_sel_hi:[0,1,0] neg_lo:[1,0,0] neg_hi:[1,0,0]
	v_cvt_pk_bf16_f32 v18, v18, v19
	v_cvt_pk_bf16_f32 v19, v20, v21
	ds_write_b64 v186, v[18:19] offset:1632
	ds_read_b32 v18, v187 offset:224
	s_waitcnt lgkmcnt(0)
	v_pk_fma_f32 v[14:15], v[18:19], v[14:15], 0 op_sel_hi:[0,1,0] neg_lo:[1,0,0] neg_hi:[1,0,0]
	v_pk_fma_f32 v[16:17], v[18:19], v[16:17], 0 op_sel_hi:[0,1,0] neg_lo:[1,0,0] neg_hi:[1,0,0]
	v_cvt_pk_bf16_f32 v14, v14, v15
	v_cvt_pk_bf16_f32 v15, v16, v17
	ds_write_b64 v186, v[14:15] offset:2176
	ds_read_b32 v14, v187 offset:232
	s_waitcnt lgkmcnt(0)
	v_pk_fma_f32 v[10:11], v[14:15], v[10:11], 0 op_sel_hi:[0,1,0] neg_lo:[1,0,0] neg_hi:[1,0,0]
	v_pk_fma_f32 v[12:13], v[14:15], v[12:13], 0 op_sel_hi:[0,1,0] neg_lo:[1,0,0] neg_hi:[1,0,0]
	v_cvt_pk_bf16_f32 v10, v10, v11
	v_cvt_pk_bf16_f32 v11, v12, v13
	ds_write_b64 v186, v[10:11] offset:2720
	ds_read_b32 v10, v187 offset:240
	s_waitcnt lgkmcnt(0)
	v_pk_fma_f32 v[6:7], v[10:11], v[6:7], 0 op_sel_hi:[0,1,0] neg_lo:[1,0,0] neg_hi:[1,0,0]
	v_pk_fma_f32 v[8:9], v[10:11], v[8:9], 0 op_sel_hi:[0,1,0] neg_lo:[1,0,0] neg_hi:[1,0,0]
	v_cvt_pk_bf16_f32 v6, v6, v7
	v_cvt_pk_bf16_f32 v7, v8, v9
	ds_write_b64 v186, v[6:7] offset:3264
	ds_read_b32 v6, v187 offset:248
	s_waitcnt lgkmcnt(0)
	v_pk_fma_f32 v[2:3], v[6:7], v[2:3], 0 op_sel_hi:[0,1,0] neg_lo:[1,0,0] neg_hi:[1,0,0]
	v_pk_fma_f32 v[4:5], v[6:7], v[4:5], 0 op_sel_hi:[0,1,0] neg_lo:[1,0,0] neg_hi:[1,0,0]
	v_cvt_pk_bf16_f32 v2, v2, v3
	v_cvt_pk_bf16_f32 v3, v4, v5
	ds_write_b64 v186, v[2:3] offset:3808
	ds_read_b128 v[2:5], v1
	s_waitcnt lgkmcnt(0)
	ds_write_b128 v184, v[2:5] offset:8192
	ds_read_b128 v[2:5], v1 offset:64
	s_waitcnt lgkmcnt(0)
	ds_write_b128 v184, v[2:5] offset:9216
	ds_read_b128 v[2:5], v1 offset:128
	s_waitcnt lgkmcnt(0)
	ds_write_b128 v184, v[2:5] offset:10240
	ds_read_b128 v[2:5], v1 offset:192
	s_waitcnt lgkmcnt(0)
	ds_write_b128 v184, v[2:5] offset:11264
	s_lshl_b32 s26, s23, 2
	s_mov_b32 s27, s21
	v_lshl_add_u64 v[2:3], v[126:127], 0, s[26:27]
	v_lshl_add_u64 v[4:5], v[128:129], 0, s[26:27]
	v_lshl_add_u64 v[6:7], v[134:135], 0, s[26:27]
	v_lshl_add_u64 v[8:9], v[136:137], 0, s[26:27]
	v_lshl_add_u64 v[10:11], v[138:139], 0, s[26:27]
	v_lshl_add_u64 v[12:13], v[140:141], 0, s[26:27]
	v_lshl_add_u64 v[14:15], v[142:143], 0, s[26:27]
	v_lshl_add_u64 v[16:17], v[144:145], 0, s[26:27]
	global_load_dwordx4 v[118:121], v[2:3], off nt
	global_load_dwordx4 v[110:113], v[4:5], off nt
	global_load_dwordx4 v[102:105], v[6:7], off nt
	global_load_dwordx4 v[98:101], v[8:9], off nt
	global_load_dwordx4 v[58:61], v[10:11], off nt
	global_load_dwordx4 v[50:53], v[12:13], off nt
	global_load_dwordx4 v[30:33], v[14:15], off nt
	global_load_dwordx4 v[22:25], v[16:17], off nt
	v_mov_b32_e32 v2, v198
	s_waitcnt vmcnt(23)
	s_waitcnt vmcnt(22)
	s_waitcnt vmcnt(21)
	s_waitcnt vmcnt(20)
	s_waitcnt vmcnt(19)
	s_waitcnt vmcnt(18)
	s_waitcnt vmcnt(17)
	s_waitcnt vmcnt(16)
	ds_read_b32 v2, v187 offset:192
	s_waitcnt lgkmcnt(0)
	v_pk_fma_f32 v[4:5], v[2:3], v[90:91], 0 op_sel_hi:[0,1,0] neg_lo:[1,0,0] neg_hi:[1,0,0]
	v_pk_fma_f32 v[2:3], v[2:3], v[92:93], 0 op_sel_hi:[0,1,0] neg_lo:[1,0,0] neg_hi:[1,0,0]
	v_cvt_pk_bf16_f32 v4, v4, v5
	v_cvt_pk_bf16_f32 v5, v2, v3
	ds_write_b64 v186, v[4:5]
	ds_read_b32 v2, v187 offset:200
	s_waitcnt lgkmcnt(0)
	v_pk_fma_f32 v[4:5], v[2:3], v[82:83], 0 op_sel_hi:[0,1,0] neg_lo:[1,0,0] neg_hi:[1,0,0]
	v_pk_fma_f32 v[2:3], v[2:3], v[84:85], 0 op_sel_hi:[0,1,0] neg_lo:[1,0,0] neg_hi:[1,0,0]
	v_cvt_pk_bf16_f32 v4, v4, v5
	v_cvt_pk_bf16_f32 v5, v2, v3
	ds_write_b64 v186, v[4:5] offset:544
	ds_read_b32 v2, v187 offset:208
	s_waitcnt lgkmcnt(0)
	v_pk_fma_f32 v[4:5], v[2:3], v[78:79], 0 op_sel_hi:[0,1,0] neg_lo:[1,0,0] neg_hi:[1,0,0]
	v_pk_fma_f32 v[2:3], v[2:3], v[80:81], 0 op_sel_hi:[0,1,0] neg_lo:[1,0,0] neg_hi:[1,0,0]
	v_cvt_pk_bf16_f32 v4, v4, v5
	v_cvt_pk_bf16_f32 v5, v2, v3
	ds_write_b64 v186, v[4:5] offset:1088
	ds_read_b32 v2, v187 offset:216
	s_waitcnt lgkmcnt(0)
	v_pk_fma_f32 v[4:5], v[2:3], v[70:71], 0 op_sel_hi:[0,1,0] neg_lo:[1,0,0] neg_hi:[1,0,0]
	v_pk_fma_f32 v[2:3], v[2:3], v[72:73], 0 op_sel_hi:[0,1,0] neg_lo:[1,0,0] neg_hi:[1,0,0]
	v_cvt_pk_bf16_f32 v4, v4, v5
	v_cvt_pk_bf16_f32 v5, v2, v3
	ds_write_b64 v186, v[4:5] offset:1632
	ds_read_b32 v2, v187 offset:224
	s_waitcnt lgkmcnt(0)
	v_pk_fma_f32 v[4:5], v[2:3], v[66:67], 0 op_sel_hi:[0,1,0] neg_lo:[1,0,0] neg_hi:[1,0,0]
	v_pk_fma_f32 v[2:3], v[2:3], v[68:69], 0 op_sel_hi:[0,1,0] neg_lo:[1,0,0] neg_hi:[1,0,0]
	v_cvt_pk_bf16_f32 v4, v4, v5
	v_cvt_pk_bf16_f32 v5, v2, v3
	ds_write_b64 v186, v[4:5] offset:2176
	ds_read_b32 v2, v187 offset:232
	s_waitcnt lgkmcnt(0)
	v_pk_fma_f32 v[4:5], v[2:3], v[62:63], 0 op_sel_hi:[0,1,0] neg_lo:[1,0,0] neg_hi:[1,0,0]
	v_pk_fma_f32 v[2:3], v[2:3], v[64:65], 0 op_sel_hi:[0,1,0] neg_lo:[1,0,0] neg_hi:[1,0,0]
	v_cvt_pk_bf16_f32 v4, v4, v5
	v_cvt_pk_bf16_f32 v5, v2, v3
	ds_write_b64 v186, v[4:5] offset:2720
	ds_read_b32 v2, v187 offset:240
	s_waitcnt lgkmcnt(0)
	v_pk_fma_f32 v[4:5], v[2:3], v[54:55], 0 op_sel_hi:[0,1,0] neg_lo:[1,0,0] neg_hi:[1,0,0]
	v_pk_fma_f32 v[2:3], v[2:3], v[56:57], 0 op_sel_hi:[0,1,0] neg_lo:[1,0,0] neg_hi:[1,0,0]
	v_cvt_pk_bf16_f32 v4, v4, v5
	v_cvt_pk_bf16_f32 v5, v2, v3
	ds_write_b64 v186, v[4:5] offset:3264
	ds_read_b32 v2, v187 offset:248
	s_waitcnt lgkmcnt(0)
	v_pk_fma_f32 v[4:5], v[2:3], v[46:47], 0 op_sel_hi:[0,1,0] neg_lo:[1,0,0] neg_hi:[1,0,0]
	v_pk_fma_f32 v[2:3], v[2:3], v[48:49], 0 op_sel_hi:[0,1,0] neg_lo:[1,0,0] neg_hi:[1,0,0]
	v_cvt_pk_bf16_f32 v4, v4, v5
	v_cvt_pk_bf16_f32 v5, v2, v3
	ds_write_b64 v186, v[4:5] offset:3808
	ds_read_b128 v[2:5], v1
	s_waitcnt lgkmcnt(0)
	ds_write_b128 v184, v[2:5] offset:12288
	ds_read_b128 v[2:5], v1 offset:64
	s_waitcnt lgkmcnt(0)
	ds_write_b128 v184, v[2:5] offset:13312
	ds_read_b128 v[2:5], v1 offset:128
	s_waitcnt lgkmcnt(0)
	ds_write_b128 v184, v[2:5] offset:14336
	ds_read_b128 v[2:5], v1 offset:192
	s_waitcnt lgkmcnt(0)
	ds_write_b128 v184, v[2:5] offset:15360
	s_lshl_b32 s24, s22, 2
	s_mov_b32 s25, s21
	v_lshl_add_u64 v[2:3], v[126:127], 0, s[24:25]
	v_lshl_add_u64 v[6:7], v[134:135], 0, s[24:25]
	v_lshl_add_u64 v[8:9], v[136:137], 0, s[24:25]
	v_lshl_add_u64 v[14:15], v[142:143], 0, s[24:25]
	v_lshl_add_u64 v[4:5], v[128:129], 0, s[24:25]
	v_lshl_add_u64 v[10:11], v[138:139], 0, s[24:25]
	v_lshl_add_u64 v[12:13], v[140:141], 0, s[24:25]
	v_lshl_add_u64 v[18:19], v[144:145], 0, s[24:25]
	global_load_dwordx4 v[94:97], v[2:3], off nt
	global_load_dwordx4 v[90:93], v[4:5], off nt
	global_load_dwordx4 v[82:85], v[6:7], off nt
	global_load_dwordx4 v[70:73], v[8:9], off nt
	global_load_dwordx4 v[54:57], v[10:11], off nt
	global_load_dwordx4 v[26:29], v[12:13], off nt
	s_nop 0
	global_load_dwordx4 v[14:17], v[14:15], off nt
	s_nop 0
	global_load_dwordx4 v[6:9], v[18:19], off nt
	v_mov_b32_e32 v2, v197
	s_waitcnt vmcnt(23)
	s_waitcnt vmcnt(22)
	s_waitcnt vmcnt(21)
	s_waitcnt vmcnt(20)
	s_waitcnt vmcnt(19)
	s_waitcnt vmcnt(18)
	s_waitcnt vmcnt(17)
	s_waitcnt vmcnt(16)
	ds_read_b32 v2, v187 offset:192
	s_waitcnt lgkmcnt(0)
	v_pk_fma_f32 v[4:5], v[2:3], v[122:123], 0 op_sel_hi:[0,1,0] neg_lo:[1,0,0] neg_hi:[1,0,0]
	v_pk_fma_f32 v[2:3], v[2:3], v[124:125], 0 op_sel_hi:[0,1,0] neg_lo:[1,0,0] neg_hi:[1,0,0]
	v_cvt_pk_bf16_f32 v4, v4, v5
	v_cvt_pk_bf16_f32 v5, v2, v3
	ds_write_b64 v186, v[4:5]
	ds_read_b32 v2, v187 offset:200
	s_waitcnt lgkmcnt(0)
	v_pk_fma_f32 v[4:5], v[2:3], v[114:115], 0 op_sel_hi:[0,1,0] neg_lo:[1,0,0] neg_hi:[1,0,0]
	v_pk_fma_f32 v[2:3], v[2:3], v[116:117], 0 op_sel_hi:[0,1,0] neg_lo:[1,0,0] neg_hi:[1,0,0]
	v_cvt_pk_bf16_f32 v4, v4, v5
	v_cvt_pk_bf16_f32 v5, v2, v3
	ds_write_b64 v186, v[4:5] offset:544
	ds_read_b32 v2, v187 offset:208
	s_waitcnt lgkmcnt(0)
	v_pk_fma_f32 v[4:5], v[2:3], v[106:107], 0 op_sel_hi:[0,1,0] neg_lo:[1,0,0] neg_hi:[1,0,0]
	v_pk_fma_f32 v[2:3], v[2:3], v[108:109], 0 op_sel_hi:[0,1,0] neg_lo:[1,0,0] neg_hi:[1,0,0]
	v_cvt_pk_bf16_f32 v4, v4, v5
	v_cvt_pk_bf16_f32 v5, v2, v3
	ds_write_b64 v186, v[4:5] offset:1088
	ds_read_b32 v2, v187 offset:216
	s_waitcnt lgkmcnt(0)
	v_pk_fma_f32 v[4:5], v[2:3], v[86:87], 0 op_sel_hi:[0,1,0] neg_lo:[1,0,0] neg_hi:[1,0,0]
	v_pk_fma_f32 v[2:3], v[2:3], v[88:89], 0 op_sel_hi:[0,1,0] neg_lo:[1,0,0] neg_hi:[1,0,0]
	v_cvt_pk_bf16_f32 v4, v4, v5
	v_cvt_pk_bf16_f32 v5, v2, v3
	ds_write_b64 v186, v[4:5] offset:1632
	ds_read_b32 v2, v187 offset:224
	s_waitcnt lgkmcnt(0)
	v_pk_fma_f32 v[4:5], v[2:3], v[74:75], 0 op_sel_hi:[0,1,0] neg_lo:[1,0,0] neg_hi:[1,0,0]
	v_pk_fma_f32 v[2:3], v[2:3], v[76:77], 0 op_sel_hi:[0,1,0] neg_lo:[1,0,0] neg_hi:[1,0,0]
	v_cvt_pk_bf16_f32 v4, v4, v5
	v_cvt_pk_bf16_f32 v5, v2, v3
	ds_write_b64 v186, v[4:5] offset:2176
	ds_read_b32 v2, v187 offset:232
	s_waitcnt lgkmcnt(0)
	v_pk_fma_f32 v[4:5], v[2:3], v[42:43], 0 op_sel_hi:[0,1,0] neg_lo:[1,0,0] neg_hi:[1,0,0]
	v_pk_fma_f32 v[2:3], v[2:3], v[44:45], 0 op_sel_hi:[0,1,0] neg_lo:[1,0,0] neg_hi:[1,0,0]
	v_cvt_pk_bf16_f32 v4, v4, v5
	v_cvt_pk_bf16_f32 v5, v2, v3
	ds_write_b64 v186, v[4:5] offset:2720
	ds_read_b32 v2, v187 offset:240
	s_waitcnt lgkmcnt(0)
	v_pk_fma_f32 v[4:5], v[2:3], v[38:39], 0 op_sel_hi:[0,1,0] neg_lo:[1,0,0] neg_hi:[1,0,0]
	v_pk_fma_f32 v[2:3], v[2:3], v[40:41], 0 op_sel_hi:[0,1,0] neg_lo:[1,0,0] neg_hi:[1,0,0]
	v_cvt_pk_bf16_f32 v4, v4, v5
	v_cvt_pk_bf16_f32 v5, v2, v3
	ds_write_b64 v186, v[4:5] offset:3264
	ds_read_b32 v2, v187 offset:248
	s_waitcnt lgkmcnt(0)
	v_pk_fma_f32 v[4:5], v[2:3], v[34:35], 0 op_sel_hi:[0,1,0] neg_lo:[1,0,0] neg_hi:[1,0,0]
	v_pk_fma_f32 v[2:3], v[2:3], v[36:37], 0 op_sel_hi:[0,1,0] neg_lo:[1,0,0] neg_hi:[1,0,0]
	v_cvt_pk_bf16_f32 v4, v4, v5
	v_cvt_pk_bf16_f32 v5, v2, v3
	ds_write_b64 v186, v[4:5] offset:3808
	ds_read_b128 v[2:5], v1
	s_waitcnt lgkmcnt(0)
	ds_write_b128 v184, v[2:5] offset:16384
	ds_read_b128 v[2:5], v1 offset:64
	s_waitcnt lgkmcnt(0)
	ds_write_b128 v184, v[2:5] offset:17408
	ds_read_b128 v[2:5], v1 offset:128
	s_waitcnt lgkmcnt(0)
	ds_write_b128 v184, v[2:5] offset:18432
	ds_read_b128 v[2:5], v1 offset:192
	s_waitcnt lgkmcnt(0)
	ds_write_b128 v184, v[2:5] offset:19456
	s_lshl_b32 s22, s7, 2
	s_mov_b32 s23, s21
	v_lshl_add_u64 v[2:3], v[126:127], 0, s[22:23]
	v_lshl_add_u64 v[4:5], v[128:129], 0, s[22:23]
	v_lshl_add_u64 v[10:11], v[134:135], 0, s[22:23]
	v_lshl_add_u64 v[12:13], v[136:137], 0, s[22:23]
	v_lshl_add_u64 v[34:35], v[138:139], 0, s[22:23]
	v_lshl_add_u64 v[36:37], v[140:141], 0, s[22:23]
	v_lshl_add_u64 v[46:47], v[142:143], 0, s[22:23]
	v_lshl_add_u64 v[48:49], v[144:145], 0, s[22:23]
	global_load_dwordx4 v[86:89], v[2:3], off nt
	global_load_dwordx4 v[78:81], v[4:5], off nt
	global_load_dwordx4 v[66:69], v[10:11], off nt
	global_load_dwordx4 v[42:45], v[12:13], off nt
	global_load_dwordx4 v[38:41], v[34:35], off nt
	global_load_dwordx4 v[18:21], v[36:37], off nt
	s_nop 0
	global_load_dwordx4 v[10:13], v[46:47], off nt
	global_load_dwordx4 v[2:5], v[48:49], off nt
	v_mov_b32_e32 v34, v196
	s_waitcnt vmcnt(23)
	s_waitcnt vmcnt(22)
	s_waitcnt vmcnt(21)
	s_waitcnt vmcnt(20)
	s_waitcnt vmcnt(19)
	s_waitcnt vmcnt(18)
	s_waitcnt vmcnt(17)
	s_waitcnt vmcnt(16)
	ds_read_b32 v34, v187 offset:192
	s_waitcnt lgkmcnt(0)
	v_pk_fma_f32 v[36:37], v[34:35], v[118:119], 0 op_sel_hi:[0,1,0] neg_lo:[1,0,0] neg_hi:[1,0,0]
	v_pk_fma_f32 v[34:35], v[34:35], v[120:121], 0 op_sel_hi:[0,1,0] neg_lo:[1,0,0] neg_hi:[1,0,0]
	v_cvt_pk_bf16_f32 v36, v36, v37
	v_cvt_pk_bf16_f32 v37, v34, v35
	ds_write_b64 v186, v[36:37]
	ds_read_b32 v34, v187 offset:200
	s_waitcnt lgkmcnt(0)
	v_pk_fma_f32 v[36:37], v[34:35], v[110:111], 0 op_sel_hi:[0,1,0] neg_lo:[1,0,0] neg_hi:[1,0,0]
	v_pk_fma_f32 v[34:35], v[34:35], v[112:113], 0 op_sel_hi:[0,1,0] neg_lo:[1,0,0] neg_hi:[1,0,0]
	v_cvt_pk_bf16_f32 v36, v36, v37
	v_cvt_pk_bf16_f32 v37, v34, v35
	ds_write_b64 v186, v[36:37] offset:544
	ds_read_b32 v34, v187 offset:208
	s_waitcnt lgkmcnt(0)
	v_pk_fma_f32 v[36:37], v[34:35], v[102:103], 0 op_sel_hi:[0,1,0] neg_lo:[1,0,0] neg_hi:[1,0,0]
	v_pk_fma_f32 v[34:35], v[34:35], v[104:105], 0 op_sel_hi:[0,1,0] neg_lo:[1,0,0] neg_hi:[1,0,0]
	v_cvt_pk_bf16_f32 v36, v36, v37
	v_cvt_pk_bf16_f32 v37, v34, v35
	ds_write_b64 v186, v[36:37] offset:1088
	ds_read_b32 v34, v187 offset:216
	s_waitcnt lgkmcnt(0)
	v_pk_fma_f32 v[36:37], v[34:35], v[98:99], 0 op_sel_hi:[0,1,0] neg_lo:[1,0,0] neg_hi:[1,0,0]
	v_pk_fma_f32 v[34:35], v[34:35], v[100:101], 0 op_sel_hi:[0,1,0] neg_lo:[1,0,0] neg_hi:[1,0,0]
	v_cvt_pk_bf16_f32 v36, v36, v37
	v_cvt_pk_bf16_f32 v37, v34, v35
	ds_write_b64 v186, v[36:37] offset:1632
	ds_read_b32 v34, v187 offset:224
	s_waitcnt lgkmcnt(0)
	v_pk_fma_f32 v[36:37], v[34:35], v[58:59], 0 op_sel_hi:[0,1,0] neg_lo:[1,0,0] neg_hi:[1,0,0]
	v_pk_fma_f32 v[34:35], v[34:35], v[60:61], 0 op_sel_hi:[0,1,0] neg_lo:[1,0,0] neg_hi:[1,0,0]
	v_cvt_pk_bf16_f32 v36, v36, v37
	v_cvt_pk_bf16_f32 v37, v34, v35
	ds_write_b64 v186, v[36:37] offset:2176
	ds_read_b32 v34, v187 offset:232
	s_waitcnt lgkmcnt(0)
	v_pk_fma_f32 v[36:37], v[34:35], v[50:51], 0 op_sel_hi:[0,1,0] neg_lo:[1,0,0] neg_hi:[1,0,0]
	v_pk_fma_f32 v[34:35], v[34:35], v[52:53], 0 op_sel_hi:[0,1,0] neg_lo:[1,0,0] neg_hi:[1,0,0]
	v_cvt_pk_bf16_f32 v36, v36, v37
	v_cvt_pk_bf16_f32 v37, v34, v35
	ds_write_b64 v186, v[36:37] offset:2720
	ds_read_b32 v34, v187 offset:240
	s_waitcnt lgkmcnt(0)
	v_pk_fma_f32 v[30:31], v[34:35], v[30:31], 0 op_sel_hi:[0,1,0] neg_lo:[1,0,0] neg_hi:[1,0,0]
	v_pk_fma_f32 v[32:33], v[34:35], v[32:33], 0 op_sel_hi:[0,1,0] neg_lo:[1,0,0] neg_hi:[1,0,0]
	v_cvt_pk_bf16_f32 v30, v30, v31
	v_cvt_pk_bf16_f32 v31, v32, v33
	ds_write_b64 v186, v[30:31] offset:3264
	ds_read_b32 v30, v187 offset:248
	s_waitcnt lgkmcnt(0)
	v_pk_fma_f32 v[22:23], v[30:31], v[22:23], 0 op_sel_hi:[0,1,0] neg_lo:[1,0,0] neg_hi:[1,0,0]
	v_pk_fma_f32 v[24:25], v[30:31], v[24:25], 0 op_sel_hi:[0,1,0] neg_lo:[1,0,0] neg_hi:[1,0,0]
	v_cvt_pk_bf16_f32 v22, v22, v23
	v_cvt_pk_bf16_f32 v23, v24, v25
	ds_write_b64 v186, v[22:23] offset:3808
	ds_read_b128 v[22:25], v1
	s_waitcnt lgkmcnt(0)
	ds_write_b128 v184, v[22:25] offset:20480
	ds_read_b128 v[22:25], v1 offset:64
	s_waitcnt lgkmcnt(0)
	ds_write_b128 v184, v[22:25] offset:21504
	ds_read_b128 v[22:25], v1 offset:128
	s_waitcnt lgkmcnt(0)
	ds_write_b128 v184, v[22:25] offset:22528
	ds_read_b128 v[22:25], v1 offset:192
	s_waitcnt lgkmcnt(0)
	ds_write_b128 v184, v[22:25] offset:23552
	v_lshl_add_u64 v[22:23], v[130:131], 0, s[30:31]
	s_movk_i32 s7, 0x2000
	v_add_co_u32_e32 v24, vcc, s7, v22
	s_movk_i32 s36, 0x4000
	s_nop 0
	v_addc_co_u32_e32 v25, vcc, 0, v23, vcc
	global_load_dwordx4 v[74:77], v[22:23], off nt
	global_load_dwordx4 v[62:65], v[24:25], off nt
	v_add_co_u32_e32 v24, vcc, s36, v22
	s_movk_i32 s37, 0x6000
	s_nop 0
	v_addc_co_u32_e32 v25, vcc, 0, v23, vcc
	v_add_co_u32_e32 v30, vcc, s37, v22
	s_mov_b32 s38, 0x8000
	s_nop 0
	v_addc_co_u32_e32 v31, vcc, 0, v23, vcc
	global_load_dwordx4 v[58:61], v[24:25], off nt
	global_load_dwordx4 v[46:49], v[30:31], off nt
	v_add_co_u32_e32 v24, vcc, s38, v22
	s_mov_b32 s39, 0xa000
	s_nop 0
	v_addc_co_u32_e32 v25, vcc, 0, v23, vcc
	v_add_co_u32_e32 v34, vcc, s39, v22
	s_mov_b32 s41, 0xc000
	s_nop 0
	v_addc_co_u32_e32 v35, vcc, 0, v23, vcc
	global_load_dwordx4 v[50:53], v[24:25], off nt
	global_load_dwordx4 v[30:33], v[34:35], off nt
	v_add_co_u32_e32 v24, vcc, s41, v22
	s_mov_b32 s42, 0xe000
	s_nop 0
	v_addc_co_u32_e32 v25, vcc, 0, v23, vcc
	v_add_co_u32_e32 v22, vcc, s42, v22
	s_nop 1
	v_addc_co_u32_e32 v23, vcc, 0, v23, vcc
	global_load_dwordx4 v[34:37], v[24:25], off nt
	s_nop 0
	global_load_dwordx4 v[22:25], v[22:23], off nt
	v_mov_b32_e32 v98, v195
	s_waitcnt vmcnt(23)
	s_waitcnt vmcnt(22)
	s_waitcnt vmcnt(21)
	s_waitcnt vmcnt(20)
	s_waitcnt vmcnt(19)
	s_waitcnt vmcnt(18)
	s_waitcnt vmcnt(17)
	s_waitcnt vmcnt(16)
	ds_read_b32 v98, v187 offset:192
	s_waitcnt lgkmcnt(0)
	v_pk_fma_f32 v[94:95], v[98:99], v[94:95], 0 op_sel_hi:[0,1,0] neg_lo:[1,0,0] neg_hi:[1,0,0]
	v_pk_fma_f32 v[96:97], v[98:99], v[96:97], 0 op_sel_hi:[0,1,0] neg_lo:[1,0,0] neg_hi:[1,0,0]
	v_cvt_pk_bf16_f32 v94, v94, v95
	v_cvt_pk_bf16_f32 v95, v96, v97
	ds_write_b64 v186, v[94:95]
	ds_read_b32 v94, v187 offset:200
	s_waitcnt lgkmcnt(0)
	v_pk_fma_f32 v[90:91], v[94:95], v[90:91], 0 op_sel_hi:[0,1,0] neg_lo:[1,0,0] neg_hi:[1,0,0]
	v_pk_fma_f32 v[92:93], v[94:95], v[92:93], 0 op_sel_hi:[0,1,0] neg_lo:[1,0,0] neg_hi:[1,0,0]
	v_cvt_pk_bf16_f32 v90, v90, v91
	v_cvt_pk_bf16_f32 v91, v92, v93
	ds_write_b64 v186, v[90:91] offset:544
	ds_read_b32 v90, v187 offset:208
	s_waitcnt lgkmcnt(0)
	v_pk_fma_f32 v[82:83], v[90:91], v[82:83], 0 op_sel_hi:[0,1,0] neg_lo:[1,0,0] neg_hi:[1,0,0]
	v_pk_fma_f32 v[84:85], v[90:91], v[84:85], 0 op_sel_hi:[0,1,0] neg_lo:[1,0,0] neg_hi:[1,0,0]
	v_cvt_pk_bf16_f32 v82, v82, v83
	v_cvt_pk_bf16_f32 v83, v84, v85
	ds_write_b64 v186, v[82:83] offset:1088
	ds_read_b32 v82, v187 offset:216
	s_waitcnt lgkmcnt(0)
	v_pk_fma_f32 v[70:71], v[82:83], v[70:71], 0 op_sel_hi:[0,1,0] neg_lo:[1,0,0] neg_hi:[1,0,0]
	v_pk_fma_f32 v[72:73], v[82:83], v[72:73], 0 op_sel_hi:[0,1,0] neg_lo:[1,0,0] neg_hi:[1,0,0]
	v_cvt_pk_bf16_f32 v70, v70, v71
	v_cvt_pk_bf16_f32 v71, v72, v73
	ds_write_b64 v186, v[70:71] offset:1632
	ds_read_b32 v70, v187 offset:224
	s_waitcnt lgkmcnt(0)
	v_pk_fma_f32 v[54:55], v[70:71], v[54:55], 0 op_sel_hi:[0,1,0] neg_lo:[1,0,0] neg_hi:[1,0,0]
	v_pk_fma_f32 v[56:57], v[70:71], v[56:57], 0 op_sel_hi:[0,1,0] neg_lo:[1,0,0] neg_hi:[1,0,0]
	v_cvt_pk_bf16_f32 v54, v54, v55
	v_cvt_pk_bf16_f32 v55, v56, v57
	ds_write_b64 v186, v[54:55] offset:2176
	ds_read_b32 v54, v187 offset:232
	s_waitcnt lgkmcnt(0)
	v_pk_fma_f32 v[26:27], v[54:55], v[26:27], 0 op_sel_hi:[0,1,0] neg_lo:[1,0,0] neg_hi:[1,0,0]
	v_pk_fma_f32 v[28:29], v[54:55], v[28:29], 0 op_sel_hi:[0,1,0] neg_lo:[1,0,0] neg_hi:[1,0,0]
	v_cvt_pk_bf16_f32 v26, v26, v27
	v_cvt_pk_bf16_f32 v27, v28, v29
	ds_write_b64 v186, v[26:27] offset:2720
	ds_read_b32 v26, v187 offset:240
	s_waitcnt lgkmcnt(0)
	v_pk_fma_f32 v[14:15], v[26:27], v[14:15], 0 op_sel_hi:[0,1,0] neg_lo:[1,0,0] neg_hi:[1,0,0]
	v_pk_fma_f32 v[16:17], v[26:27], v[16:17], 0 op_sel_hi:[0,1,0] neg_lo:[1,0,0] neg_hi:[1,0,0]
	v_cvt_pk_bf16_f32 v14, v14, v15
	v_cvt_pk_bf16_f32 v15, v16, v17
	ds_write_b64 v186, v[14:15] offset:3264
	ds_read_b32 v14, v187 offset:248
	s_waitcnt lgkmcnt(0)
	v_pk_fma_f32 v[6:7], v[14:15], v[6:7], 0 op_sel_hi:[0,1,0] neg_lo:[1,0,0] neg_hi:[1,0,0]
	v_pk_fma_f32 v[8:9], v[14:15], v[8:9], 0 op_sel_hi:[0,1,0] neg_lo:[1,0,0] neg_hi:[1,0,0]
	v_cvt_pk_bf16_f32 v6, v6, v7
	v_cvt_pk_bf16_f32 v7, v8, v9
	ds_write_b64 v186, v[6:7] offset:3808
	ds_read_b128 v[6:9], v1
	s_waitcnt lgkmcnt(0)
	ds_write_b128 v184, v[6:9] offset:24576
	ds_read_b128 v[6:9], v1 offset:64
	s_waitcnt lgkmcnt(0)
	ds_write_b128 v184, v[6:9] offset:25600
	ds_read_b128 v[6:9], v1 offset:128
	s_waitcnt lgkmcnt(0)
	ds_write_b128 v184, v[6:9] offset:26624
	ds_read_b128 v[6:9], v1 offset:192
	s_waitcnt lgkmcnt(0)
	ds_write_b128 v184, v[6:9] offset:27648
	s_mov_b64 s[44:45], 0x10000
	v_lshl_add_u64 v[150:151], v[130:131], 0, s[44:45]
	s_mov_b64 s[44:45], 0x12000
	v_lshl_add_u64 v[152:153], v[130:131], 0, s[44:45]
	s_mov_b64 s[44:45], 0x14000
	v_lshl_add_u64 v[156:157], v[130:131], 0, s[44:45]
	s_mov_b64 s[44:45], 0x16000
	v_lshl_add_u64 v[158:159], v[130:131], 0, s[44:45]
	s_mov_b64 s[44:45], 0x18000
	v_lshl_add_u64 v[160:161], v[130:131], 0, s[44:45]
	s_mov_b64 s[44:45], 0x1a000
	v_lshl_add_u64 v[162:163], v[130:131], 0, s[44:45]
	s_mov_b64 s[44:45], 0x1c000
	v_lshl_add_u64 v[164:165], v[130:131], 0, s[44:45]
	s_mov_b64 s[44:45], 0x1e000
	v_lshl_add_u64 v[6:7], v[150:151], 0, s[30:31]
	v_lshl_add_u64 v[8:9], v[152:153], 0, s[30:31]
	v_lshl_add_u64 v[14:15], v[156:157], 0, s[30:31]
	v_lshl_add_u64 v[16:17], v[158:159], 0, s[30:31]
	v_lshl_add_u64 v[26:27], v[160:161], 0, s[30:31]
	v_lshl_add_u64 v[28:29], v[162:163], 0, s[30:31]
	v_lshl_add_u64 v[166:167], v[130:131], 0, s[44:45]
	v_lshl_add_u64 v[98:99], v[164:165], 0, s[30:31]
	v_lshl_add_u64 v[100:101], v[166:167], 0, s[30:31]
	global_load_dwordx4 v[94:97], v[6:7], off nt
	global_load_dwordx4 v[90:93], v[8:9], off nt
	global_load_dwordx4 v[82:85], v[14:15], off nt
	global_load_dwordx4 v[70:73], v[16:17], off nt
	global_load_dwordx4 v[54:57], v[26:27], off nt
	s_nop 0
	global_load_dwordx4 v[26:29], v[28:29], off nt
	s_nop 0
	global_load_dwordx4 v[14:17], v[98:99], off nt
	global_load_dwordx4 v[6:9], v[100:101], off nt
	v_mov_b32_e32 v98, v194
	s_waitcnt vmcnt(23)
	s_waitcnt vmcnt(22)
	s_waitcnt vmcnt(21)
	s_waitcnt vmcnt(20)
	s_waitcnt vmcnt(19)
	s_waitcnt vmcnt(18)
	s_waitcnt vmcnt(17)
	s_waitcnt vmcnt(16)
	ds_read_b32 v98, v187 offset:192
	s_waitcnt lgkmcnt(0)
	v_pk_fma_f32 v[86:87], v[98:99], v[86:87], 0 op_sel_hi:[0,1,0] neg_lo:[1,0,0] neg_hi:[1,0,0]
	v_pk_fma_f32 v[88:89], v[98:99], v[88:89], 0 op_sel_hi:[0,1,0] neg_lo:[1,0,0] neg_hi:[1,0,0]
	v_cvt_pk_bf16_f32 v86, v86, v87
	v_cvt_pk_bf16_f32 v87, v88, v89
	ds_write_b64 v186, v[86:87]
	ds_read_b32 v86, v187 offset:200
	s_waitcnt lgkmcnt(0)
	v_pk_fma_f32 v[78:79], v[86:87], v[78:79], 0 op_sel_hi:[0,1,0] neg_lo:[1,0,0] neg_hi:[1,0,0]
	v_pk_fma_f32 v[80:81], v[86:87], v[80:81], 0 op_sel_hi:[0,1,0] neg_lo:[1,0,0] neg_hi:[1,0,0]
	v_cvt_pk_bf16_f32 v78, v78, v79
	v_cvt_pk_bf16_f32 v79, v80, v81
	ds_write_b64 v186, v[78:79] offset:544
	ds_read_b32 v78, v187 offset:208
	s_waitcnt lgkmcnt(0)
	v_pk_fma_f32 v[66:67], v[78:79], v[66:67], 0 op_sel_hi:[0,1,0] neg_lo:[1,0,0] neg_hi:[1,0,0]
	v_pk_fma_f32 v[68:69], v[78:79], v[68:69], 0 op_sel_hi:[0,1,0] neg_lo:[1,0,0] neg_hi:[1,0,0]
	v_cvt_pk_bf16_f32 v66, v66, v67
	v_cvt_pk_bf16_f32 v67, v68, v69
	ds_write_b64 v186, v[66:67] offset:1088
	ds_read_b32 v66, v187 offset:216
	s_waitcnt lgkmcnt(0)
	v_pk_fma_f32 v[42:43], v[66:67], v[42:43], 0 op_sel_hi:[0,1,0] neg_lo:[1,0,0] neg_hi:[1,0,0]
	v_pk_fma_f32 v[44:45], v[66:67], v[44:45], 0 op_sel_hi:[0,1,0] neg_lo:[1,0,0] neg_hi:[1,0,0]
	v_cvt_pk_bf16_f32 v42, v42, v43
	v_cvt_pk_bf16_f32 v43, v44, v45
	ds_write_b64 v186, v[42:43] offset:1632
	ds_read_b32 v42, v187 offset:224
	s_waitcnt lgkmcnt(0)
	v_pk_fma_f32 v[38:39], v[42:43], v[38:39], 0 op_sel_hi:[0,1,0] neg_lo:[1,0,0] neg_hi:[1,0,0]
	v_pk_fma_f32 v[40:41], v[42:43], v[40:41], 0 op_sel_hi:[0,1,0] neg_lo:[1,0,0] neg_hi:[1,0,0]
	v_cvt_pk_bf16_f32 v38, v38, v39
	v_cvt_pk_bf16_f32 v39, v40, v41
	ds_write_b64 v186, v[38:39] offset:2176
	ds_read_b32 v38, v187 offset:232
	s_waitcnt lgkmcnt(0)
	v_pk_fma_f32 v[18:19], v[38:39], v[18:19], 0 op_sel_hi:[0,1,0] neg_lo:[1,0,0] neg_hi:[1,0,0]
	v_pk_fma_f32 v[20:21], v[38:39], v[20:21], 0 op_sel_hi:[0,1,0] neg_lo:[1,0,0] neg_hi:[1,0,0]
	v_cvt_pk_bf16_f32 v18, v18, v19
	v_cvt_pk_bf16_f32 v19, v20, v21
	ds_write_b64 v186, v[18:19] offset:2720
	ds_read_b32 v18, v187 offset:240
	s_waitcnt lgkmcnt(0)
	v_pk_fma_f32 v[10:11], v[18:19], v[10:11], 0 op_sel_hi:[0,1,0] neg_lo:[1,0,0] neg_hi:[1,0,0]
	v_pk_fma_f32 v[12:13], v[18:19], v[12:13], 0 op_sel_hi:[0,1,0] neg_lo:[1,0,0] neg_hi:[1,0,0]
	v_cvt_pk_bf16_f32 v10, v10, v11
	v_cvt_pk_bf16_f32 v11, v12, v13
	ds_write_b64 v186, v[10:11] offset:3264
	ds_read_b32 v10, v187 offset:248
	s_waitcnt lgkmcnt(0)
	v_pk_fma_f32 v[2:3], v[10:11], v[2:3], 0 op_sel_hi:[0,1,0] neg_lo:[1,0,0] neg_hi:[1,0,0]
	v_pk_fma_f32 v[4:5], v[10:11], v[4:5], 0 op_sel_hi:[0,1,0] neg_lo:[1,0,0] neg_hi:[1,0,0]
	v_cvt_pk_bf16_f32 v2, v2, v3
	v_cvt_pk_bf16_f32 v3, v4, v5
	ds_write_b64 v186, v[2:3] offset:3808
	ds_read_b128 v[2:5], v1
	s_waitcnt lgkmcnt(0)
	ds_write_b128 v184, v[2:5] offset:28672
	ds_read_b128 v[2:5], v1 offset:64
	s_waitcnt lgkmcnt(0)
	ds_write_b128 v184, v[2:5] offset:29696
	ds_read_b128 v[2:5], v1 offset:128
	s_waitcnt lgkmcnt(0)
	ds_write_b128 v184, v[2:5] offset:30720
	ds_read_b128 v[2:5], v1 offset:192
	s_waitcnt lgkmcnt(0)
	ds_write_b128 v184, v[2:5] offset:31744
	s_mov_b64 s[44:45], 0x20000
	v_lshl_add_u64 v[168:169], v[130:131], 0, s[44:45]
	s_mov_b64 s[44:45], 0x22000
	v_lshl_add_u64 v[170:171], v[130:131], 0, s[44:45]
	s_mov_b64 s[44:45], 0x24000
	v_lshl_add_u64 v[172:173], v[130:131], 0, s[44:45]
	s_mov_b64 s[44:45], 0x26000
	v_lshl_add_u64 v[174:175], v[130:131], 0, s[44:45]
	s_mov_b64 s[44:45], 0x28000
	v_lshl_add_u64 v[176:177], v[130:131], 0, s[44:45]
	s_mov_b64 s[44:45], 0x2a000
	v_lshl_add_u64 v[178:179], v[130:131], 0, s[44:45]
	s_mov_b64 s[44:45], 0x2c000
	v_lshl_add_u64 v[180:181], v[130:131], 0, s[44:45]
	s_mov_b64 s[44:45], 0x2e000
	v_lshl_add_u64 v[2:3], v[168:169], 0, s[30:31]
	v_lshl_add_u64 v[4:5], v[170:171], 0, s[30:31]
	v_lshl_add_u64 v[10:11], v[172:173], 0, s[30:31]
	v_lshl_add_u64 v[12:13], v[174:175], 0, s[30:31]
	v_lshl_add_u64 v[18:19], v[176:177], 0, s[30:31]
	v_lshl_add_u64 v[20:21], v[178:179], 0, s[30:31]
	v_lshl_add_u64 v[182:183], v[130:131], 0, s[44:45]
	v_lshl_add_u64 v[42:43], v[180:181], 0, s[30:31]
	v_lshl_add_u64 v[44:45], v[182:183], 0, s[30:31]
	global_load_dwordx4 v[106:109], v[2:3], off nt
	global_load_dwordx4 v[98:101], v[4:5], off nt
	global_load_dwordx4 v[78:81], v[10:11], off nt
	global_load_dwordx4 v[66:69], v[12:13], off nt
	global_load_dwordx4 v[38:41], v[18:19], off nt
	s_nop 0
	global_load_dwordx4 v[18:21], v[20:21], off nt
	s_nop 0
	global_load_dwordx4 v[10:13], v[42:43], off nt
	global_load_dwordx4 v[2:5], v[44:45], off nt
	v_mov_b32_e32 v42, v198
	s_waitcnt vmcnt(23)
	s_waitcnt vmcnt(22)
	s_waitcnt vmcnt(21)
	s_waitcnt vmcnt(20)
	s_waitcnt vmcnt(19)
	s_waitcnt vmcnt(18)
	s_waitcnt vmcnt(17)
	s_waitcnt vmcnt(16)
	ds_read_b32 v42, v187
	s_waitcnt lgkmcnt(0)
	v_pk_fma_f32 v[44:45], v[42:43], v[74:75], 0 op_sel_hi:[0,1,0] neg_lo:[1,0,0] neg_hi:[1,0,0]
	v_pk_fma_f32 v[42:43], v[42:43], v[76:77], 0 op_sel_hi:[0,1,0] neg_lo:[1,0,0] neg_hi:[1,0,0]
	v_cvt_pk_bf16_f32 v44, v44, v45
	v_cvt_pk_bf16_f32 v45, v42, v43
	ds_write_b64 v186, v[44:45]
	ds_read_b32 v42, v187 offset:8
	s_waitcnt lgkmcnt(0)
	v_pk_fma_f32 v[44:45], v[42:43], v[62:63], 0 op_sel_hi:[0,1,0] neg_lo:[1,0,0] neg_hi:[1,0,0]
	v_pk_fma_f32 v[42:43], v[42:43], v[64:65], 0 op_sel_hi:[0,1,0] neg_lo:[1,0,0] neg_hi:[1,0,0]
	v_cvt_pk_bf16_f32 v44, v44, v45
	v_cvt_pk_bf16_f32 v45, v42, v43
	ds_write_b64 v186, v[44:45] offset:544
	ds_read_b32 v42, v187 offset:16
	s_waitcnt lgkmcnt(0)
	v_pk_fma_f32 v[44:45], v[42:43], v[58:59], 0 op_sel_hi:[0,1,0] neg_lo:[1,0,0] neg_hi:[1,0,0]
	v_pk_fma_f32 v[42:43], v[42:43], v[60:61], 0 op_sel_hi:[0,1,0] neg_lo:[1,0,0] neg_hi:[1,0,0]
	v_cvt_pk_bf16_f32 v44, v44, v45
	v_cvt_pk_bf16_f32 v45, v42, v43
	ds_write_b64 v186, v[44:45] offset:1088
	ds_read_b32 v42, v187 offset:24
	s_waitcnt lgkmcnt(0)
	v_pk_fma_f32 v[44:45], v[42:43], v[46:47], 0 op_sel_hi:[0,1,0] neg_lo:[1,0,0] neg_hi:[1,0,0]
	v_pk_fma_f32 v[42:43], v[42:43], v[48:49], 0 op_sel_hi:[0,1,0] neg_lo:[1,0,0] neg_hi:[1,0,0]
	v_cvt_pk_bf16_f32 v44, v44, v45
	v_cvt_pk_bf16_f32 v45, v42, v43
	ds_write_b64 v186, v[44:45] offset:1632
	ds_read_b32 v42, v187 offset:32
	s_waitcnt lgkmcnt(0)
	v_pk_fma_f32 v[44:45], v[42:43], v[50:51], 0 op_sel_hi:[0,1,0] neg_lo:[1,0,0] neg_hi:[1,0,0]
	v_pk_fma_f32 v[42:43], v[42:43], v[52:53], 0 op_sel_hi:[0,1,0] neg_lo:[1,0,0] neg_hi:[1,0,0]
	v_cvt_pk_bf16_f32 v44, v44, v45
	v_cvt_pk_bf16_f32 v45, v42, v43
	ds_write_b64 v186, v[44:45] offset:2176
	ds_read_b32 v42, v187 offset:40
	s_waitcnt lgkmcnt(0)
	v_pk_fma_f32 v[30:31], v[42:43], v[30:31], 0 op_sel_hi:[0,1,0] neg_lo:[1,0,0] neg_hi:[1,0,0]
	v_pk_fma_f32 v[32:33], v[42:43], v[32:33], 0 op_sel_hi:[0,1,0] neg_lo:[1,0,0] neg_hi:[1,0,0]
	v_cvt_pk_bf16_f32 v30, v30, v31
	v_cvt_pk_bf16_f32 v31, v32, v33
	ds_write_b64 v186, v[30:31] offset:2720
	ds_read_b32 v30, v187 offset:48
	s_waitcnt lgkmcnt(0)
	v_pk_fma_f32 v[32:33], v[30:31], v[34:35], 0 op_sel_hi:[0,1,0] neg_lo:[1,0,0] neg_hi:[1,0,0]
	v_pk_fma_f32 v[30:31], v[30:31], v[36:37], 0 op_sel_hi:[0,1,0] neg_lo:[1,0,0] neg_hi:[1,0,0]
	v_cvt_pk_bf16_f32 v32, v32, v33
	v_cvt_pk_bf16_f32 v33, v30, v31
	ds_write_b64 v186, v[32:33] offset:3264
	ds_read_b32 v30, v187 offset:56
	s_waitcnt lgkmcnt(0)
	v_pk_fma_f32 v[22:23], v[30:31], v[22:23], 0 op_sel_hi:[0,1,0] neg_lo:[1,0,0] neg_hi:[1,0,0]
	v_pk_fma_f32 v[24:25], v[30:31], v[24:25], 0 op_sel_hi:[0,1,0] neg_lo:[1,0,0] neg_hi:[1,0,0]
	v_cvt_pk_bf16_f32 v22, v22, v23
	v_cvt_pk_bf16_f32 v23, v24, v25
	ds_write_b64 v186, v[22:23] offset:3808
	ds_read_b128 a[0:3], v1
	ds_read_b128 a[4:7], v1 offset:64
	ds_read_b128 a[8:11], v1 offset:128
	ds_read_b128 a[12:15], v1 offset:192
	v_lshl_add_u64 v[22:23], v[130:131], 0, s[28:29]
	v_add_co_u32_e32 v24, vcc, s7, v22
	s_nop 1
	v_addc_co_u32_e32 v25, vcc, 0, v23, vcc
	global_load_dwordx4 v[102:105], v[22:23], off nt
	global_load_dwordx4 v[86:89], v[24:25], off nt
	v_add_co_u32_e32 v24, vcc, s36, v22
	s_nop 1
	v_addc_co_u32_e32 v25, vcc, 0, v23, vcc
	v_add_co_u32_e32 v30, vcc, s37, v22
	s_nop 1
	v_addc_co_u32_e32 v31, vcc, 0, v23, vcc
	global_load_dwordx4 v[74:77], v[24:25], off nt
	global_load_dwordx4 v[62:65], v[30:31], off nt
	v_add_co_u32_e32 v24, vcc, s38, v22
	s_nop 1
	v_addc_co_u32_e32 v25, vcc, 0, v23, vcc
	v_add_co_u32_e32 v30, vcc, s39, v22
	s_nop 1
	v_addc_co_u32_e32 v31, vcc, 0, v23, vcc
	global_load_dwordx4 v[58:61], v[24:25], off nt
	global_load_dwordx4 v[46:49], v[30:31], off nt
	v_add_co_u32_e32 v24, vcc, s41, v22
	s_nop 1
	v_addc_co_u32_e32 v25, vcc, 0, v23, vcc
	v_add_co_u32_e32 v22, vcc, s42, v22
	s_nop 1
	v_addc_co_u32_e32 v23, vcc, 0, v23, vcc
	global_load_dwordx4 v[42:45], v[24:25], off nt
	global_load_dwordx4 v[30:33], v[22:23], off nt
	v_mov_b32_e32 v22, v198
	s_waitcnt vmcnt(23)
	s_waitcnt vmcnt(22)
	s_waitcnt vmcnt(21)
	s_waitcnt vmcnt(20)
	s_waitcnt vmcnt(19)
	s_waitcnt vmcnt(18)
	s_waitcnt vmcnt(17)
	s_waitcnt vmcnt(16)
	ds_read_b32 v22, v187 offset:64
	s_waitcnt lgkmcnt(0)
	v_pk_fma_f32 v[24:25], v[22:23], v[94:95], 0 op_sel_hi:[0,1,0] neg_lo:[1,0,0] neg_hi:[1,0,0]
	v_pk_fma_f32 v[22:23], v[22:23], v[96:97], 0 op_sel_hi:[0,1,0] neg_lo:[1,0,0] neg_hi:[1,0,0]
	v_cvt_pk_bf16_f32 v24, v24, v25
	v_cvt_pk_bf16_f32 v25, v22, v23
	ds_write_b64 v186, v[24:25]
	ds_read_b32 v22, v187 offset:72
	s_waitcnt lgkmcnt(0)
	v_pk_fma_f32 v[24:25], v[22:23], v[90:91], 0 op_sel_hi:[0,1,0] neg_lo:[1,0,0] neg_hi:[1,0,0]
	v_pk_fma_f32 v[22:23], v[22:23], v[92:93], 0 op_sel_hi:[0,1,0] neg_lo:[1,0,0] neg_hi:[1,0,0]
	v_cvt_pk_bf16_f32 v24, v24, v25
	v_cvt_pk_bf16_f32 v25, v22, v23
	ds_write_b64 v186, v[24:25] offset:544
	ds_read_b32 v22, v187 offset:80
	s_waitcnt lgkmcnt(0)
	v_pk_fma_f32 v[24:25], v[22:23], v[82:83], 0 op_sel_hi:[0,1,0] neg_lo:[1,0,0] neg_hi:[1,0,0]
	v_pk_fma_f32 v[22:23], v[22:23], v[84:85], 0 op_sel_hi:[0,1,0] neg_lo:[1,0,0] neg_hi:[1,0,0]
	v_cvt_pk_bf16_f32 v24, v24, v25
	v_cvt_pk_bf16_f32 v25, v22, v23
	ds_write_b64 v186, v[24:25] offset:1088
	ds_read_b32 v22, v187 offset:88
	s_waitcnt lgkmcnt(0)
	v_pk_fma_f32 v[24:25], v[22:23], v[70:71], 0 op_sel_hi:[0,1,0] neg_lo:[1,0,0] neg_hi:[1,0,0]
	v_pk_fma_f32 v[22:23], v[22:23], v[72:73], 0 op_sel_hi:[0,1,0] neg_lo:[1,0,0] neg_hi:[1,0,0]
	v_cvt_pk_bf16_f32 v24, v24, v25
	v_cvt_pk_bf16_f32 v25, v22, v23
	ds_write_b64 v186, v[24:25] offset:1632
	ds_read_b32 v22, v187 offset:96
	s_waitcnt lgkmcnt(0)
	v_pk_fma_f32 v[24:25], v[22:23], v[54:55], 0 op_sel_hi:[0,1,0] neg_lo:[1,0,0] neg_hi:[1,0,0]
	v_pk_fma_f32 v[22:23], v[22:23], v[56:57], 0 op_sel_hi:[0,1,0] neg_lo:[1,0,0] neg_hi:[1,0,0]
	v_cvt_pk_bf16_f32 v24, v24, v25
	v_cvt_pk_bf16_f32 v25, v22, v23
	ds_write_b64 v186, v[24:25] offset:2176
	ds_read_b32 v22, v187 offset:104
	s_waitcnt lgkmcnt(0)
	v_pk_fma_f32 v[24:25], v[22:23], v[26:27], 0 op_sel_hi:[0,1,0] neg_lo:[1,0,0] neg_hi:[1,0,0]
	v_pk_fma_f32 v[22:23], v[22:23], v[28:29], 0 op_sel_hi:[0,1,0] neg_lo:[1,0,0] neg_hi:[1,0,0]
	v_cvt_pk_bf16_f32 v24, v24, v25
	v_cvt_pk_bf16_f32 v25, v22, v23
	ds_write_b64 v186, v[24:25] offset:2720
	ds_read_b32 v22, v187 offset:112
	s_waitcnt lgkmcnt(0)
	v_pk_fma_f32 v[14:15], v[22:23], v[14:15], 0 op_sel_hi:[0,1,0] neg_lo:[1,0,0] neg_hi:[1,0,0]
	v_pk_fma_f32 v[16:17], v[22:23], v[16:17], 0 op_sel_hi:[0,1,0] neg_lo:[1,0,0] neg_hi:[1,0,0]
	v_cvt_pk_bf16_f32 v14, v14, v15
	v_cvt_pk_bf16_f32 v15, v16, v17
	ds_write_b64 v186, v[14:15] offset:3264
	ds_read_b32 v14, v187 offset:120
	s_waitcnt lgkmcnt(0)
	v_pk_fma_f32 v[6:7], v[14:15], v[6:7], 0 op_sel_hi:[0,1,0] neg_lo:[1,0,0] neg_hi:[1,0,0]
	v_pk_fma_f32 v[8:9], v[14:15], v[8:9], 0 op_sel_hi:[0,1,0] neg_lo:[1,0,0] neg_hi:[1,0,0]
	v_cvt_pk_bf16_f32 v6, v6, v7
	v_cvt_pk_bf16_f32 v7, v8, v9
	ds_write_b64 v186, v[6:7] offset:3808
	ds_read_b128 a[16:19], v1
	ds_read_b128 a[20:23], v1 offset:64
	ds_read_b128 a[24:27], v1 offset:128
	ds_read_b128 a[28:31], v1 offset:192
	v_lshl_add_u64 v[6:7], v[150:151], 0, s[28:29]
	v_lshl_add_u64 v[8:9], v[152:153], 0, s[28:29]
	v_lshl_add_u64 v[14:15], v[156:157], 0, s[28:29]
	v_lshl_add_u64 v[16:17], v[158:159], 0, s[28:29]
	v_lshl_add_u64 v[22:23], v[160:161], 0, s[28:29]
	v_lshl_add_u64 v[24:25], v[162:163], 0, s[28:29]
	v_lshl_add_u64 v[26:27], v[164:165], 0, s[28:29]
	v_lshl_add_u64 v[28:29], v[166:167], 0, s[28:29]
	global_load_dwordx4 v[110:113], v[6:7], off nt
	global_load_dwordx4 v[90:93], v[8:9], off nt
	global_load_dwordx4 v[70:73], v[14:15], off nt
	global_load_dwordx4 v[50:53], v[16:17], off nt
	global_load_dwordx4 v[34:37], v[22:23], off nt
	s_nop 0
	global_load_dwordx4 v[22:25], v[24:25], off nt
	s_nop 0
	global_load_dwordx4 v[14:17], v[26:27], off nt
	global_load_dwordx4 v[6:9], v[28:29], off nt
	s_waitcnt vmcnt(23)
	s_waitcnt vmcnt(22)
	s_waitcnt vmcnt(21)
	s_waitcnt vmcnt(20)
	s_waitcnt vmcnt(19)
	s_waitcnt vmcnt(18)
	s_waitcnt vmcnt(17)
	s_waitcnt vmcnt(16)
	ds_read_b32 v26, v187 offset:128
	s_waitcnt lgkmcnt(0)
	v_pk_fma_f32 v[28:29], v[26:27], v[106:107], 0 op_sel_hi:[0,1,0] neg_lo:[1,0,0] neg_hi:[1,0,0]
	v_pk_fma_f32 v[26:27], v[26:27], v[108:109], 0 op_sel_hi:[0,1,0] neg_lo:[1,0,0] neg_hi:[1,0,0]
	v_cvt_pk_bf16_f32 v28, v28, v29
	v_cvt_pk_bf16_f32 v29, v26, v27
	ds_write_b64 v186, v[28:29]
	ds_read_b32 v26, v187 offset:136
	s_waitcnt lgkmcnt(0)
	v_pk_fma_f32 v[28:29], v[26:27], v[98:99], 0 op_sel_hi:[0,1,0] neg_lo:[1,0,0] neg_hi:[1,0,0]
	v_pk_fma_f32 v[26:27], v[26:27], v[100:101], 0 op_sel_hi:[0,1,0] neg_lo:[1,0,0] neg_hi:[1,0,0]
	v_cvt_pk_bf16_f32 v28, v28, v29
	v_cvt_pk_bf16_f32 v29, v26, v27
	ds_write_b64 v186, v[28:29] offset:544
	ds_read_b32 v26, v187 offset:144
	s_waitcnt lgkmcnt(0)
	v_pk_fma_f32 v[28:29], v[26:27], v[78:79], 0 op_sel_hi:[0,1,0] neg_lo:[1,0,0] neg_hi:[1,0,0]
	v_pk_fma_f32 v[26:27], v[26:27], v[80:81], 0 op_sel_hi:[0,1,0] neg_lo:[1,0,0] neg_hi:[1,0,0]
	v_cvt_pk_bf16_f32 v28, v28, v29
	v_cvt_pk_bf16_f32 v29, v26, v27
	ds_write_b64 v186, v[28:29] offset:1088
	ds_read_b32 v26, v187 offset:152
	s_waitcnt lgkmcnt(0)
	v_pk_fma_f32 v[28:29], v[26:27], v[66:67], 0 op_sel_hi:[0,1,0] neg_lo:[1,0,0] neg_hi:[1,0,0]
	v_pk_fma_f32 v[26:27], v[26:27], v[68:69], 0 op_sel_hi:[0,1,0] neg_lo:[1,0,0] neg_hi:[1,0,0]
	v_cvt_pk_bf16_f32 v28, v28, v29
	v_cvt_pk_bf16_f32 v29, v26, v27
	ds_write_b64 v186, v[28:29] offset:1632
	ds_read_b32 v26, v187 offset:160
	s_waitcnt lgkmcnt(0)
	v_pk_fma_f32 v[28:29], v[26:27], v[38:39], 0 op_sel_hi:[0,1,0] neg_lo:[1,0,0] neg_hi:[1,0,0]
	v_pk_fma_f32 v[26:27], v[26:27], v[40:41], 0 op_sel_hi:[0,1,0] neg_lo:[1,0,0] neg_hi:[1,0,0]
	v_cvt_pk_bf16_f32 v28, v28, v29
	v_cvt_pk_bf16_f32 v29, v26, v27
	ds_write_b64 v186, v[28:29] offset:2176
	ds_read_b32 v26, v187 offset:168
	s_waitcnt lgkmcnt(0)
	v_pk_fma_f32 v[18:19], v[26:27], v[18:19], 0 op_sel_hi:[0,1,0] neg_lo:[1,0,0] neg_hi:[1,0,0]
	v_pk_fma_f32 v[20:21], v[26:27], v[20:21], 0 op_sel_hi:[0,1,0] neg_lo:[1,0,0] neg_hi:[1,0,0]
	v_cvt_pk_bf16_f32 v18, v18, v19
	v_cvt_pk_bf16_f32 v19, v20, v21
	ds_write_b64 v186, v[18:19] offset:2720
	ds_read_b32 v18, v187 offset:176
	s_waitcnt lgkmcnt(0)
	v_pk_fma_f32 v[10:11], v[18:19], v[10:11], 0 op_sel_hi:[0,1,0] neg_lo:[1,0,0] neg_hi:[1,0,0]
	v_pk_fma_f32 v[12:13], v[18:19], v[12:13], 0 op_sel_hi:[0,1,0] neg_lo:[1,0,0] neg_hi:[1,0,0]
	v_cvt_pk_bf16_f32 v10, v10, v11
	v_cvt_pk_bf16_f32 v11, v12, v13
	ds_write_b64 v186, v[10:11] offset:3264
	ds_read_b32 v10, v187 offset:184
	s_waitcnt lgkmcnt(0)
	v_pk_fma_f32 v[2:3], v[10:11], v[2:3], 0 op_sel_hi:[0,1,0] neg_lo:[1,0,0] neg_hi:[1,0,0]
	v_pk_fma_f32 v[4:5], v[10:11], v[4:5], 0 op_sel_hi:[0,1,0] neg_lo:[1,0,0] neg_hi:[1,0,0]
	v_cvt_pk_bf16_f32 v2, v2, v3
	v_cvt_pk_bf16_f32 v3, v4, v5
	ds_write_b64 v186, v[2:3] offset:3808
	ds_read_b128 a[32:35], v1
	ds_read_b128 a[36:39], v1 offset:64
	ds_read_b128 a[40:43], v1 offset:128
	ds_read_b128 a[44:47], v1 offset:192
	v_lshl_add_u64 v[2:3], v[168:169], 0, s[28:29]
	v_lshl_add_u64 v[4:5], v[170:171], 0, s[28:29]
	v_lshl_add_u64 v[10:11], v[172:173], 0, s[28:29]
	v_lshl_add_u64 v[12:13], v[174:175], 0, s[28:29]
	v_lshl_add_u64 v[18:19], v[176:177], 0, s[28:29]
	v_lshl_add_u64 v[20:21], v[178:179], 0, s[28:29]
	v_lshl_add_u64 v[26:27], v[180:181], 0, s[28:29]
	v_lshl_add_u64 v[28:29], v[182:183], 0, s[28:29]
	global_load_dwordx4 v[106:109], v[2:3], off nt
	global_load_dwordx4 v[94:97], v[4:5], off nt
	global_load_dwordx4 v[66:69], v[10:11], off nt
	global_load_dwordx4 v[54:57], v[12:13], off nt
	global_load_dwordx4 v[38:41], v[18:19], off nt
	s_nop 0
	global_load_dwordx4 v[18:21], v[20:21], off nt
	s_nop 0
	global_load_dwordx4 v[10:13], v[26:27], off nt
	global_load_dwordx4 v[2:5], v[28:29], off nt
	v_mov_b32_e32 v26, v197
	s_waitcnt vmcnt(23)
	s_waitcnt vmcnt(22)
	s_waitcnt vmcnt(21)
	s_waitcnt vmcnt(20)
	s_waitcnt vmcnt(19)
	s_waitcnt vmcnt(18)
	s_waitcnt vmcnt(17)
	s_waitcnt vmcnt(16)
	ds_read_b32 v26, v187
	s_waitcnt lgkmcnt(0)
	v_pk_fma_f32 v[28:29], v[26:27], v[102:103], 0 op_sel_hi:[0,1,0] neg_lo:[1,0,0] neg_hi:[1,0,0]
	v_pk_fma_f32 v[26:27], v[26:27], v[104:105], 0 op_sel_hi:[0,1,0] neg_lo:[1,0,0] neg_hi:[1,0,0]
	v_cvt_pk_bf16_f32 v28, v28, v29
	v_cvt_pk_bf16_f32 v29, v26, v27
	ds_write_b64 v186, v[28:29]
	ds_read_b32 v26, v187 offset:8
	s_waitcnt lgkmcnt(0)
	v_pk_fma_f32 v[28:29], v[26:27], v[86:87], 0 op_sel_hi:[0,1,0] neg_lo:[1,0,0] neg_hi:[1,0,0]
	v_pk_fma_f32 v[26:27], v[26:27], v[88:89], 0 op_sel_hi:[0,1,0] neg_lo:[1,0,0] neg_hi:[1,0,0]
	v_cvt_pk_bf16_f32 v28, v28, v29
	v_cvt_pk_bf16_f32 v29, v26, v27
	ds_write_b64 v186, v[28:29] offset:544
	ds_read_b32 v26, v187 offset:16
	s_waitcnt lgkmcnt(0)
	v_pk_fma_f32 v[28:29], v[26:27], v[74:75], 0 op_sel_hi:[0,1,0] neg_lo:[1,0,0] neg_hi:[1,0,0]
	v_pk_fma_f32 v[26:27], v[26:27], v[76:77], 0 op_sel_hi:[0,1,0] neg_lo:[1,0,0] neg_hi:[1,0,0]
	v_cvt_pk_bf16_f32 v28, v28, v29
	v_cvt_pk_bf16_f32 v29, v26, v27
	ds_write_b64 v186, v[28:29] offset:1088
	ds_read_b32 v26, v187 offset:24
	s_waitcnt lgkmcnt(0)
	v_pk_fma_f32 v[28:29], v[26:27], v[62:63], 0 op_sel_hi:[0,1,0] neg_lo:[1,0,0] neg_hi:[1,0,0]
	v_pk_fma_f32 v[26:27], v[26:27], v[64:65], 0 op_sel_hi:[0,1,0] neg_lo:[1,0,0] neg_hi:[1,0,0]
	v_cvt_pk_bf16_f32 v28, v28, v29
	v_cvt_pk_bf16_f32 v29, v26, v27
	ds_write_b64 v186, v[28:29] offset:1632
	ds_read_b32 v26, v187 offset:32
	s_waitcnt lgkmcnt(0)
	v_pk_fma_f32 v[28:29], v[26:27], v[58:59], 0 op_sel_hi:[0,1,0] neg_lo:[1,0,0] neg_hi:[1,0,0]
	v_pk_fma_f32 v[26:27], v[26:27], v[60:61], 0 op_sel_hi:[0,1,0] neg_lo:[1,0,0] neg_hi:[1,0,0]
	v_cvt_pk_bf16_f32 v28, v28, v29
	v_cvt_pk_bf16_f32 v29, v26, v27
	ds_write_b64 v186, v[28:29] offset:2176
	ds_read_b32 v26, v187 offset:40
	s_waitcnt lgkmcnt(0)
	v_pk_fma_f32 v[28:29], v[26:27], v[46:47], 0 op_sel_hi:[0,1,0] neg_lo:[1,0,0] neg_hi:[1,0,0]
	v_pk_fma_f32 v[26:27], v[26:27], v[48:49], 0 op_sel_hi:[0,1,0] neg_lo:[1,0,0] neg_hi:[1,0,0]
	v_cvt_pk_bf16_f32 v28, v28, v29
	v_cvt_pk_bf16_f32 v29, v26, v27
	ds_write_b64 v186, v[28:29] offset:2720
	ds_read_b32 v26, v187 offset:48
	s_waitcnt lgkmcnt(0)
	v_pk_fma_f32 v[28:29], v[26:27], v[42:43], 0 op_sel_hi:[0,1,0] neg_lo:[1,0,0] neg_hi:[1,0,0]
	v_pk_fma_f32 v[26:27], v[26:27], v[44:45], 0 op_sel_hi:[0,1,0] neg_lo:[1,0,0] neg_hi:[1,0,0]
	v_cvt_pk_bf16_f32 v28, v28, v29
	v_cvt_pk_bf16_f32 v29, v26, v27
	ds_write_b64 v186, v[28:29] offset:3264
	ds_read_b32 v26, v187 offset:56
	s_waitcnt lgkmcnt(0)
	v_pk_fma_f32 v[28:29], v[26:27], v[30:31], 0 op_sel_hi:[0,1,0] neg_lo:[1,0,0] neg_hi:[1,0,0]
	v_pk_fma_f32 v[26:27], v[26:27], v[32:33], 0 op_sel_hi:[0,1,0] neg_lo:[1,0,0] neg_hi:[1,0,0]
	v_cvt_pk_bf16_f32 v28, v28, v29
	v_cvt_pk_bf16_f32 v29, v26, v27
	ds_write_b64 v186, v[28:29] offset:3808
	ds_read_b128 a[48:51], v1
	ds_read_b128 a[52:55], v1 offset:64
	ds_read_b128 a[56:59], v1 offset:128
	ds_read_b128 a[60:63], v1 offset:192
	v_lshl_add_u64 v[26:27], v[130:131], 0, s[26:27]
	v_add_co_u32_e32 v28, vcc, s7, v26
	s_nop 1
	v_addc_co_u32_e32 v29, vcc, 0, v27, vcc
	global_load_dwordx4 v[86:89], v[26:27], off nt
	global_load_dwordx4 v[82:85], v[28:29], off nt
	v_add_co_u32_e32 v28, vcc, s36, v26
	s_nop 1
	v_addc_co_u32_e32 v29, vcc, 0, v27, vcc
	v_add_co_u32_e32 v30, vcc, s37, v26
	s_nop 1
	v_addc_co_u32_e32 v31, vcc, 0, v27, vcc
	global_load_dwordx4 v[78:81], v[28:29], off nt
	global_load_dwordx4 v[58:61], v[30:31], off nt
	v_add_co_u32_e32 v28, vcc, s38, v26
	s_nop 1
	v_addc_co_u32_e32 v29, vcc, 0, v27, vcc
	v_add_co_u32_e32 v30, vcc, s39, v26
	s_nop 1
	v_addc_co_u32_e32 v31, vcc, 0, v27, vcc
	global_load_dwordx4 v[46:49], v[28:29], off nt
	global_load_dwordx4 v[42:45], v[30:31], off nt
	v_add_co_u32_e32 v28, vcc, s41, v26
	s_nop 1
	v_addc_co_u32_e32 v29, vcc, 0, v27, vcc
	v_add_co_u32_e32 v26, vcc, s42, v26
	s_nop 1
	v_addc_co_u32_e32 v27, vcc, 0, v27, vcc
	global_load_dwordx4 v[30:33], v[28:29], off nt
	s_nop 0
	global_load_dwordx4 v[26:29], v[26:27], off nt
	v_mov_b32_e32 v62, v197
	s_waitcnt vmcnt(23)
	s_waitcnt vmcnt(22)
	s_waitcnt vmcnt(21)
	s_waitcnt vmcnt(20)
	s_waitcnt vmcnt(19)
	s_waitcnt vmcnt(18)
	s_waitcnt vmcnt(17)
	s_waitcnt vmcnt(16)
	ds_read_b32 v62, v187 offset:64
	s_waitcnt lgkmcnt(0)
	v_pk_fma_f32 v[64:65], v[62:63], v[110:111], 0 op_sel_hi:[0,1,0] neg_lo:[1,0,0] neg_hi:[1,0,0]
	v_pk_fma_f32 v[62:63], v[62:63], v[112:113], 0 op_sel_hi:[0,1,0] neg_lo:[1,0,0] neg_hi:[1,0,0]
	v_cvt_pk_bf16_f32 v64, v64, v65
	v_cvt_pk_bf16_f32 v65, v62, v63
	ds_write_b64 v186, v[64:65]
	ds_read_b32 v62, v187 offset:72
	s_waitcnt lgkmcnt(0)
	v_pk_fma_f32 v[64:65], v[62:63], v[90:91], 0 op_sel_hi:[0,1,0] neg_lo:[1,0,0] neg_hi:[1,0,0]
	v_pk_fma_f32 v[62:63], v[62:63], v[92:93], 0 op_sel_hi:[0,1,0] neg_lo:[1,0,0] neg_hi:[1,0,0]
	v_cvt_pk_bf16_f32 v64, v64, v65
	v_cvt_pk_bf16_f32 v65, v62, v63
	ds_write_b64 v186, v[64:65] offset:544
	ds_read_b32 v62, v187 offset:80
	s_waitcnt lgkmcnt(0)
	v_pk_fma_f32 v[64:65], v[62:63], v[70:71], 0 op_sel_hi:[0,1,0] neg_lo:[1,0,0] neg_hi:[1,0,0]
	v_pk_fma_f32 v[62:63], v[62:63], v[72:73], 0 op_sel_hi:[0,1,0] neg_lo:[1,0,0] neg_hi:[1,0,0]
	v_cvt_pk_bf16_f32 v64, v64, v65
	v_cvt_pk_bf16_f32 v65, v62, v63
	ds_write_b64 v186, v[64:65] offset:1088
	ds_read_b32 v62, v187 offset:88
	s_waitcnt lgkmcnt(0)
	v_pk_fma_f32 v[50:51], v[62:63], v[50:51], 0 op_sel_hi:[0,1,0] neg_lo:[1,0,0] neg_hi:[1,0,0]
	v_pk_fma_f32 v[52:53], v[62:63], v[52:53], 0 op_sel_hi:[0,1,0] neg_lo:[1,0,0] neg_hi:[1,0,0]
	v_cvt_pk_bf16_f32 v50, v50, v51
	v_cvt_pk_bf16_f32 v51, v52, v53
	ds_write_b64 v186, v[50:51] offset:1632
	ds_read_b32 v50, v187 offset:96
	s_waitcnt lgkmcnt(0)
	v_pk_fma_f32 v[34:35], v[50:51], v[34:35], 0 op_sel_hi:[0,1,0] neg_lo:[1,0,0] neg_hi:[1,0,0]
	v_pk_fma_f32 v[36:37], v[50:51], v[36:37], 0 op_sel_hi:[0,1,0] neg_lo:[1,0,0] neg_hi:[1,0,0]
	v_cvt_pk_bf16_f32 v34, v34, v35
	v_cvt_pk_bf16_f32 v35, v36, v37
	ds_write_b64 v186, v[34:35] offset:2176
	ds_read_b32 v34, v187 offset:104
	s_waitcnt lgkmcnt(0)
	v_pk_fma_f32 v[22:23], v[34:35], v[22:23], 0 op_sel_hi:[0,1,0] neg_lo:[1,0,0] neg_hi:[1,0,0]
	v_pk_fma_f32 v[24:25], v[34:35], v[24:25], 0 op_sel_hi:[0,1,0] neg_lo:[1,0,0] neg_hi:[1,0,0]
	v_cvt_pk_bf16_f32 v22, v22, v23
	v_cvt_pk_bf16_f32 v23, v24, v25
	ds_write_b64 v186, v[22:23] offset:2720
	ds_read_b32 v22, v187 offset:112
	s_waitcnt lgkmcnt(0)
	v_pk_fma_f32 v[14:15], v[22:23], v[14:15], 0 op_sel_hi:[0,1,0] neg_lo:[1,0,0] neg_hi:[1,0,0]
	v_pk_fma_f32 v[16:17], v[22:23], v[16:17], 0 op_sel_hi:[0,1,0] neg_lo:[1,0,0] neg_hi:[1,0,0]
	v_cvt_pk_bf16_f32 v14, v14, v15
	v_cvt_pk_bf16_f32 v15, v16, v17
	ds_write_b64 v186, v[14:15] offset:3264
	ds_read_b32 v14, v187 offset:120
	s_waitcnt lgkmcnt(0)
	v_pk_fma_f32 v[6:7], v[14:15], v[6:7], 0 op_sel_hi:[0,1,0] neg_lo:[1,0,0] neg_hi:[1,0,0]
	v_pk_fma_f32 v[8:9], v[14:15], v[8:9], 0 op_sel_hi:[0,1,0] neg_lo:[1,0,0] neg_hi:[1,0,0]
	v_cvt_pk_bf16_f32 v6, v6, v7
	v_cvt_pk_bf16_f32 v7, v8, v9
	ds_write_b64 v186, v[6:7] offset:3808
	ds_read_b128 a[64:67], v1
	ds_read_b128 a[68:71], v1 offset:64
	ds_read_b128 a[72:75], v1 offset:128
	ds_read_b128 a[76:79], v1 offset:192
	v_lshl_add_u64 v[6:7], v[150:151], 0, s[26:27]
	v_lshl_add_u64 v[8:9], v[152:153], 0, s[26:27]
	v_lshl_add_u64 v[14:15], v[156:157], 0, s[26:27]
	v_lshl_add_u64 v[16:17], v[158:159], 0, s[26:27]
	v_lshl_add_u64 v[22:23], v[160:161], 0, s[26:27]
	v_lshl_add_u64 v[24:25], v[162:163], 0, s[26:27]
	v_lshl_add_u64 v[70:71], v[164:165], 0, s[26:27]
	v_lshl_add_u64 v[72:73], v[166:167], 0, s[26:27]
	global_load_dwordx4 v[110:113], v[6:7], off nt
	global_load_dwordx4 v[98:101], v[8:9], off nt
	global_load_dwordx4 v[62:65], v[14:15], off nt
	global_load_dwordx4 v[50:53], v[16:17], off nt
	global_load_dwordx4 v[34:37], v[22:23], off nt
	s_nop 0
	global_load_dwordx4 v[22:25], v[24:25], off nt
	s_nop 0
	global_load_dwordx4 v[14:17], v[70:71], off nt
	global_load_dwordx4 v[6:9], v[72:73], off nt
	s_waitcnt vmcnt(23)
	s_waitcnt vmcnt(22)
	s_waitcnt vmcnt(21)
	s_waitcnt vmcnt(20)
	s_waitcnt vmcnt(19)
	s_waitcnt vmcnt(18)
	s_waitcnt vmcnt(17)
	s_waitcnt vmcnt(16)
	ds_read_b32 v70, v187 offset:128
	s_waitcnt lgkmcnt(0)
	v_pk_fma_f32 v[72:73], v[70:71], v[106:107], 0 op_sel_hi:[0,1,0] neg_lo:[1,0,0] neg_hi:[1,0,0]
	v_pk_fma_f32 v[70:71], v[70:71], v[108:109], 0 op_sel_hi:[0,1,0] neg_lo:[1,0,0] neg_hi:[1,0,0]
	v_cvt_pk_bf16_f32 v72, v72, v73
	v_cvt_pk_bf16_f32 v73, v70, v71
	ds_write_b64 v186, v[72:73]
	ds_read_b32 v70, v187 offset:136
	s_waitcnt lgkmcnt(0)
	v_pk_fma_f32 v[72:73], v[70:71], v[94:95], 0 op_sel_hi:[0,1,0] neg_lo:[1,0,0] neg_hi:[1,0,0]
	v_pk_fma_f32 v[70:71], v[70:71], v[96:97], 0 op_sel_hi:[0,1,0] neg_lo:[1,0,0] neg_hi:[1,0,0]
	v_cvt_pk_bf16_f32 v72, v72, v73
	v_cvt_pk_bf16_f32 v73, v70, v71
	ds_write_b64 v186, v[72:73] offset:544
	ds_read_b32 v70, v187 offset:144
	s_waitcnt lgkmcnt(0)
	v_pk_fma_f32 v[66:67], v[70:71], v[66:67], 0 op_sel_hi:[0,1,0] neg_lo:[1,0,0] neg_hi:[1,0,0]
	v_pk_fma_f32 v[68:69], v[70:71], v[68:69], 0 op_sel_hi:[0,1,0] neg_lo:[1,0,0] neg_hi:[1,0,0]
	v_cvt_pk_bf16_f32 v66, v66, v67
	v_cvt_pk_bf16_f32 v67, v68, v69
	ds_write_b64 v186, v[66:67] offset:1088
	ds_read_b32 v66, v187 offset:152
	s_waitcnt lgkmcnt(0)
	v_pk_fma_f32 v[54:55], v[66:67], v[54:55], 0 op_sel_hi:[0,1,0] neg_lo:[1,0,0] neg_hi:[1,0,0]
	v_pk_fma_f32 v[56:57], v[66:67], v[56:57], 0 op_sel_hi:[0,1,0] neg_lo:[1,0,0] neg_hi:[1,0,0]
	v_cvt_pk_bf16_f32 v54, v54, v55
	v_cvt_pk_bf16_f32 v55, v56, v57
	ds_write_b64 v186, v[54:55] offset:1632
	ds_read_b32 v54, v187 offset:160
	s_waitcnt lgkmcnt(0)
	v_pk_fma_f32 v[38:39], v[54:55], v[38:39], 0 op_sel_hi:[0,1,0] neg_lo:[1,0,0] neg_hi:[1,0,0]
	v_pk_fma_f32 v[40:41], v[54:55], v[40:41], 0 op_sel_hi:[0,1,0] neg_lo:[1,0,0] neg_hi:[1,0,0]
	v_cvt_pk_bf16_f32 v38, v38, v39
	v_cvt_pk_bf16_f32 v39, v40, v41
	ds_write_b64 v186, v[38:39] offset:2176
	ds_read_b32 v38, v187 offset:168
	s_waitcnt lgkmcnt(0)
	v_pk_fma_f32 v[18:19], v[38:39], v[18:19], 0 op_sel_hi:[0,1,0] neg_lo:[1,0,0] neg_hi:[1,0,0]
	v_pk_fma_f32 v[20:21], v[38:39], v[20:21], 0 op_sel_hi:[0,1,0] neg_lo:[1,0,0] neg_hi:[1,0,0]
	v_cvt_pk_bf16_f32 v18, v18, v19
	v_cvt_pk_bf16_f32 v19, v20, v21
	ds_write_b64 v186, v[18:19] offset:2720
	ds_read_b32 v18, v187 offset:176
	s_waitcnt lgkmcnt(0)
	v_pk_fma_f32 v[10:11], v[18:19], v[10:11], 0 op_sel_hi:[0,1,0] neg_lo:[1,0,0] neg_hi:[1,0,0]
	v_pk_fma_f32 v[12:13], v[18:19], v[12:13], 0 op_sel_hi:[0,1,0] neg_lo:[1,0,0] neg_hi:[1,0,0]
	v_cvt_pk_bf16_f32 v10, v10, v11
	v_cvt_pk_bf16_f32 v11, v12, v13
	ds_write_b64 v186, v[10:11] offset:3264
	ds_read_b32 v10, v187 offset:184
	s_waitcnt lgkmcnt(0)
	v_pk_fma_f32 v[2:3], v[10:11], v[2:3], 0 op_sel_hi:[0,1,0] neg_lo:[1,0,0] neg_hi:[1,0,0]
	v_pk_fma_f32 v[4:5], v[10:11], v[4:5], 0 op_sel_hi:[0,1,0] neg_lo:[1,0,0] neg_hi:[1,0,0]
	v_cvt_pk_bf16_f32 v2, v2, v3
	v_cvt_pk_bf16_f32 v3, v4, v5
	ds_write_b64 v186, v[2:3] offset:3808
	ds_read_b128 a[80:83], v1
	ds_read_b128 a[84:87], v1 offset:64
	ds_read_b128 a[88:91], v1 offset:128
	ds_read_b128 a[92:95], v1 offset:192
	v_lshl_add_u64 v[2:3], v[168:169], 0, s[26:27]
	v_lshl_add_u64 v[4:5], v[170:171], 0, s[26:27]
	v_lshl_add_u64 v[10:11], v[172:173], 0, s[26:27]
	v_lshl_add_u64 v[12:13], v[174:175], 0, s[26:27]
	v_lshl_add_u64 v[18:19], v[176:177], 0, s[26:27]
	v_lshl_add_u64 v[20:21], v[178:179], 0, s[26:27]
	v_lshl_add_u64 v[66:67], v[180:181], 0, s[26:27]
	v_lshl_add_u64 v[68:69], v[182:183], 0, s[26:27]
	global_load_dwordx4 v[106:109], v[2:3], off nt
	global_load_dwordx4 v[94:97], v[4:5], off nt
	global_load_dwordx4 v[74:77], v[10:11], off nt
	global_load_dwordx4 v[54:57], v[12:13], off nt
	global_load_dwordx4 v[38:41], v[18:19], off nt
	s_nop 0
	global_load_dwordx4 v[18:21], v[20:21], off nt
	s_nop 0
	global_load_dwordx4 v[10:13], v[66:67], off nt
	global_load_dwordx4 v[2:5], v[68:69], off nt
	v_mov_b32_e32 v66, v196
	s_waitcnt vmcnt(23)
	s_waitcnt vmcnt(22)
	s_waitcnt vmcnt(21)
	s_waitcnt vmcnt(20)
	s_waitcnt vmcnt(19)
	s_waitcnt vmcnt(18)
	s_waitcnt vmcnt(17)
	s_waitcnt vmcnt(16)
	ds_read_b32 v66, v187
	s_waitcnt lgkmcnt(0)
	v_pk_fma_f32 v[68:69], v[66:67], v[86:87], 0 op_sel_hi:[0,1,0] neg_lo:[1,0,0] neg_hi:[1,0,0]
	v_pk_fma_f32 v[66:67], v[66:67], v[88:89], 0 op_sel_hi:[0,1,0] neg_lo:[1,0,0] neg_hi:[1,0,0]
	v_cvt_pk_bf16_f32 v68, v68, v69
	v_cvt_pk_bf16_f32 v69, v66, v67
	ds_write_b64 v186, v[68:69]
	ds_read_b32 v66, v187 offset:8
	s_waitcnt lgkmcnt(0)
	v_pk_fma_f32 v[68:69], v[66:67], v[82:83], 0 op_sel_hi:[0,1,0] neg_lo:[1,0,0] neg_hi:[1,0,0]
	v_pk_fma_f32 v[66:67], v[66:67], v[84:85], 0 op_sel_hi:[0,1,0] neg_lo:[1,0,0] neg_hi:[1,0,0]
	v_cvt_pk_bf16_f32 v68, v68, v69
	v_cvt_pk_bf16_f32 v69, v66, v67
	ds_write_b64 v186, v[68:69] offset:544
	ds_read_b32 v66, v187 offset:16
	s_waitcnt lgkmcnt(0)
	v_pk_fma_f32 v[68:69], v[66:67], v[78:79], 0 op_sel_hi:[0,1,0] neg_lo:[1,0,0] neg_hi:[1,0,0]
	v_pk_fma_f32 v[66:67], v[66:67], v[80:81], 0 op_sel_hi:[0,1,0] neg_lo:[1,0,0] neg_hi:[1,0,0]
	v_cvt_pk_bf16_f32 v68, v68, v69
	v_cvt_pk_bf16_f32 v69, v66, v67
	ds_write_b64 v186, v[68:69] offset:1088
	ds_read_b32 v66, v187 offset:24
	s_waitcnt lgkmcnt(0)
	v_pk_fma_f32 v[58:59], v[66:67], v[58:59], 0 op_sel_hi:[0,1,0] neg_lo:[1,0,0] neg_hi:[1,0,0]
	v_pk_fma_f32 v[60:61], v[66:67], v[60:61], 0 op_sel_hi:[0,1,0] neg_lo:[1,0,0] neg_hi:[1,0,0]
	v_cvt_pk_bf16_f32 v58, v58, v59
	v_cvt_pk_bf16_f32 v59, v60, v61
	ds_write_b64 v186, v[58:59] offset:1632
	ds_read_b32 v58, v187 offset:32
	s_waitcnt lgkmcnt(0)
	v_pk_fma_f32 v[46:47], v[58:59], v[46:47], 0 op_sel_hi:[0,1,0] neg_lo:[1,0,0] neg_hi:[1,0,0]
	v_pk_fma_f32 v[48:49], v[58:59], v[48:49], 0 op_sel_hi:[0,1,0] neg_lo:[1,0,0] neg_hi:[1,0,0]
	v_cvt_pk_bf16_f32 v46, v46, v47
	v_cvt_pk_bf16_f32 v47, v48, v49
	ds_write_b64 v186, v[46:47] offset:2176
	ds_read_b32 v46, v187 offset:40
	s_waitcnt lgkmcnt(0)
	v_pk_fma_f32 v[42:43], v[46:47], v[42:43], 0 op_sel_hi:[0,1,0] neg_lo:[1,0,0] neg_hi:[1,0,0]
	v_pk_fma_f32 v[44:45], v[46:47], v[44:45], 0 op_sel_hi:[0,1,0] neg_lo:[1,0,0] neg_hi:[1,0,0]
	v_cvt_pk_bf16_f32 v42, v42, v43
	v_cvt_pk_bf16_f32 v43, v44, v45
	ds_write_b64 v186, v[42:43] offset:2720
	ds_read_b32 v42, v187 offset:48
	s_waitcnt lgkmcnt(0)
	v_pk_fma_f32 v[30:31], v[42:43], v[30:31], 0 op_sel_hi:[0,1,0] neg_lo:[1,0,0] neg_hi:[1,0,0]
	v_pk_fma_f32 v[32:33], v[42:43], v[32:33], 0 op_sel_hi:[0,1,0] neg_lo:[1,0,0] neg_hi:[1,0,0]
	v_cvt_pk_bf16_f32 v30, v30, v31
	v_cvt_pk_bf16_f32 v31, v32, v33
	ds_write_b64 v186, v[30:31] offset:3264
	ds_read_b32 v30, v187 offset:56
	s_waitcnt lgkmcnt(0)
	v_pk_fma_f32 v[26:27], v[30:31], v[26:27], 0 op_sel_hi:[0,1,0] neg_lo:[1,0,0] neg_hi:[1,0,0]
	v_pk_fma_f32 v[28:29], v[30:31], v[28:29], 0 op_sel_hi:[0,1,0] neg_lo:[1,0,0] neg_hi:[1,0,0]
	v_cvt_pk_bf16_f32 v26, v26, v27
	v_cvt_pk_bf16_f32 v27, v28, v29
	ds_write_b64 v186, v[26:27] offset:3808
	ds_read_b128 a[96:99], v1
	ds_read_b128 a[100:103], v1 offset:64
	ds_read_b128 a[104:107], v1 offset:128
	ds_read_b128 a[108:111], v1 offset:192
	v_lshl_add_u64 v[26:27], v[130:131], 0, s[24:25]
	v_add_co_u32_e32 v28, vcc, s7, v26
	s_nop 1
	v_addc_co_u32_e32 v29, vcc, 0, v27, vcc
	global_load_dwordx4 v[102:105], v[26:27], off nt
	global_load_dwordx4 v[90:93], v[28:29], off nt
	v_add_co_u32_e32 v28, vcc, s36, v26
	s_nop 1
	v_addc_co_u32_e32 v29, vcc, 0, v27, vcc
	v_add_co_u32_e32 v30, vcc, s37, v26
	s_nop 1
	v_addc_co_u32_e32 v31, vcc, 0, v27, vcc
	global_load_dwordx4 v[86:89], v[28:29], off nt
	global_load_dwordx4 v[70:73], v[30:31], off nt
	v_add_co_u32_e32 v28, vcc, s38, v26
	s_nop 1
	v_addc_co_u32_e32 v29, vcc, 0, v27, vcc
	v_add_co_u32_e32 v30, vcc, s39, v26
	s_nop 1
	v_addc_co_u32_e32 v31, vcc, 0, v27, vcc
	global_load_dwordx4 v[66:69], v[28:29], off nt
	global_load_dwordx4 v[46:49], v[30:31], off nt
	v_add_co_u32_e32 v28, vcc, s41, v26
	s_nop 1
	v_addc_co_u32_e32 v29, vcc, 0, v27, vcc
	v_add_co_u32_e32 v26, vcc, s42, v26
	s_nop 1
	v_addc_co_u32_e32 v27, vcc, 0, v27, vcc
	global_load_dwordx4 v[42:45], v[28:29], off nt
	global_load_dwordx4 v[30:33], v[26:27], off nt
	v_mov_b32_e32 v26, v196
	s_waitcnt vmcnt(23)
	s_waitcnt vmcnt(22)
	s_waitcnt vmcnt(21)
	s_waitcnt vmcnt(20)
	s_waitcnt vmcnt(19)
	s_waitcnt vmcnt(18)
	s_waitcnt vmcnt(17)
	s_waitcnt vmcnt(16)
	ds_read_b32 v26, v187 offset:64
	s_waitcnt lgkmcnt(0)
	v_pk_fma_f32 v[28:29], v[26:27], v[110:111], 0 op_sel_hi:[0,1,0] neg_lo:[1,0,0] neg_hi:[1,0,0]
	v_pk_fma_f32 v[26:27], v[26:27], v[112:113], 0 op_sel_hi:[0,1,0] neg_lo:[1,0,0] neg_hi:[1,0,0]
	v_cvt_pk_bf16_f32 v28, v28, v29
	v_cvt_pk_bf16_f32 v29, v26, v27
	ds_write_b64 v186, v[28:29]
	ds_read_b32 v26, v187 offset:72
	s_waitcnt lgkmcnt(0)
	v_pk_fma_f32 v[28:29], v[26:27], v[98:99], 0 op_sel_hi:[0,1,0] neg_lo:[1,0,0] neg_hi:[1,0,0]
	v_pk_fma_f32 v[26:27], v[26:27], v[100:101], 0 op_sel_hi:[0,1,0] neg_lo:[1,0,0] neg_hi:[1,0,0]
	v_cvt_pk_bf16_f32 v28, v28, v29
	v_cvt_pk_bf16_f32 v29, v26, v27
	ds_write_b64 v186, v[28:29] offset:544
	ds_read_b32 v26, v187 offset:80
	s_waitcnt lgkmcnt(0)
	v_pk_fma_f32 v[28:29], v[26:27], v[62:63], 0 op_sel_hi:[0,1,0] neg_lo:[1,0,0] neg_hi:[1,0,0]
	v_pk_fma_f32 v[26:27], v[26:27], v[64:65], 0 op_sel_hi:[0,1,0] neg_lo:[1,0,0] neg_hi:[1,0,0]
	v_cvt_pk_bf16_f32 v28, v28, v29
	v_cvt_pk_bf16_f32 v29, v26, v27
	ds_write_b64 v186, v[28:29] offset:1088
	ds_read_b32 v26, v187 offset:88
	s_waitcnt lgkmcnt(0)
	v_pk_fma_f32 v[28:29], v[26:27], v[50:51], 0 op_sel_hi:[0,1,0] neg_lo:[1,0,0] neg_hi:[1,0,0]
	v_pk_fma_f32 v[26:27], v[26:27], v[52:53], 0 op_sel_hi:[0,1,0] neg_lo:[1,0,0] neg_hi:[1,0,0]
	v_cvt_pk_bf16_f32 v28, v28, v29
	v_cvt_pk_bf16_f32 v29, v26, v27
	ds_write_b64 v186, v[28:29] offset:1632
	ds_read_b32 v26, v187 offset:96
	s_waitcnt lgkmcnt(0)
	v_pk_fma_f32 v[28:29], v[26:27], v[34:35], 0 op_sel_hi:[0,1,0] neg_lo:[1,0,0] neg_hi:[1,0,0]
	v_pk_fma_f32 v[26:27], v[26:27], v[36:37], 0 op_sel_hi:[0,1,0] neg_lo:[1,0,0] neg_hi:[1,0,0]
	v_cvt_pk_bf16_f32 v28, v28, v29
	v_cvt_pk_bf16_f32 v29, v26, v27
	ds_write_b64 v186, v[28:29] offset:2176
	ds_read_b32 v26, v187 offset:104
	s_waitcnt lgkmcnt(0)
	v_pk_fma_f32 v[22:23], v[26:27], v[22:23], 0 op_sel_hi:[0,1,0] neg_lo:[1,0,0] neg_hi:[1,0,0]
	v_pk_fma_f32 v[24:25], v[26:27], v[24:25], 0 op_sel_hi:[0,1,0] neg_lo:[1,0,0] neg_hi:[1,0,0]
	v_cvt_pk_bf16_f32 v22, v22, v23
	v_cvt_pk_bf16_f32 v23, v24, v25
	ds_write_b64 v186, v[22:23] offset:2720
	ds_read_b32 v22, v187 offset:112
	s_waitcnt lgkmcnt(0)
	v_pk_fma_f32 v[14:15], v[22:23], v[14:15], 0 op_sel_hi:[0,1,0] neg_lo:[1,0,0] neg_hi:[1,0,0]
	v_pk_fma_f32 v[16:17], v[22:23], v[16:17], 0 op_sel_hi:[0,1,0] neg_lo:[1,0,0] neg_hi:[1,0,0]
	v_cvt_pk_bf16_f32 v14, v14, v15
	v_cvt_pk_bf16_f32 v15, v16, v17
	ds_write_b64 v186, v[14:15] offset:3264
	ds_read_b32 v14, v187 offset:120
	s_waitcnt lgkmcnt(0)
	v_pk_fma_f32 v[6:7], v[14:15], v[6:7], 0 op_sel_hi:[0,1,0] neg_lo:[1,0,0] neg_hi:[1,0,0]
	v_pk_fma_f32 v[8:9], v[14:15], v[8:9], 0 op_sel_hi:[0,1,0] neg_lo:[1,0,0] neg_hi:[1,0,0]
	v_cvt_pk_bf16_f32 v6, v6, v7
	v_cvt_pk_bf16_f32 v7, v8, v9
	ds_write_b64 v186, v[6:7] offset:3808
	ds_read_b128 a[112:115], v1
	ds_read_b128 a[116:119], v1 offset:64
	ds_read_b128 a[120:123], v1 offset:128
	ds_read_b128 a[124:127], v1 offset:192
	v_lshl_add_u64 v[6:7], v[150:151], 0, s[24:25]
	v_lshl_add_u64 v[8:9], v[152:153], 0, s[24:25]
	v_lshl_add_u64 v[14:15], v[156:157], 0, s[24:25]
	v_lshl_add_u64 v[16:17], v[158:159], 0, s[24:25]
	v_lshl_add_u64 v[22:23], v[160:161], 0, s[24:25]
	v_lshl_add_u64 v[24:25], v[162:163], 0, s[24:25]
	v_lshl_add_u64 v[26:27], v[164:165], 0, s[24:25]
	v_lshl_add_u64 v[28:29], v[166:167], 0, s[24:25]
	global_load_dwordx4 v[110:113], v[6:7], off nt
	global_load_dwordx4 v[98:101], v[8:9], off nt
	global_load_dwordx4 v[78:81], v[14:15], off nt
	global_load_dwordx4 v[58:61], v[16:17], off nt
	global_load_dwordx4 v[34:37], v[22:23], off nt
	s_nop 0
	global_load_dwordx4 v[22:25], v[24:25], off nt
	s_nop 0
	global_load_dwordx4 v[14:17], v[26:27], off nt
	global_load_dwordx4 v[6:9], v[28:29], off nt
	s_waitcnt vmcnt(23)
	s_waitcnt vmcnt(22)
	s_waitcnt vmcnt(21)
	s_waitcnt vmcnt(20)
	s_waitcnt vmcnt(19)
	s_waitcnt vmcnt(18)
	s_waitcnt vmcnt(17)
	s_waitcnt vmcnt(16)
	ds_read_b32 v26, v187 offset:128
	s_waitcnt lgkmcnt(0)
	v_pk_fma_f32 v[28:29], v[26:27], v[106:107], 0 op_sel_hi:[0,1,0] neg_lo:[1,0,0] neg_hi:[1,0,0]
	v_pk_fma_f32 v[26:27], v[26:27], v[108:109], 0 op_sel_hi:[0,1,0] neg_lo:[1,0,0] neg_hi:[1,0,0]
	v_cvt_pk_bf16_f32 v28, v28, v29
	v_cvt_pk_bf16_f32 v29, v26, v27
	ds_write_b64 v186, v[28:29]
	ds_read_b32 v26, v187 offset:136
	s_waitcnt lgkmcnt(0)
	v_pk_fma_f32 v[28:29], v[26:27], v[94:95], 0 op_sel_hi:[0,1,0] neg_lo:[1,0,0] neg_hi:[1,0,0]
	v_pk_fma_f32 v[26:27], v[26:27], v[96:97], 0 op_sel_hi:[0,1,0] neg_lo:[1,0,0] neg_hi:[1,0,0]
	v_cvt_pk_bf16_f32 v28, v28, v29
	v_cvt_pk_bf16_f32 v29, v26, v27
	ds_write_b64 v186, v[28:29] offset:544
	ds_read_b32 v26, v187 offset:144
	s_waitcnt lgkmcnt(0)
	v_pk_fma_f32 v[28:29], v[26:27], v[74:75], 0 op_sel_hi:[0,1,0] neg_lo:[1,0,0] neg_hi:[1,0,0]
	v_pk_fma_f32 v[26:27], v[26:27], v[76:77], 0 op_sel_hi:[0,1,0] neg_lo:[1,0,0] neg_hi:[1,0,0]
	v_cvt_pk_bf16_f32 v28, v28, v29
	v_cvt_pk_bf16_f32 v29, v26, v27
	ds_write_b64 v186, v[28:29] offset:1088
	ds_read_b32 v26, v187 offset:152
	s_waitcnt lgkmcnt(0)
	v_pk_fma_f32 v[28:29], v[26:27], v[54:55], 0 op_sel_hi:[0,1,0] neg_lo:[1,0,0] neg_hi:[1,0,0]
	v_pk_fma_f32 v[26:27], v[26:27], v[56:57], 0 op_sel_hi:[0,1,0] neg_lo:[1,0,0] neg_hi:[1,0,0]
	v_cvt_pk_bf16_f32 v28, v28, v29
	v_cvt_pk_bf16_f32 v29, v26, v27
	ds_write_b64 v186, v[28:29] offset:1632
	ds_read_b32 v26, v187 offset:160
	s_waitcnt lgkmcnt(0)
	v_pk_fma_f32 v[28:29], v[26:27], v[38:39], 0 op_sel_hi:[0,1,0] neg_lo:[1,0,0] neg_hi:[1,0,0]
	v_pk_fma_f32 v[26:27], v[26:27], v[40:41], 0 op_sel_hi:[0,1,0] neg_lo:[1,0,0] neg_hi:[1,0,0]
	v_cvt_pk_bf16_f32 v28, v28, v29
	v_cvt_pk_bf16_f32 v29, v26, v27
	ds_write_b64 v186, v[28:29] offset:2176
	ds_read_b32 v26, v187 offset:168
	s_waitcnt lgkmcnt(0)
	v_pk_fma_f32 v[18:19], v[26:27], v[18:19], 0 op_sel_hi:[0,1,0] neg_lo:[1,0,0] neg_hi:[1,0,0]
	v_pk_fma_f32 v[20:21], v[26:27], v[20:21], 0 op_sel_hi:[0,1,0] neg_lo:[1,0,0] neg_hi:[1,0,0]
	v_cvt_pk_bf16_f32 v18, v18, v19
	v_cvt_pk_bf16_f32 v19, v20, v21
	ds_write_b64 v186, v[18:19] offset:2720
	ds_read_b32 v18, v187 offset:176
	s_waitcnt lgkmcnt(0)
	v_pk_fma_f32 v[10:11], v[18:19], v[10:11], 0 op_sel_hi:[0,1,0] neg_lo:[1,0,0] neg_hi:[1,0,0]
	v_pk_fma_f32 v[12:13], v[18:19], v[12:13], 0 op_sel_hi:[0,1,0] neg_lo:[1,0,0] neg_hi:[1,0,0]
	v_cvt_pk_bf16_f32 v10, v10, v11
	v_cvt_pk_bf16_f32 v11, v12, v13
	ds_write_b64 v186, v[10:11] offset:3264
	ds_read_b32 v10, v187 offset:184
	s_waitcnt lgkmcnt(0)
	v_pk_fma_f32 v[2:3], v[10:11], v[2:3], 0 op_sel_hi:[0,1,0] neg_lo:[1,0,0] neg_hi:[1,0,0]
	v_pk_fma_f32 v[4:5], v[10:11], v[4:5], 0 op_sel_hi:[0,1,0] neg_lo:[1,0,0] neg_hi:[1,0,0]
	v_cvt_pk_bf16_f32 v2, v2, v3
	v_cvt_pk_bf16_f32 v3, v4, v5
	ds_write_b64 v186, v[2:3] offset:3808
	ds_read_b128 a[128:131], v1
	ds_read_b128 a[132:135], v1 offset:64
	ds_read_b128 a[136:139], v1 offset:128
	ds_read_b128 a[140:143], v1 offset:192
	v_lshl_add_u64 v[2:3], v[168:169], 0, s[24:25]
	v_lshl_add_u64 v[4:5], v[170:171], 0, s[24:25]
	v_lshl_add_u64 v[10:11], v[172:173], 0, s[24:25]
	v_lshl_add_u64 v[12:13], v[174:175], 0, s[24:25]
	v_lshl_add_u64 v[18:19], v[176:177], 0, s[24:25]
	v_lshl_add_u64 v[20:21], v[178:179], 0, s[24:25]
	v_lshl_add_u64 v[50:51], v[180:181], 0, s[24:25]
	v_lshl_add_u64 v[52:53], v[182:183], 0, s[24:25]
	global_load_dwordx4 v[114:117], v[2:3], off nt
	global_load_dwordx4 v[94:97], v[4:5], off nt
	global_load_dwordx4 v[82:85], v[10:11], off nt
	global_load_dwordx4 v[62:65], v[12:13], off nt
	global_load_dwordx4 v[38:41], v[18:19], off nt
	global_load_dwordx4 v[26:29], v[20:21], off nt
	s_nop 0
	global_load_dwordx4 v[10:13], v[50:51], off nt
	global_load_dwordx4 v[2:5], v[52:53], off nt
	v_mov_b32_e32 v18, v195
	s_waitcnt vmcnt(23)
	s_waitcnt vmcnt(22)
	s_waitcnt vmcnt(21)
	s_waitcnt vmcnt(20)
	s_waitcnt vmcnt(19)
	s_waitcnt vmcnt(18)
	s_waitcnt vmcnt(17)
	s_waitcnt vmcnt(16)
	ds_read_b32 v18, v187
	s_waitcnt lgkmcnt(0)
	v_pk_fma_f32 v[20:21], v[18:19], v[102:103], 0 op_sel_hi:[0,1,0] neg_lo:[1,0,0] neg_hi:[1,0,0]
	v_pk_fma_f32 v[18:19], v[18:19], v[104:105], 0 op_sel_hi:[0,1,0] neg_lo:[1,0,0] neg_hi:[1,0,0]
	v_cvt_pk_bf16_f32 v20, v20, v21
	v_cvt_pk_bf16_f32 v21, v18, v19
	ds_write_b64 v186, v[20:21]
	ds_read_b32 v18, v187 offset:8
	s_waitcnt lgkmcnt(0)
	v_pk_fma_f32 v[20:21], v[18:19], v[90:91], 0 op_sel_hi:[0,1,0] neg_lo:[1,0,0] neg_hi:[1,0,0]
	v_pk_fma_f32 v[18:19], v[18:19], v[92:93], 0 op_sel_hi:[0,1,0] neg_lo:[1,0,0] neg_hi:[1,0,0]
	v_cvt_pk_bf16_f32 v20, v20, v21
	v_cvt_pk_bf16_f32 v21, v18, v19
	ds_write_b64 v186, v[20:21] offset:544
	ds_read_b32 v18, v187 offset:16
	s_waitcnt lgkmcnt(0)
	v_pk_fma_f32 v[20:21], v[18:19], v[86:87], 0 op_sel_hi:[0,1,0] neg_lo:[1,0,0] neg_hi:[1,0,0]
	v_pk_fma_f32 v[18:19], v[18:19], v[88:89], 0 op_sel_hi:[0,1,0] neg_lo:[1,0,0] neg_hi:[1,0,0]
	v_cvt_pk_bf16_f32 v20, v20, v21
	v_cvt_pk_bf16_f32 v21, v18, v19
	ds_write_b64 v186, v[20:21] offset:1088
	ds_read_b32 v18, v187 offset:24
	s_waitcnt lgkmcnt(0)
	v_pk_fma_f32 v[20:21], v[18:19], v[70:71], 0 op_sel_hi:[0,1,0] neg_lo:[1,0,0] neg_hi:[1,0,0]
	v_pk_fma_f32 v[18:19], v[18:19], v[72:73], 0 op_sel_hi:[0,1,0] neg_lo:[1,0,0] neg_hi:[1,0,0]
	v_cvt_pk_bf16_f32 v20, v20, v21
	v_cvt_pk_bf16_f32 v21, v18, v19
	ds_write_b64 v186, v[20:21] offset:1632
	ds_read_b32 v18, v187 offset:32
	s_waitcnt lgkmcnt(0)
	v_pk_fma_f32 v[20:21], v[18:19], v[66:67], 0 op_sel_hi:[0,1,0] neg_lo:[1,0,0] neg_hi:[1,0,0]
	v_pk_fma_f32 v[18:19], v[18:19], v[68:69], 0 op_sel_hi:[0,1,0] neg_lo:[1,0,0] neg_hi:[1,0,0]
	v_cvt_pk_bf16_f32 v20, v20, v21
	v_cvt_pk_bf16_f32 v21, v18, v19
	ds_write_b64 v186, v[20:21] offset:2176
	ds_read_b32 v18, v187 offset:40
	s_waitcnt lgkmcnt(0)
	v_pk_fma_f32 v[20:21], v[18:19], v[46:47], 0 op_sel_hi:[0,1,0] neg_lo:[1,0,0] neg_hi:[1,0,0]
	v_pk_fma_f32 v[18:19], v[18:19], v[48:49], 0 op_sel_hi:[0,1,0] neg_lo:[1,0,0] neg_hi:[1,0,0]
	v_cvt_pk_bf16_f32 v20, v20, v21
	v_cvt_pk_bf16_f32 v21, v18, v19
	ds_write_b64 v186, v[20:21] offset:2720
	ds_read_b32 v18, v187 offset:48
	s_waitcnt lgkmcnt(0)
	v_pk_fma_f32 v[20:21], v[18:19], v[42:43], 0 op_sel_hi:[0,1,0] neg_lo:[1,0,0] neg_hi:[1,0,0]
	v_pk_fma_f32 v[18:19], v[18:19], v[44:45], 0 op_sel_hi:[0,1,0] neg_lo:[1,0,0] neg_hi:[1,0,0]
	v_cvt_pk_bf16_f32 v20, v20, v21
	v_cvt_pk_bf16_f32 v21, v18, v19
	ds_write_b64 v186, v[20:21] offset:3264
	ds_read_b32 v18, v187 offset:56
	s_waitcnt lgkmcnt(0)
	v_pk_fma_f32 v[20:21], v[18:19], v[30:31], 0 op_sel_hi:[0,1,0] neg_lo:[1,0,0] neg_hi:[1,0,0]
	v_pk_fma_f32 v[18:19], v[18:19], v[32:33], 0 op_sel_hi:[0,1,0] neg_lo:[1,0,0] neg_hi:[1,0,0]
	v_cvt_pk_bf16_f32 v20, v20, v21
	v_cvt_pk_bf16_f32 v21, v18, v19
	ds_write_b64 v186, v[20:21] offset:3808
	ds_read_b128 a[144:147], v1
	ds_read_b128 a[148:151], v1 offset:64
	ds_read_b128 a[152:155], v1 offset:128
	ds_read_b128 a[156:159], v1 offset:192
	v_lshl_add_u64 v[18:19], v[130:131], 0, s[22:23]
	v_add_co_u32_e32 v20, vcc, s7, v18
	s_nop 1
	v_addc_co_u32_e32 v21, vcc, 0, v19, vcc
	global_load_dwordx4 v[106:109], v[18:19], off nt
	global_load_dwordx4 v[90:93], v[20:21], off nt
	v_add_co_u32_e32 v20, vcc, s36, v18
	s_nop 1
	v_addc_co_u32_e32 v21, vcc, 0, v19, vcc
	v_add_co_u32_e32 v30, vcc, s37, v18
	s_nop 1
	v_addc_co_u32_e32 v31, vcc, 0, v19, vcc
	global_load_dwordx4 v[86:89], v[20:21], off nt
	global_load_dwordx4 v[74:77], v[30:31], off nt
	v_add_co_u32_e32 v20, vcc, s38, v18
	s_nop 1
	v_addc_co_u32_e32 v21, vcc, 0, v19, vcc
	v_add_co_u32_e32 v30, vcc, s39, v18
	s_nop 1
	v_addc_co_u32_e32 v31, vcc, 0, v19, vcc
	global_load_dwordx4 v[70:73], v[20:21], off nt
	global_load_dwordx4 v[54:57], v[30:31], off nt
	v_add_co_u32_e32 v20, vcc, s41, v18
	s_nop 1
	v_addc_co_u32_e32 v21, vcc, 0, v19, vcc
	v_add_co_u32_e32 v18, vcc, s42, v18
	s_nop 1
	v_addc_co_u32_e32 v19, vcc, 0, v19, vcc
	global_load_dwordx4 v[50:53], v[20:21], off nt
	global_load_dwordx4 v[46:49], v[18:19], off nt
	v_mov_b32_e32 v18, v195
	s_waitcnt vmcnt(23)
	s_waitcnt vmcnt(22)
	s_waitcnt vmcnt(21)
	s_waitcnt vmcnt(20)
	s_waitcnt vmcnt(19)
	s_waitcnt vmcnt(18)
	s_waitcnt vmcnt(17)
	s_waitcnt vmcnt(16)
	ds_read_b32 v18, v187 offset:64
	s_waitcnt lgkmcnt(0)
	v_pk_fma_f32 v[20:21], v[18:19], v[110:111], 0 op_sel_hi:[0,1,0] neg_lo:[1,0,0] neg_hi:[1,0,0]
	v_pk_fma_f32 v[18:19], v[18:19], v[112:113], 0 op_sel_hi:[0,1,0] neg_lo:[1,0,0] neg_hi:[1,0,0]
	v_cvt_pk_bf16_f32 v20, v20, v21
	v_cvt_pk_bf16_f32 v21, v18, v19
	ds_write_b64 v186, v[20:21]
	ds_read_b32 v18, v187 offset:72
	s_waitcnt lgkmcnt(0)
	v_pk_fma_f32 v[20:21], v[18:19], v[98:99], 0 op_sel_hi:[0,1,0] neg_lo:[1,0,0] neg_hi:[1,0,0]
	v_pk_fma_f32 v[18:19], v[18:19], v[100:101], 0 op_sel_hi:[0,1,0] neg_lo:[1,0,0] neg_hi:[1,0,0]
	v_cvt_pk_bf16_f32 v20, v20, v21
	v_cvt_pk_bf16_f32 v21, v18, v19
	ds_write_b64 v186, v[20:21] offset:544
	ds_read_b32 v18, v187 offset:80
	s_waitcnt lgkmcnt(0)
	v_pk_fma_f32 v[20:21], v[18:19], v[78:79], 0 op_sel_hi:[0,1,0] neg_lo:[1,0,0] neg_hi:[1,0,0]
	v_pk_fma_f32 v[18:19], v[18:19], v[80:81], 0 op_sel_hi:[0,1,0] neg_lo:[1,0,0] neg_hi:[1,0,0]
	v_cvt_pk_bf16_f32 v20, v20, v21
	v_cvt_pk_bf16_f32 v21, v18, v19
	ds_write_b64 v186, v[20:21] offset:1088
	ds_read_b32 v18, v187 offset:88
	s_waitcnt lgkmcnt(0)
	v_pk_fma_f32 v[20:21], v[18:19], v[58:59], 0 op_sel_hi:[0,1,0] neg_lo:[1,0,0] neg_hi:[1,0,0]
	v_pk_fma_f32 v[18:19], v[18:19], v[60:61], 0 op_sel_hi:[0,1,0] neg_lo:[1,0,0] neg_hi:[1,0,0]
	v_cvt_pk_bf16_f32 v20, v20, v21
	v_cvt_pk_bf16_f32 v21, v18, v19
	ds_write_b64 v186, v[20:21] offset:1632
	ds_read_b32 v18, v187 offset:96
	s_waitcnt lgkmcnt(0)
	v_pk_fma_f32 v[20:21], v[18:19], v[34:35], 0 op_sel_hi:[0,1,0] neg_lo:[1,0,0] neg_hi:[1,0,0]
	v_pk_fma_f32 v[18:19], v[18:19], v[36:37], 0 op_sel_hi:[0,1,0] neg_lo:[1,0,0] neg_hi:[1,0,0]
	v_cvt_pk_bf16_f32 v20, v20, v21
	v_cvt_pk_bf16_f32 v21, v18, v19
	ds_write_b64 v186, v[20:21] offset:2176
	ds_read_b32 v18, v187 offset:104
	s_waitcnt lgkmcnt(0)
	v_pk_fma_f32 v[20:21], v[18:19], v[22:23], 0 op_sel_hi:[0,1,0] neg_lo:[1,0,0] neg_hi:[1,0,0]
	v_pk_fma_f32 v[18:19], v[18:19], v[24:25], 0 op_sel_hi:[0,1,0] neg_lo:[1,0,0] neg_hi:[1,0,0]
	v_cvt_pk_bf16_f32 v20, v20, v21
	v_cvt_pk_bf16_f32 v21, v18, v19
	ds_write_b64 v186, v[20:21] offset:2720
	ds_read_b32 v18, v187 offset:112
	s_waitcnt lgkmcnt(0)
	v_pk_fma_f32 v[14:15], v[18:19], v[14:15], 0 op_sel_hi:[0,1,0] neg_lo:[1,0,0] neg_hi:[1,0,0]
	v_pk_fma_f32 v[16:17], v[18:19], v[16:17], 0 op_sel_hi:[0,1,0] neg_lo:[1,0,0] neg_hi:[1,0,0]
	v_cvt_pk_bf16_f32 v14, v14, v15
	v_cvt_pk_bf16_f32 v15, v16, v17
	ds_write_b64 v186, v[14:15] offset:3264
	ds_read_b32 v14, v187 offset:120
	s_waitcnt lgkmcnt(0)
	v_pk_fma_f32 v[6:7], v[14:15], v[6:7], 0 op_sel_hi:[0,1,0] neg_lo:[1,0,0] neg_hi:[1,0,0]
	v_pk_fma_f32 v[8:9], v[14:15], v[8:9], 0 op_sel_hi:[0,1,0] neg_lo:[1,0,0] neg_hi:[1,0,0]
	v_cvt_pk_bf16_f32 v6, v6, v7
	v_cvt_pk_bf16_f32 v7, v8, v9
	ds_write_b64 v186, v[6:7] offset:3808
	ds_read_b128 a[160:163], v1
	ds_read_b128 a[164:167], v1 offset:64
	ds_read_b128 a[168:171], v1 offset:128
	ds_read_b128 a[172:175], v1 offset:192
	v_lshl_add_u64 v[6:7], v[150:151], 0, s[22:23]
	v_lshl_add_u64 v[18:19], v[160:161], 0, s[22:23]
	v_lshl_add_u64 v[20:21], v[162:163], 0, s[22:23]
	v_lshl_add_u64 v[22:23], v[164:165], 0, s[22:23]
	v_lshl_add_u64 v[8:9], v[152:153], 0, s[22:23]
	v_lshl_add_u64 v[14:15], v[156:157], 0, s[22:23]
	v_lshl_add_u64 v[16:17], v[158:159], 0, s[22:23]
	v_lshl_add_u64 v[34:35], v[166:167], 0, s[22:23]
	global_load_dwordx4 v[110:113], v[6:7], off nt
	global_load_dwordx4 v[98:101], v[8:9], off nt
	global_load_dwordx4 v[78:81], v[14:15], off nt
	global_load_dwordx4 v[66:69], v[16:17], off nt
	global_load_dwordx4 v[58:61], v[18:19], off nt
	global_load_dwordx4 v[30:33], v[20:21], off nt
	s_nop 0
	global_load_dwordx4 v[22:25], v[22:23], off nt
	s_nop 0
	global_load_dwordx4 v[18:21], v[34:35], off nt
	s_waitcnt vmcnt(23)
	s_waitcnt vmcnt(22)
	s_waitcnt vmcnt(21)
	s_waitcnt vmcnt(20)
	s_waitcnt vmcnt(19)
	s_waitcnt vmcnt(18)
	s_waitcnt vmcnt(17)
	s_waitcnt vmcnt(16)
	ds_read_b32 v6, v187 offset:128
	s_waitcnt lgkmcnt(0)
	v_pk_fma_f32 v[8:9], v[6:7], v[114:115], 0 op_sel_hi:[0,1,0] neg_lo:[1,0,0] neg_hi:[1,0,0]
	v_pk_fma_f32 v[6:7], v[6:7], v[116:117], 0 op_sel_hi:[0,1,0] neg_lo:[1,0,0] neg_hi:[1,0,0]
	v_cvt_pk_bf16_f32 v8, v8, v9
	v_cvt_pk_bf16_f32 v9, v6, v7
	ds_write_b64 v186, v[8:9]
	ds_read_b32 v6, v187 offset:136
	s_waitcnt lgkmcnt(0)
	v_pk_fma_f32 v[8:9], v[6:7], v[94:95], 0 op_sel_hi:[0,1,0] neg_lo:[1,0,0] neg_hi:[1,0,0]
	v_pk_fma_f32 v[6:7], v[6:7], v[96:97], 0 op_sel_hi:[0,1,0] neg_lo:[1,0,0] neg_hi:[1,0,0]
	v_cvt_pk_bf16_f32 v8, v8, v9
	v_cvt_pk_bf16_f32 v9, v6, v7
	ds_write_b64 v186, v[8:9] offset:544
	ds_read_b32 v6, v187 offset:144
	s_waitcnt lgkmcnt(0)
	v_pk_fma_f32 v[8:9], v[6:7], v[82:83], 0 op_sel_hi:[0,1,0] neg_lo:[1,0,0] neg_hi:[1,0,0]
	v_pk_fma_f32 v[6:7], v[6:7], v[84:85], 0 op_sel_hi:[0,1,0] neg_lo:[1,0,0] neg_hi:[1,0,0]
	v_cvt_pk_bf16_f32 v8, v8, v9
	v_cvt_pk_bf16_f32 v9, v6, v7
	ds_write_b64 v186, v[8:9] offset:1088
	ds_read_b32 v6, v187 offset:152
	s_waitcnt lgkmcnt(0)
	v_pk_fma_f32 v[8:9], v[6:7], v[62:63], 0 op_sel_hi:[0,1,0] neg_lo:[1,0,0] neg_hi:[1,0,0]
	v_pk_fma_f32 v[6:7], v[6:7], v[64:65], 0 op_sel_hi:[0,1,0] neg_lo:[1,0,0] neg_hi:[1,0,0]
	v_cvt_pk_bf16_f32 v8, v8, v9
	v_cvt_pk_bf16_f32 v9, v6, v7
	ds_write_b64 v186, v[8:9] offset:1632
	ds_read_b32 v6, v187 offset:160
	s_waitcnt lgkmcnt(0)
	v_pk_fma_f32 v[8:9], v[6:7], v[38:39], 0 op_sel_hi:[0,1,0] neg_lo:[1,0,0] neg_hi:[1,0,0]
	v_pk_fma_f32 v[6:7], v[6:7], v[40:41], 0 op_sel_hi:[0,1,0] neg_lo:[1,0,0] neg_hi:[1,0,0]
	v_cvt_pk_bf16_f32 v8, v8, v9
	v_cvt_pk_bf16_f32 v9, v6, v7
	ds_write_b64 v186, v[8:9] offset:2176
	ds_read_b32 v6, v187 offset:168
	s_waitcnt lgkmcnt(0)
	v_pk_fma_f32 v[8:9], v[6:7], v[26:27], 0 op_sel_hi:[0,1,0] neg_lo:[1,0,0] neg_hi:[1,0,0]
	v_pk_fma_f32 v[6:7], v[6:7], v[28:29], 0 op_sel_hi:[0,1,0] neg_lo:[1,0,0] neg_hi:[1,0,0]
	v_cvt_pk_bf16_f32 v8, v8, v9
	v_cvt_pk_bf16_f32 v9, v6, v7
	ds_write_b64 v186, v[8:9] offset:2720
	ds_read_b32 v6, v187 offset:176
	s_waitcnt lgkmcnt(0)
	v_pk_fma_f32 v[8:9], v[6:7], v[10:11], 0 op_sel_hi:[0,1,0] neg_lo:[1,0,0] neg_hi:[1,0,0]
	v_pk_fma_f32 v[6:7], v[6:7], v[12:13], 0 op_sel_hi:[0,1,0] neg_lo:[1,0,0] neg_hi:[1,0,0]
	v_cvt_pk_bf16_f32 v8, v8, v9
	v_cvt_pk_bf16_f32 v9, v6, v7
	ds_write_b64 v186, v[8:9] offset:3264
	ds_read_b32 v6, v187 offset:184
	s_waitcnt lgkmcnt(0)
	v_pk_fma_f32 v[2:3], v[6:7], v[2:3], 0 op_sel_hi:[0,1,0] neg_lo:[1,0,0] neg_hi:[1,0,0]
	v_pk_fma_f32 v[4:5], v[6:7], v[4:5], 0 op_sel_hi:[0,1,0] neg_lo:[1,0,0] neg_hi:[1,0,0]
	v_cvt_pk_bf16_f32 v2, v2, v3
	v_cvt_pk_bf16_f32 v3, v4, v5
	ds_write_b64 v186, v[2:3] offset:3808
	ds_read_b128 a[176:179], v1
	ds_read_b128 a[180:183], v1 offset:64
	ds_read_b128 a[184:187], v1 offset:128
	ds_read_b128 a[188:191], v1 offset:192
	v_lshl_add_u64 v[2:3], v[168:169], 0, s[22:23]
	v_lshl_add_u64 v[4:5], v[170:171], 0, s[22:23]
	v_lshl_add_u64 v[6:7], v[172:173], 0, s[22:23]
	v_lshl_add_u64 v[8:9], v[174:175], 0, s[22:23]
	v_lshl_add_u64 v[10:11], v[176:177], 0, s[22:23]
	v_lshl_add_u64 v[12:13], v[178:179], 0, s[22:23]
	v_lshl_add_u64 v[14:15], v[180:181], 0, s[22:23]
	v_lshl_add_u64 v[16:17], v[182:183], 0, s[22:23]
	global_load_dwordx4 v[114:117], v[2:3], off nt
	global_load_dwordx4 v[102:105], v[4:5], off nt
	global_load_dwordx4 v[94:97], v[6:7], off nt
	global_load_dwordx4 v[82:85], v[8:9], off nt
	global_load_dwordx4 v[62:65], v[10:11], off nt
	global_load_dwordx4 v[42:45], v[12:13], off nt
	global_load_dwordx4 v[38:41], v[14:15], off nt
	global_load_dwordx4 v[34:37], v[16:17], off nt
	v_mov_b32_e32 v2, v194
	s_waitcnt vmcnt(23)
	s_waitcnt vmcnt(22)
	s_waitcnt vmcnt(21)
	s_waitcnt vmcnt(20)
	s_waitcnt vmcnt(19)
	s_waitcnt vmcnt(18)
	s_waitcnt vmcnt(17)
	s_waitcnt vmcnt(16)
	ds_read_b32 v2, v187
	s_waitcnt lgkmcnt(0)
	v_pk_fma_f32 v[4:5], v[2:3], v[106:107], 0 op_sel_hi:[0,1,0] neg_lo:[1,0,0] neg_hi:[1,0,0]
	v_pk_fma_f32 v[2:3], v[2:3], v[108:109], 0 op_sel_hi:[0,1,0] neg_lo:[1,0,0] neg_hi:[1,0,0]
	v_cvt_pk_bf16_f32 v4, v4, v5
	v_cvt_pk_bf16_f32 v5, v2, v3
	ds_write_b64 v186, v[4:5]
	ds_read_b32 v2, v187 offset:8
	s_waitcnt lgkmcnt(0)
	v_pk_fma_f32 v[4:5], v[2:3], v[90:91], 0 op_sel_hi:[0,1,0] neg_lo:[1,0,0] neg_hi:[1,0,0]
	v_pk_fma_f32 v[2:3], v[2:3], v[92:93], 0 op_sel_hi:[0,1,0] neg_lo:[1,0,0] neg_hi:[1,0,0]
	v_cvt_pk_bf16_f32 v4, v4, v5
	v_cvt_pk_bf16_f32 v5, v2, v3
	ds_write_b64 v186, v[4:5] offset:544
	ds_read_b32 v2, v187 offset:16
	s_waitcnt lgkmcnt(0)
	v_pk_fma_f32 v[4:5], v[2:3], v[86:87], 0 op_sel_hi:[0,1,0] neg_lo:[1,0,0] neg_hi:[1,0,0]
	v_pk_fma_f32 v[2:3], v[2:3], v[88:89], 0 op_sel_hi:[0,1,0] neg_lo:[1,0,0] neg_hi:[1,0,0]
	v_cvt_pk_bf16_f32 v4, v4, v5
	v_cvt_pk_bf16_f32 v5, v2, v3
	ds_write_b64 v186, v[4:5] offset:1088
	ds_read_b32 v2, v187 offset:24
	s_waitcnt lgkmcnt(0)
	v_pk_fma_f32 v[4:5], v[2:3], v[74:75], 0 op_sel_hi:[0,1,0] neg_lo:[1,0,0] neg_hi:[1,0,0]
	v_pk_fma_f32 v[2:3], v[2:3], v[76:77], 0 op_sel_hi:[0,1,0] neg_lo:[1,0,0] neg_hi:[1,0,0]
	v_cvt_pk_bf16_f32 v4, v4, v5
	v_cvt_pk_bf16_f32 v5, v2, v3
	ds_write_b64 v186, v[4:5] offset:1632
	ds_read_b32 v2, v187 offset:32
	s_waitcnt lgkmcnt(0)
	v_pk_fma_f32 v[4:5], v[2:3], v[70:71], 0 op_sel_hi:[0,1,0] neg_lo:[1,0,0] neg_hi:[1,0,0]
	v_pk_fma_f32 v[2:3], v[2:3], v[72:73], 0 op_sel_hi:[0,1,0] neg_lo:[1,0,0] neg_hi:[1,0,0]
	v_cvt_pk_bf16_f32 v4, v4, v5
	v_cvt_pk_bf16_f32 v5, v2, v3
	ds_write_b64 v186, v[4:5] offset:2176
	ds_read_b32 v2, v187 offset:40
	s_waitcnt lgkmcnt(0)
	v_pk_fma_f32 v[4:5], v[2:3], v[54:55], 0 op_sel_hi:[0,1,0] neg_lo:[1,0,0] neg_hi:[1,0,0]
	v_pk_fma_f32 v[2:3], v[2:3], v[56:57], 0 op_sel_hi:[0,1,0] neg_lo:[1,0,0] neg_hi:[1,0,0]
	v_cvt_pk_bf16_f32 v4, v4, v5
	v_cvt_pk_bf16_f32 v5, v2, v3
	ds_write_b64 v186, v[4:5] offset:2720
	ds_read_b32 v2, v187 offset:48
	s_waitcnt lgkmcnt(0)
	v_pk_fma_f32 v[4:5], v[2:3], v[50:51], 0 op_sel_hi:[0,1,0] neg_lo:[1,0,0] neg_hi:[1,0,0]
	v_pk_fma_f32 v[2:3], v[2:3], v[52:53], 0 op_sel_hi:[0,1,0] neg_lo:[1,0,0] neg_hi:[1,0,0]
	v_cvt_pk_bf16_f32 v4, v4, v5
	v_cvt_pk_bf16_f32 v5, v2, v3
	ds_write_b64 v186, v[4:5] offset:3264
	ds_read_b32 v2, v187 offset:56
	s_waitcnt lgkmcnt(0)
	v_pk_fma_f32 v[4:5], v[2:3], v[46:47], 0 op_sel_hi:[0,1,0] neg_lo:[1,0,0] neg_hi:[1,0,0]
	v_pk_fma_f32 v[2:3], v[2:3], v[48:49], 0 op_sel_hi:[0,1,0] neg_lo:[1,0,0] neg_hi:[1,0,0]
	v_cvt_pk_bf16_f32 v4, v4, v5
	v_cvt_pk_bf16_f32 v5, v2, v3
	ds_write_b64 v186, v[4:5] offset:3808
	ds_read_b128 a[192:195], v1
	ds_read_b128 a[196:199], v1 offset:64
	ds_read_b128 a[200:203], v1 offset:128
	ds_read_b128 a[204:207], v1 offset:192
	v_lshl_add_u64 v[118:119], v[130:131], 0, s[20:21]
	v_add_co_u32_e32 v126, vcc, s7, v118
	s_nop 1
	v_addc_co_u32_e32 v127, vcc, 0, v119, vcc
	v_add_co_u32_e32 v128, vcc, s36, v118
	global_load_dwordx4 v[90:93], v[118:119], off nt
	global_load_dwordx4 v[86:89], v[126:127], off nt
	v_addc_co_u32_e32 v129, vcc, 0, v119, vcc
	v_add_co_u32_e32 v134, vcc, s37, v118
	s_nop 1
	v_addc_co_u32_e32 v135, vcc, 0, v119, vcc
	v_add_co_u32_e32 v136, vcc, s38, v118
	global_load_dwordx4 v[54:57], v[128:129], off nt
	global_load_dwordx4 v[50:53], v[134:135], off nt
	v_addc_co_u32_e32 v137, vcc, 0, v119, vcc
	v_add_co_u32_e32 v138, vcc, s39, v118
	s_nop 1
	v_addc_co_u32_e32 v139, vcc, 0, v119, vcc
	v_add_co_u32_e32 v140, vcc, s41, v118
	global_load_dwordx4 v[14:17], v[136:137], off nt
	global_load_dwordx4 v[10:13], v[138:139], off nt
	v_addc_co_u32_e32 v141, vcc, 0, v119, vcc
	v_add_co_u32_e32 v142, vcc, s42, v118
	s_nop 1
	v_addc_co_u32_e32 v143, vcc, 0, v119, vcc
	global_load_dwordx4 v[6:9], v[140:141], off nt
	global_load_dwordx4 v[2:5], v[142:143], off nt
	v_mov_b32_e32 v26, v194
	s_waitcnt vmcnt(23)
	s_waitcnt vmcnt(22)
	s_waitcnt vmcnt(21)
	s_waitcnt vmcnt(20)
	s_waitcnt vmcnt(19)
	s_waitcnt vmcnt(18)
	s_waitcnt vmcnt(17)
	s_waitcnt vmcnt(16)
	ds_read_b32 v26, v187 offset:64
	s_waitcnt lgkmcnt(0)
	v_pk_fma_f32 v[28:29], v[26:27], v[110:111], 0 op_sel_hi:[0,1,0] neg_lo:[1,0,0] neg_hi:[1,0,0]
	v_pk_fma_f32 v[26:27], v[26:27], v[112:113], 0 op_sel_hi:[0,1,0] neg_lo:[1,0,0] neg_hi:[1,0,0]
	v_cvt_pk_bf16_f32 v28, v28, v29
	v_cvt_pk_bf16_f32 v29, v26, v27
	ds_write_b64 v186, v[28:29]
	ds_read_b32 v26, v187 offset:72
	s_waitcnt lgkmcnt(0)
	v_pk_fma_f32 v[28:29], v[26:27], v[98:99], 0 op_sel_hi:[0,1,0] neg_lo:[1,0,0] neg_hi:[1,0,0]
	v_pk_fma_f32 v[26:27], v[26:27], v[100:101], 0 op_sel_hi:[0,1,0] neg_lo:[1,0,0] neg_hi:[1,0,0]
	v_cvt_pk_bf16_f32 v28, v28, v29
	v_cvt_pk_bf16_f32 v29, v26, v27
	ds_write_b64 v186, v[28:29] offset:544
	ds_read_b32 v26, v187 offset:80
	s_waitcnt lgkmcnt(0)
	v_pk_fma_f32 v[28:29], v[26:27], v[78:79], 0 op_sel_hi:[0,1,0] neg_lo:[1,0,0] neg_hi:[1,0,0]
	v_pk_fma_f32 v[26:27], v[26:27], v[80:81], 0 op_sel_hi:[0,1,0] neg_lo:[1,0,0] neg_hi:[1,0,0]
	v_cvt_pk_bf16_f32 v28, v28, v29
	v_cvt_pk_bf16_f32 v29, v26, v27
	ds_write_b64 v186, v[28:29] offset:1088
	ds_read_b32 v26, v187 offset:88
	s_waitcnt lgkmcnt(0)
	v_pk_fma_f32 v[28:29], v[26:27], v[66:67], 0 op_sel_hi:[0,1,0] neg_lo:[1,0,0] neg_hi:[1,0,0]
	v_pk_fma_f32 v[26:27], v[26:27], v[68:69], 0 op_sel_hi:[0,1,0] neg_lo:[1,0,0] neg_hi:[1,0,0]
	v_cvt_pk_bf16_f32 v28, v28, v29
	v_cvt_pk_bf16_f32 v29, v26, v27
	ds_write_b64 v186, v[28:29] offset:1632
	ds_read_b32 v26, v187 offset:96
	s_waitcnt lgkmcnt(0)
	v_pk_fma_f32 v[28:29], v[26:27], v[58:59], 0 op_sel_hi:[0,1,0] neg_lo:[1,0,0] neg_hi:[1,0,0]
	v_pk_fma_f32 v[26:27], v[26:27], v[60:61], 0 op_sel_hi:[0,1,0] neg_lo:[1,0,0] neg_hi:[1,0,0]
	v_cvt_pk_bf16_f32 v28, v28, v29
	v_cvt_pk_bf16_f32 v29, v26, v27
	ds_write_b64 v186, v[28:29] offset:2176
	ds_read_b32 v26, v187 offset:104
	s_waitcnt lgkmcnt(0)
	v_pk_fma_f32 v[28:29], v[26:27], v[30:31], 0 op_sel_hi:[0,1,0] neg_lo:[1,0,0] neg_hi:[1,0,0]
	v_pk_fma_f32 v[26:27], v[26:27], v[32:33], 0 op_sel_hi:[0,1,0] neg_lo:[1,0,0] neg_hi:[1,0,0]
	v_cvt_pk_bf16_f32 v28, v28, v29
	v_cvt_pk_bf16_f32 v29, v26, v27
	ds_write_b64 v186, v[28:29] offset:2720
	ds_read_b32 v26, v187 offset:112
	s_waitcnt lgkmcnt(0)
	v_pk_fma_f32 v[22:23], v[26:27], v[22:23], 0 op_sel_hi:[0,1,0] neg_lo:[1,0,0] neg_hi:[1,0,0]
	v_pk_fma_f32 v[24:25], v[26:27], v[24:25], 0 op_sel_hi:[0,1,0] neg_lo:[1,0,0] neg_hi:[1,0,0]
	v_cvt_pk_bf16_f32 v22, v22, v23
	v_cvt_pk_bf16_f32 v23, v24, v25
	ds_write_b64 v186, v[22:23] offset:3264
	ds_read_b32 v22, v187 offset:120
	s_waitcnt lgkmcnt(0)
	v_pk_fma_f32 v[18:19], v[22:23], v[18:19], 0 op_sel_hi:[0,1,0] neg_lo:[1,0,0] neg_hi:[1,0,0]
	v_pk_fma_f32 v[20:21], v[22:23], v[20:21], 0 op_sel_hi:[0,1,0] neg_lo:[1,0,0] neg_hi:[1,0,0]
	v_cvt_pk_bf16_f32 v18, v18, v19
	v_cvt_pk_bf16_f32 v19, v20, v21
	ds_write_b64 v186, v[18:19] offset:3808
	ds_read_b128 a[208:211], v1
	ds_read_b128 a[212:215], v1 offset:64
	ds_read_b128 a[216:219], v1 offset:128
	ds_read_b128 a[220:223], v1 offset:192
	v_lshl_add_u64 v[18:19], v[150:151], 0, s[20:21]
	v_lshl_add_u64 v[20:21], v[152:153], 0, s[20:21]
	v_lshl_add_u64 v[22:23], v[156:157], 0, s[20:21]
	v_lshl_add_u64 v[24:25], v[158:159], 0, s[20:21]
	v_lshl_add_u64 v[26:27], v[160:161], 0, s[20:21]
	v_lshl_add_u64 v[28:29], v[162:163], 0, s[20:21]
	v_lshl_add_u64 v[46:47], v[164:165], 0, s[20:21]
	v_lshl_add_u64 v[48:49], v[166:167], 0, s[20:21]
	global_load_dwordx4 v[78:81], v[18:19], off nt
	global_load_dwordx4 v[74:77], v[20:21], off nt
	global_load_dwordx4 v[70:73], v[22:23], off nt
	global_load_dwordx4 v[66:69], v[24:25], off nt
	global_load_dwordx4 v[30:33], v[26:27], off nt
	s_nop 0
	global_load_dwordx4 v[26:29], v[28:29], off nt
	s_nop 0
	global_load_dwordx4 v[22:25], v[46:47], off nt
	global_load_dwordx4 v[18:21], v[48:49], off nt
	s_waitcnt vmcnt(23)
	s_waitcnt vmcnt(22)
	s_waitcnt vmcnt(21)
	s_waitcnt vmcnt(20)
	s_waitcnt vmcnt(19)
	s_waitcnt vmcnt(18)
	s_waitcnt vmcnt(17)
	s_waitcnt vmcnt(16)
	ds_read_b32 v46, v187 offset:128
	s_waitcnt lgkmcnt(0)
	v_pk_fma_f32 v[48:49], v[46:47], v[114:115], 0 op_sel_hi:[0,1,0] neg_lo:[1,0,0] neg_hi:[1,0,0]
	v_pk_fma_f32 v[46:47], v[46:47], v[116:117], 0 op_sel_hi:[0,1,0] neg_lo:[1,0,0] neg_hi:[1,0,0]
	v_cvt_pk_bf16_f32 v48, v48, v49
	v_cvt_pk_bf16_f32 v49, v46, v47
	ds_write_b64 v186, v[48:49]
	ds_read_b32 v46, v187 offset:136
	s_waitcnt lgkmcnt(0)
	v_pk_fma_f32 v[48:49], v[46:47], v[102:103], 0 op_sel_hi:[0,1,0] neg_lo:[1,0,0] neg_hi:[1,0,0]
	v_pk_fma_f32 v[46:47], v[46:47], v[104:105], 0 op_sel_hi:[0,1,0] neg_lo:[1,0,0] neg_hi:[1,0,0]
	v_cvt_pk_bf16_f32 v48, v48, v49
	v_cvt_pk_bf16_f32 v49, v46, v47
	ds_write_b64 v186, v[48:49] offset:544
	ds_read_b32 v46, v187 offset:144
	s_waitcnt lgkmcnt(0)
	v_pk_fma_f32 v[48:49], v[46:47], v[94:95], 0 op_sel_hi:[0,1,0] neg_lo:[1,0,0] neg_hi:[1,0,0]
	v_pk_fma_f32 v[46:47], v[46:47], v[96:97], 0 op_sel_hi:[0,1,0] neg_lo:[1,0,0] neg_hi:[1,0,0]
	v_cvt_pk_bf16_f32 v48, v48, v49
	v_cvt_pk_bf16_f32 v49, v46, v47
	ds_write_b64 v186, v[48:49] offset:1088
	ds_read_b32 v46, v187 offset:152
	s_waitcnt lgkmcnt(0)
	v_pk_fma_f32 v[48:49], v[46:47], v[82:83], 0 op_sel_hi:[0,1,0] neg_lo:[1,0,0] neg_hi:[1,0,0]
	v_pk_fma_f32 v[46:47], v[46:47], v[84:85], 0 op_sel_hi:[0,1,0] neg_lo:[1,0,0] neg_hi:[1,0,0]
	v_cvt_pk_bf16_f32 v48, v48, v49
	v_cvt_pk_bf16_f32 v49, v46, v47
	ds_write_b64 v186, v[48:49] offset:1632
	ds_read_b32 v46, v187 offset:160
	s_waitcnt lgkmcnt(0)
	v_pk_fma_f32 v[48:49], v[46:47], v[62:63], 0 op_sel_hi:[0,1,0] neg_lo:[1,0,0] neg_hi:[1,0,0]
	v_pk_fma_f32 v[46:47], v[46:47], v[64:65], 0 op_sel_hi:[0,1,0] neg_lo:[1,0,0] neg_hi:[1,0,0]
	v_cvt_pk_bf16_f32 v48, v48, v49
	v_cvt_pk_bf16_f32 v49, v46, v47
	ds_write_b64 v186, v[48:49] offset:2176
	ds_read_b32 v46, v187 offset:168
	s_waitcnt lgkmcnt(0)
	v_pk_fma_f32 v[42:43], v[46:47], v[42:43], 0 op_sel_hi:[0,1,0] neg_lo:[1,0,0] neg_hi:[1,0,0]
	v_pk_fma_f32 v[44:45], v[46:47], v[44:45], 0 op_sel_hi:[0,1,0] neg_lo:[1,0,0] neg_hi:[1,0,0]
	v_cvt_pk_bf16_f32 v42, v42, v43
	v_cvt_pk_bf16_f32 v43, v44, v45
	ds_write_b64 v186, v[42:43] offset:2720
	ds_read_b32 v42, v187 offset:176
	s_waitcnt lgkmcnt(0)
	v_pk_fma_f32 v[38:39], v[42:43], v[38:39], 0 op_sel_hi:[0,1,0] neg_lo:[1,0,0] neg_hi:[1,0,0]
	v_pk_fma_f32 v[40:41], v[42:43], v[40:41], 0 op_sel_hi:[0,1,0] neg_lo:[1,0,0] neg_hi:[1,0,0]
	v_cvt_pk_bf16_f32 v38, v38, v39
	v_cvt_pk_bf16_f32 v39, v40, v41
	ds_write_b64 v186, v[38:39] offset:3264
	ds_read_b32 v38, v187 offset:184
	s_waitcnt lgkmcnt(0)
	v_pk_fma_f32 v[34:35], v[38:39], v[34:35], 0 op_sel_hi:[0,1,0] neg_lo:[1,0,0] neg_hi:[1,0,0]
	v_pk_fma_f32 v[36:37], v[38:39], v[36:37], 0 op_sel_hi:[0,1,0] neg_lo:[1,0,0] neg_hi:[1,0,0]
	v_cvt_pk_bf16_f32 v34, v34, v35
	v_cvt_pk_bf16_f32 v35, v36, v37
	ds_write_b64 v186, v[34:35] offset:3808
	ds_read_b128 a[224:227], v1
	ds_read_b128 a[228:231], v1 offset:64
	ds_read_b128 a[232:235], v1 offset:128
	ds_read_b128 a[236:239], v1 offset:192
	v_lshl_add_u64 v[34:35], v[168:169], 0, s[20:21]
	v_lshl_add_u64 v[36:37], v[170:171], 0, s[20:21]
	v_lshl_add_u64 v[38:39], v[172:173], 0, s[20:21]
	v_lshl_add_u64 v[40:41], v[174:175], 0, s[20:21]
	v_lshl_add_u64 v[42:43], v[176:177], 0, s[20:21]
	v_lshl_add_u64 v[44:45], v[178:179], 0, s[20:21]
	v_lshl_add_u64 v[58:59], v[180:181], 0, s[20:21]
	v_lshl_add_u64 v[60:61], v[182:183], 0, s[20:21]
	global_load_dwordx4 v[122:125], v[34:35], off nt
	global_load_dwordx4 v[106:109], v[36:37], off nt
	global_load_dwordx4 v[94:97], v[38:39], off nt
	global_load_dwordx4 v[82:85], v[40:41], off nt
	global_load_dwordx4 v[46:49], v[42:43], off nt
	s_nop 0
	global_load_dwordx4 v[42:45], v[44:45], off nt
	s_nop 0
	global_load_dwordx4 v[38:41], v[58:59], off nt
	global_load_dwordx4 v[34:37], v[60:61], off nt
	v_mov_b32_e32 v98, v133
	s_waitcnt vmcnt(23)
	s_waitcnt vmcnt(22)
	s_waitcnt vmcnt(21)
	s_waitcnt vmcnt(20)
	s_waitcnt vmcnt(19)
	s_waitcnt vmcnt(18)
	s_waitcnt vmcnt(17)
	s_waitcnt vmcnt(16)
	ds_read_b32 v58, v187
	v_add_u32_e32 v99, 1, v98
	v_cmp_eq_u32_e32 vcc, v98, v132
	s_nop 1
	v_cndmask_b32_e64 v60, 0, 1.0, vcc
	v_cmp_eq_u32_e32 vcc, v99, v132
	s_nop 1
	v_cndmask_b32_e64 v61, 0, 1.0, vcc
	s_waitcnt lgkmcnt(0)
	v_pk_fma_f32 v[62:63], v[58:59], v[90:91], v[60:61] op_sel_hi:[0,1,1] neg_lo:[1,0,0] neg_hi:[1,0,0]
	v_add_u32_e32 v90, 3, v98
	v_add_u32_e32 v91, 2, v98
	v_cmp_eq_u32_e32 vcc, v90, v132
	v_cvt_pk_bf16_f32 v62, v62, v63
	s_nop 0
	v_cndmask_b32_e64 v65, 0, 1.0, vcc
	v_cmp_eq_u32_e32 vcc, v91, v132
	s_nop 1
	v_cndmask_b32_e64 v64, 0, 1.0, vcc
	v_pk_fma_f32 v[58:59], v[58:59], v[92:93], v[64:65] op_sel_hi:[0,1,1] neg_lo:[1,0,0] neg_hi:[1,0,0]
	v_cvt_pk_bf16_f32 v63, v58, v59
	ds_write_b64 v186, v[62:63]
	ds_read_b32 v58, v187 offset:8
	v_cmp_eq_u32_e32 vcc, v98, v193
	s_nop 1
	v_cndmask_b32_e64 v62, 0, 1.0, vcc
	v_cmp_eq_u32_e32 vcc, v99, v193
	s_nop 1
	v_cndmask_b32_e64 v63, 0, 1.0, vcc
	v_cmp_eq_u32_e32 vcc, v90, v193
	s_waitcnt lgkmcnt(0)
	v_pk_fma_f32 v[62:63], v[58:59], v[86:87], v[62:63] op_sel_hi:[0,1,1] neg_lo:[1,0,0] neg_hi:[1,0,0]
	v_cvt_pk_bf16_f32 v62, v62, v63
	v_cndmask_b32_e64 v61, 0, 1.0, vcc
	v_pk_fma_f32 v[58:59], v[58:59], v[88:89], v[60:61] op_sel_hi:[0,1,1] neg_lo:[1,0,0] neg_hi:[1,0,0]
	v_cvt_pk_bf16_f32 v63, v58, v59
	ds_write_b64 v186, v[62:63] offset:544
	ds_read_b32 v58, v187 offset:16
	v_cmp_eq_u32_e32 vcc, v98, v192
	s_nop 1
	v_cndmask_b32_e64 v60, 0, 1.0, vcc
	v_cmp_eq_u32_e32 vcc, v99, v192
	s_nop 1
	v_cndmask_b32_e64 v61, 0, 1.0, vcc
	v_cmp_eq_u32_e32 vcc, v90, v192
	s_waitcnt lgkmcnt(0)
	v_pk_fma_f32 v[54:55], v[58:59], v[54:55], v[60:61] op_sel_hi:[0,1,1] neg_lo:[1,0,0] neg_hi:[1,0,0]
	v_cvt_pk_bf16_f32 v54, v54, v55
	v_cndmask_b32_e64 v61, 0, 1.0, vcc
	v_cmp_eq_u32_e32 vcc, v91, v192
	s_nop 1
	v_cndmask_b32_e64 v60, 0, 1.0, vcc
	v_pk_fma_f32 v[56:57], v[58:59], v[56:57], v[60:61] op_sel_hi:[0,1,1] neg_lo:[1,0,0] neg_hi:[1,0,0]
	v_cvt_pk_bf16_f32 v55, v56, v57
	ds_write_b64 v186, v[54:55] offset:1088
	ds_read_b32 v54, v187 offset:24
	v_cmp_eq_u32_e32 vcc, v98, v190
	s_nop 1
	v_cndmask_b32_e64 v56, 0, 1.0, vcc
	v_cmp_eq_u32_e32 vcc, v99, v190
	s_nop 1
	v_cndmask_b32_e64 v57, 0, 1.0, vcc
	v_cmp_eq_u32_e32 vcc, v90, v190
	s_waitcnt lgkmcnt(0)
	v_pk_fma_f32 v[50:51], v[54:55], v[50:51], v[56:57] op_sel_hi:[0,1,1] neg_lo:[1,0,0] neg_hi:[1,0,0]
	v_cvt_pk_bf16_f32 v50, v50, v51
	v_cndmask_b32_e64 v57, 0, 1.0, vcc
	v_cmp_eq_u32_e32 vcc, v91, v190
	s_nop 1
	v_cndmask_b32_e64 v56, 0, 1.0, vcc
	v_pk_fma_f32 v[52:53], v[54:55], v[52:53], v[56:57] op_sel_hi:[0,1,1] neg_lo:[1,0,0] neg_hi:[1,0,0]
	v_cvt_pk_bf16_f32 v51, v52, v53
	ds_write_b64 v186, v[50:51] offset:1632
	ds_read_b32 v50, v187 offset:32
	v_cmp_eq_u32_e32 vcc, v98, v149
	s_nop 1
	v_cndmask_b32_e64 v52, 0, 1.0, vcc
	v_cmp_eq_u32_e32 vcc, v99, v149
	s_nop 1
	v_cndmask_b32_e64 v53, 0, 1.0, vcc
	v_cmp_eq_u32_e32 vcc, v90, v149
	s_waitcnt lgkmcnt(0)
	v_pk_fma_f32 v[14:15], v[50:51], v[14:15], v[52:53] op_sel_hi:[0,1,1] neg_lo:[1,0,0] neg_hi:[1,0,0]
	v_cvt_pk_bf16_f32 v14, v14, v15
	v_cndmask_b32_e64 v53, 0, 1.0, vcc
	v_cmp_eq_u32_e32 vcc, v91, v149
	s_nop 1
	v_cndmask_b32_e64 v52, 0, 1.0, vcc
	v_pk_fma_f32 v[16:17], v[50:51], v[16:17], v[52:53] op_sel_hi:[0,1,1] neg_lo:[1,0,0] neg_hi:[1,0,0]
	v_cvt_pk_bf16_f32 v15, v16, v17
	ds_write_b64 v186, v[14:15] offset:2176
	ds_read_b32 v14, v187 offset:40
	v_cmp_eq_u32_e32 vcc, v98, v148
	s_nop 1
	v_cndmask_b32_e64 v16, 0, 1.0, vcc
	v_cmp_eq_u32_e32 vcc, v99, v148
	s_nop 1
	v_cndmask_b32_e64 v17, 0, 1.0, vcc
	v_cmp_eq_u32_e32 vcc, v90, v148
	s_waitcnt lgkmcnt(0)
	v_pk_fma_f32 v[10:11], v[14:15], v[10:11], v[16:17] op_sel_hi:[0,1,1] neg_lo:[1,0,0] neg_hi:[1,0,0]
	v_cvt_pk_bf16_f32 v10, v10, v11
	v_cndmask_b32_e64 v17, 0, 1.0, vcc
	v_cmp_eq_u32_e32 vcc, v91, v148
	s_nop 1
	v_cndmask_b32_e64 v16, 0, 1.0, vcc
	v_pk_fma_f32 v[12:13], v[14:15], v[12:13], v[16:17] op_sel_hi:[0,1,1] neg_lo:[1,0,0] neg_hi:[1,0,0]
	v_cvt_pk_bf16_f32 v11, v12, v13
	ds_write_b64 v186, v[10:11] offset:2720
	ds_read_b32 v10, v187 offset:48
	v_cmp_eq_u32_e32 vcc, v98, v147
	s_nop 1
	v_cndmask_b32_e64 v12, 0, 1.0, vcc
	v_cmp_eq_u32_e32 vcc, v99, v147
	s_nop 1
	v_cndmask_b32_e64 v13, 0, 1.0, vcc
	v_cmp_eq_u32_e32 vcc, v90, v147
	s_waitcnt lgkmcnt(0)
	v_pk_fma_f32 v[6:7], v[10:11], v[6:7], v[12:13] op_sel_hi:[0,1,1] neg_lo:[1,0,0] neg_hi:[1,0,0]
	v_cvt_pk_bf16_f32 v6, v6, v7
	v_cndmask_b32_e64 v13, 0, 1.0, vcc
	v_cmp_eq_u32_e32 vcc, v91, v147
	s_nop 1
	v_cndmask_b32_e64 v12, 0, 1.0, vcc
	v_pk_fma_f32 v[8:9], v[10:11], v[8:9], v[12:13] op_sel_hi:[0,1,1] neg_lo:[1,0,0] neg_hi:[1,0,0]
	v_cvt_pk_bf16_f32 v7, v8, v9
	ds_write_b64 v186, v[6:7] offset:3264
	ds_read_b32 v6, v187 offset:56
	v_cmp_eq_u32_e32 vcc, v98, v146
	s_nop 1
	v_cndmask_b32_e64 v8, 0, 1.0, vcc
	v_cmp_eq_u32_e32 vcc, v99, v146
	s_nop 1
	v_cndmask_b32_e64 v9, 0, 1.0, vcc
	v_cmp_eq_u32_e32 vcc, v90, v146
	s_waitcnt lgkmcnt(0)
	v_pk_fma_f32 v[2:3], v[6:7], v[2:3], v[8:9] op_sel_hi:[0,1,1] neg_lo:[1,0,0] neg_hi:[1,0,0]
	v_cvt_pk_bf16_f32 v2, v2, v3
	v_cndmask_b32_e64 v9, 0, 1.0, vcc
	v_cmp_eq_u32_e32 vcc, v91, v146
	s_nop 1
	v_cndmask_b32_e64 v8, 0, 1.0, vcc
	v_pk_fma_f32 v[4:5], v[6:7], v[4:5], v[8:9] op_sel_hi:[0,1,1] neg_lo:[1,0,0] neg_hi:[1,0,0]
	v_cvt_pk_bf16_f32 v3, v4, v5
	ds_write_b64 v186, v[2:3] offset:3808
	ds_read_b128 v[2:5], v1
	ds_read_b128 v[6:9], v1 offset:64
	ds_read_b128 v[10:13], v1 offset:128
	ds_read_b128 v[14:17], v1 offset:192
	global_load_dwordx4 v[118:121], v[118:119], off offset:512 nt
	s_nop 0
	global_load_dwordx4 v[110:113], v[126:127], off offset:512 nt
	global_load_dwordx4 v[98:101], v[128:129], off offset:512 nt
	global_load_dwordx4 v[86:89], v[134:135], off offset:512 nt
	global_load_dwordx4 v[62:65], v[136:137], off offset:512 nt
	global_load_dwordx4 v[58:61], v[138:139], off offset:512 nt
	global_load_dwordx4 v[54:57], v[140:141], off offset:512 nt
	global_load_dwordx4 v[50:53], v[142:143], off offset:512 nt
	v_mov_b32_e32 v91, v133
	s_waitcnt vmcnt(23)
	s_waitcnt vmcnt(22)
	s_waitcnt vmcnt(21)
	s_waitcnt vmcnt(20)
	s_waitcnt vmcnt(19)
	s_waitcnt vmcnt(18)
	s_waitcnt vmcnt(17)
	s_waitcnt vmcnt(16)
	ds_read_b32 v90, v187 offset:64
	v_or_b32_e32 v138, 16, v132
	v_add_u32_e32 v102, 1, v91
	v_cmp_eq_u32_e32 vcc, v91, v138
	v_add_u32_e32 v103, 3, v91
	v_add_u32_e32 v104, 2, v91
	v_cndmask_b32_e64 v92, 0, 1.0, vcc
	v_cmp_eq_u32_e32 vcc, v102, v138
	v_or_b32_e32 v139, 18, v132
	v_or_b32_e32 v140, 20, v132
	v_cndmask_b32_e64 v93, 0, 1.0, vcc
	v_cmp_eq_u32_e32 vcc, v103, v138
	s_waitcnt lgkmcnt(0)
	v_pk_fma_f32 v[78:79], v[90:91], v[78:79], v[92:93] op_sel_hi:[0,1,1] neg_lo:[1,0,0] neg_hi:[1,0,0]
	v_cvt_pk_bf16_f32 v78, v78, v79
	v_cndmask_b32_e64 v93, 0, 1.0, vcc
	v_cmp_eq_u32_e32 vcc, v104, v138
	v_or_b32_e32 v141, 22, v132
	v_or_b32_e32 v142, 24, v132
	v_cndmask_b32_e64 v92, 0, 1.0, vcc
	v_pk_fma_f32 v[80:81], v[90:91], v[80:81], v[92:93] op_sel_hi:[0,1,1] neg_lo:[1,0,0] neg_hi:[1,0,0]
	v_cvt_pk_bf16_f32 v79, v80, v81
	ds_write_b64 v186, v[78:79]
	ds_read_b32 v78, v187 offset:72
	v_cmp_eq_u32_e32 vcc, v91, v139
	v_or_b32_e32 v143, 26, v132
	v_or_b32_e32 v144, 28, v132
	v_cndmask_b32_e64 v80, 0, 1.0, vcc
	v_cmp_eq_u32_e32 vcc, v102, v139
	v_or_b32_e32 v145, 30, v132
	s_nop 0
	v_cndmask_b32_e64 v81, 0, 1.0, vcc
	v_cmp_eq_u32_e32 vcc, v103, v139
	s_waitcnt lgkmcnt(0)
	v_pk_fma_f32 v[74:75], v[78:79], v[74:75], v[80:81] op_sel_hi:[0,1,1] neg_lo:[1,0,0] neg_hi:[1,0,0]
	v_cvt_pk_bf16_f32 v74, v74, v75
	v_cndmask_b32_e64 v81, 0, 1.0, vcc
	v_cmp_eq_u32_e32 vcc, v104, v139
	s_nop 1
	v_cndmask_b32_e64 v80, 0, 1.0, vcc
	v_pk_fma_f32 v[76:77], v[78:79], v[76:77], v[80:81] op_sel_hi:[0,1,1] neg_lo:[1,0,0] neg_hi:[1,0,0]
	v_cvt_pk_bf16_f32 v75, v76, v77
	ds_write_b64 v186, v[74:75] offset:544
	ds_read_b32 v74, v187 offset:80
	v_cmp_eq_u32_e32 vcc, v91, v140
	s_nop 1
	v_cndmask_b32_e64 v76, 0, 1.0, vcc
	v_cmp_eq_u32_e32 vcc, v102, v140
	s_nop 1
	v_cndmask_b32_e64 v77, 0, 1.0, vcc
	v_cmp_eq_u32_e32 vcc, v103, v140
	s_waitcnt lgkmcnt(0)
	v_pk_fma_f32 v[70:71], v[74:75], v[70:71], v[76:77] op_sel_hi:[0,1,1] neg_lo:[1,0,0] neg_hi:[1,0,0]
	v_cvt_pk_bf16_f32 v70, v70, v71
	v_cndmask_b32_e64 v77, 0, 1.0, vcc
	v_cmp_eq_u32_e32 vcc, v104, v140
	s_nop 1
	v_cndmask_b32_e64 v76, 0, 1.0, vcc
	v_pk_fma_f32 v[72:73], v[74:75], v[72:73], v[76:77] op_sel_hi:[0,1,1] neg_lo:[1,0,0] neg_hi:[1,0,0]
	v_cvt_pk_bf16_f32 v71, v72, v73
	ds_write_b64 v186, v[70:71] offset:1088
	ds_read_b32 v70, v187 offset:88
	v_cmp_eq_u32_e32 vcc, v91, v141
	s_nop 1
	v_cndmask_b32_e64 v72, 0, 1.0, vcc
	v_cmp_eq_u32_e32 vcc, v102, v141
	s_nop 1
	v_cndmask_b32_e64 v73, 0, 1.0, vcc
	v_cmp_eq_u32_e32 vcc, v103, v141
	s_waitcnt lgkmcnt(0)
	v_pk_fma_f32 v[66:67], v[70:71], v[66:67], v[72:73] op_sel_hi:[0,1,1] neg_lo:[1,0,0] neg_hi:[1,0,0]
	v_cvt_pk_bf16_f32 v66, v66, v67
	v_cndmask_b32_e64 v73, 0, 1.0, vcc
	v_cmp_eq_u32_e32 vcc, v104, v141
	s_nop 1
	v_cndmask_b32_e64 v72, 0, 1.0, vcc
	v_pk_fma_f32 v[68:69], v[70:71], v[68:69], v[72:73] op_sel_hi:[0,1,1] neg_lo:[1,0,0] neg_hi:[1,0,0]
	v_cvt_pk_bf16_f32 v67, v68, v69
	ds_write_b64 v186, v[66:67] offset:1632
	ds_read_b32 v66, v187 offset:96
	v_cmp_eq_u32_e32 vcc, v91, v142
	s_nop 1
	v_cndmask_b32_e64 v68, 0, 1.0, vcc
	v_cmp_eq_u32_e32 vcc, v102, v142
	s_nop 1
	v_cndmask_b32_e64 v69, 0, 1.0, vcc
	v_cmp_eq_u32_e32 vcc, v103, v142
	s_waitcnt lgkmcnt(0)
	v_pk_fma_f32 v[30:31], v[66:67], v[30:31], v[68:69] op_sel_hi:[0,1,1] neg_lo:[1,0,0] neg_hi:[1,0,0]
	v_cvt_pk_bf16_f32 v30, v30, v31
	v_cndmask_b32_e64 v69, 0, 1.0, vcc
	v_cmp_eq_u32_e32 vcc, v104, v142
	s_nop 1
	v_cndmask_b32_e64 v68, 0, 1.0, vcc
	v_pk_fma_f32 v[32:33], v[66:67], v[32:33], v[68:69] op_sel_hi:[0,1,1] neg_lo:[1,0,0] neg_hi:[1,0,0]
	v_cvt_pk_bf16_f32 v31, v32, v33
	ds_write_b64 v186, v[30:31] offset:2176
	ds_read_b32 v30, v187 offset:104
	v_cmp_eq_u32_e32 vcc, v91, v143
	s_nop 1
	v_cndmask_b32_e64 v32, 0, 1.0, vcc
	v_cmp_eq_u32_e32 vcc, v102, v143
	s_nop 1
	v_cndmask_b32_e64 v33, 0, 1.0, vcc
	v_cmp_eq_u32_e32 vcc, v103, v143
	s_waitcnt lgkmcnt(0)
	v_pk_fma_f32 v[26:27], v[30:31], v[26:27], v[32:33] op_sel_hi:[0,1,1] neg_lo:[1,0,0] neg_hi:[1,0,0]
	v_cvt_pk_bf16_f32 v26, v26, v27
	v_cndmask_b32_e64 v33, 0, 1.0, vcc
	v_cmp_eq_u32_e32 vcc, v104, v143
	s_nop 1
	v_cndmask_b32_e64 v32, 0, 1.0, vcc
	v_pk_fma_f32 v[28:29], v[30:31], v[28:29], v[32:33] op_sel_hi:[0,1,1] neg_lo:[1,0,0] neg_hi:[1,0,0]
	v_cvt_pk_bf16_f32 v27, v28, v29
	ds_write_b64 v186, v[26:27] offset:2720
	ds_read_b32 v26, v187 offset:112
	v_cmp_eq_u32_e32 vcc, v91, v144
	s_nop 1
	v_cndmask_b32_e64 v28, 0, 1.0, vcc
	v_cmp_eq_u32_e32 vcc, v102, v144
	s_nop 1
	v_cndmask_b32_e64 v29, 0, 1.0, vcc
	v_cmp_eq_u32_e32 vcc, v103, v144
	s_waitcnt lgkmcnt(0)
	v_pk_fma_f32 v[22:23], v[26:27], v[22:23], v[28:29] op_sel_hi:[0,1,1] neg_lo:[1,0,0] neg_hi:[1,0,0]
	v_cvt_pk_bf16_f32 v22, v22, v23
	v_cndmask_b32_e64 v29, 0, 1.0, vcc
	v_cmp_eq_u32_e32 vcc, v104, v144
	s_nop 1
	v_cndmask_b32_e64 v28, 0, 1.0, vcc
	v_pk_fma_f32 v[24:25], v[26:27], v[24:25], v[28:29] op_sel_hi:[0,1,1] neg_lo:[1,0,0] neg_hi:[1,0,0]
	v_cvt_pk_bf16_f32 v23, v24, v25
	ds_write_b64 v186, v[22:23] offset:3264
	ds_read_b32 v22, v187 offset:120
	v_cmp_eq_u32_e32 vcc, v91, v145
	s_nop 1
	v_cndmask_b32_e64 v24, 0, 1.0, vcc
	v_cmp_eq_u32_e32 vcc, v102, v145
	s_nop 1
	v_cndmask_b32_e64 v25, 0, 1.0, vcc
	v_cmp_eq_u32_e32 vcc, v103, v145
	s_waitcnt lgkmcnt(0)
	v_pk_fma_f32 v[18:19], v[22:23], v[18:19], v[24:25] op_sel_hi:[0,1,1] neg_lo:[1,0,0] neg_hi:[1,0,0]
	v_cvt_pk_bf16_f32 v18, v18, v19
	v_cndmask_b32_e64 v25, 0, 1.0, vcc
	v_cmp_eq_u32_e32 vcc, v104, v145
	s_nop 1
	v_cndmask_b32_e64 v24, 0, 1.0, vcc
	v_pk_fma_f32 v[20:21], v[22:23], v[20:21], v[24:25] op_sel_hi:[0,1,1] neg_lo:[1,0,0] neg_hi:[1,0,0]
	v_cvt_pk_bf16_f32 v19, v20, v21
	ds_write_b64 v186, v[18:19] offset:3808
	ds_read_b128 v[18:21], v1
	ds_read_b128 v[22:25], v1 offset:64
	ds_read_b128 v[26:29], v1 offset:128
	ds_read_b128 v[30:33], v1 offset:192
	v_lshl_add_u64 v[66:67], v[150:151], 0, s[8:9]
	v_lshl_add_u64 v[68:69], v[152:153], 0, s[8:9]
	v_lshl_add_u64 v[70:71], v[156:157], 0, s[8:9]
	v_lshl_add_u64 v[72:73], v[158:159], 0, s[8:9]
	v_lshl_add_u64 v[74:75], v[160:161], 0, s[8:9]
	v_lshl_add_u64 v[76:77], v[162:163], 0, s[8:9]
	v_lshl_add_u64 v[134:135], v[164:165], 0, s[8:9]
	v_lshl_add_u64 v[136:137], v[166:167], 0, s[8:9]
	global_load_dwordx4 v[126:129], v[66:67], off nt
	global_load_dwordx4 v[114:117], v[68:69], off nt
	global_load_dwordx4 v[102:105], v[70:71], off nt
	global_load_dwordx4 v[90:93], v[72:73], off nt
	global_load_dwordx4 v[78:81], v[74:75], off nt
	s_nop 0
	global_load_dwordx4 v[74:77], v[76:77], off nt
	s_nop 0
	global_load_dwordx4 v[70:73], v[134:135], off nt
	global_load_dwordx4 v[66:69], v[136:137], off nt
	s_waitcnt vmcnt(23)
	s_waitcnt vmcnt(22)
	s_waitcnt vmcnt(21)
	s_waitcnt vmcnt(20)
	s_waitcnt vmcnt(19)
	s_waitcnt vmcnt(18)
	s_waitcnt vmcnt(17)
	s_waitcnt vmcnt(16)
	ds_read_b32 v134, v187 offset:128
	v_or_b32_e32 v194, 32, v132
	v_add_u32_e32 v135, 1, v133
	v_cmp_eq_u32_e32 vcc, v133, v194
	v_add_u32_e32 v202, 3, v133
	v_add_u32_e32 v203, 2, v133
	v_cndmask_b32_e64 v136, 0, 1.0, vcc
	v_cmp_eq_u32_e32 vcc, v135, v194
	v_or_b32_e32 v195, 34, v132
	v_or_b32_e32 v196, 36, v132
	v_cndmask_b32_e64 v137, 0, 1.0, vcc
	v_cmp_eq_u32_e32 vcc, v202, v194
	s_waitcnt lgkmcnt(0)
	v_pk_fma_f32 v[122:123], v[134:135], v[122:123], v[136:137] op_sel_hi:[0,1,1] neg_lo:[1,0,0] neg_hi:[1,0,0]
	v_cvt_pk_bf16_f32 v122, v122, v123
	v_cndmask_b32_e64 v137, 0, 1.0, vcc
	v_cmp_eq_u32_e32 vcc, v203, v194
	v_or_b32_e32 v197, 38, v132
	v_or_b32_e32 v198, 40, v132
	v_cndmask_b32_e64 v136, 0, 1.0, vcc
	v_pk_fma_f32 v[124:125], v[134:135], v[124:125], v[136:137] op_sel_hi:[0,1,1] neg_lo:[1,0,0] neg_hi:[1,0,0]
	v_cvt_pk_bf16_f32 v123, v124, v125
	ds_write_b64 v186, v[122:123]
	ds_read_b32 v122, v187 offset:136
	v_cmp_eq_u32_e32 vcc, v133, v195
	v_or_b32_e32 v199, 42, v132
	v_or_b32_e32 v200, 44, v132
	v_cndmask_b32_e64 v124, 0, 1.0, vcc
	v_cmp_eq_u32_e32 vcc, v135, v195
	v_or_b32_e32 v201, 46, v132
	s_nop 0
	v_cndmask_b32_e64 v125, 0, 1.0, vcc
	v_cmp_eq_u32_e32 vcc, v202, v195
	s_waitcnt lgkmcnt(0)
	v_pk_fma_f32 v[106:107], v[122:123], v[106:107], v[124:125] op_sel_hi:[0,1,1] neg_lo:[1,0,0] neg_hi:[1,0,0]
	v_cvt_pk_bf16_f32 v106, v106, v107
	v_cndmask_b32_e64 v125, 0, 1.0, vcc
	v_cmp_eq_u32_e32 vcc, v203, v195
	s_nop 1
	v_cndmask_b32_e64 v124, 0, 1.0, vcc
	v_pk_fma_f32 v[108:109], v[122:123], v[108:109], v[124:125] op_sel_hi:[0,1,1] neg_lo:[1,0,0] neg_hi:[1,0,0]
	v_cvt_pk_bf16_f32 v107, v108, v109
	ds_write_b64 v186, v[106:107] offset:544
	ds_read_b32 v106, v187 offset:144
	v_cmp_eq_u32_e32 vcc, v133, v196
	s_nop 1
	v_cndmask_b32_e64 v108, 0, 1.0, vcc
	v_cmp_eq_u32_e32 vcc, v135, v196
	s_nop 1
	v_cndmask_b32_e64 v109, 0, 1.0, vcc
	v_cmp_eq_u32_e32 vcc, v202, v196
	s_waitcnt lgkmcnt(0)
	v_pk_fma_f32 v[94:95], v[106:107], v[94:95], v[108:109] op_sel_hi:[0,1,1] neg_lo:[1,0,0] neg_hi:[1,0,0]
	v_cvt_pk_bf16_f32 v94, v94, v95
	v_cndmask_b32_e64 v109, 0, 1.0, vcc
	v_cmp_eq_u32_e32 vcc, v203, v196
	s_nop 1
	v_cndmask_b32_e64 v108, 0, 1.0, vcc
	v_pk_fma_f32 v[96:97], v[106:107], v[96:97], v[108:109] op_sel_hi:[0,1,1] neg_lo:[1,0,0] neg_hi:[1,0,0]
	v_cvt_pk_bf16_f32 v95, v96, v97
	ds_write_b64 v186, v[94:95] offset:1088
	ds_read_b32 v94, v187 offset:152
	v_cmp_eq_u32_e32 vcc, v133, v197
	s_nop 1
	v_cndmask_b32_e64 v96, 0, 1.0, vcc
	v_cmp_eq_u32_e32 vcc, v135, v197
	s_nop 1
	v_cndmask_b32_e64 v97, 0, 1.0, vcc
	v_cmp_eq_u32_e32 vcc, v202, v197
	s_waitcnt lgkmcnt(0)
	v_pk_fma_f32 v[82:83], v[94:95], v[82:83], v[96:97] op_sel_hi:[0,1,1] neg_lo:[1,0,0] neg_hi:[1,0,0]
	v_cvt_pk_bf16_f32 v82, v82, v83
	v_cndmask_b32_e64 v97, 0, 1.0, vcc
	v_cmp_eq_u32_e32 vcc, v203, v197
	s_nop 1
	v_cndmask_b32_e64 v96, 0, 1.0, vcc
	v_pk_fma_f32 v[84:85], v[94:95], v[84:85], v[96:97] op_sel_hi:[0,1,1] neg_lo:[1,0,0] neg_hi:[1,0,0]
	v_cvt_pk_bf16_f32 v83, v84, v85
	ds_write_b64 v186, v[82:83] offset:1632
	ds_read_b32 v82, v187 offset:160
	v_cmp_eq_u32_e32 vcc, v133, v198
	s_nop 1
	v_cndmask_b32_e64 v84, 0, 1.0, vcc
	v_cmp_eq_u32_e32 vcc, v135, v198
	s_nop 1
	v_cndmask_b32_e64 v85, 0, 1.0, vcc
	v_cmp_eq_u32_e32 vcc, v202, v198
	s_waitcnt lgkmcnt(0)
	v_pk_fma_f32 v[46:47], v[82:83], v[46:47], v[84:85] op_sel_hi:[0,1,1] neg_lo:[1,0,0] neg_hi:[1,0,0]
	v_cvt_pk_bf16_f32 v46, v46, v47
	v_cndmask_b32_e64 v85, 0, 1.0, vcc
	v_cmp_eq_u32_e32 vcc, v203, v198
	s_nop 1
	v_cndmask_b32_e64 v84, 0, 1.0, vcc
	v_pk_fma_f32 v[48:49], v[82:83], v[48:49], v[84:85] op_sel_hi:[0,1,1] neg_lo:[1,0,0] neg_hi:[1,0,0]
	v_cvt_pk_bf16_f32 v47, v48, v49
	ds_write_b64 v186, v[46:47] offset:2176
	ds_read_b32 v46, v187 offset:168
	v_cmp_eq_u32_e32 vcc, v133, v199
	s_nop 1
	v_cndmask_b32_e64 v48, 0, 1.0, vcc
	v_cmp_eq_u32_e32 vcc, v135, v199
	s_nop 1
	v_cndmask_b32_e64 v49, 0, 1.0, vcc
	v_cmp_eq_u32_e32 vcc, v202, v199
	s_waitcnt lgkmcnt(0)
	v_pk_fma_f32 v[42:43], v[46:47], v[42:43], v[48:49] op_sel_hi:[0,1,1] neg_lo:[1,0,0] neg_hi:[1,0,0]
	v_cvt_pk_bf16_f32 v42, v42, v43
	v_cndmask_b32_e64 v49, 0, 1.0, vcc
	v_cmp_eq_u32_e32 vcc, v203, v199
	s_nop 1
	v_cndmask_b32_e64 v48, 0, 1.0, vcc
	v_pk_fma_f32 v[44:45], v[46:47], v[44:45], v[48:49] op_sel_hi:[0,1,1] neg_lo:[1,0,0] neg_hi:[1,0,0]
	v_cvt_pk_bf16_f32 v43, v44, v45
	ds_write_b64 v186, v[42:43] offset:2720
	ds_read_b32 v42, v187 offset:176
	v_cmp_eq_u32_e32 vcc, v133, v200
	s_nop 1
	v_cndmask_b32_e64 v44, 0, 1.0, vcc
	v_cmp_eq_u32_e32 vcc, v135, v200
	s_nop 1
	v_cndmask_b32_e64 v45, 0, 1.0, vcc
	v_cmp_eq_u32_e32 vcc, v202, v200
	s_waitcnt lgkmcnt(0)
	v_pk_fma_f32 v[38:39], v[42:43], v[38:39], v[44:45] op_sel_hi:[0,1,1] neg_lo:[1,0,0] neg_hi:[1,0,0]
	v_cvt_pk_bf16_f32 v38, v38, v39
	v_cndmask_b32_e64 v45, 0, 1.0, vcc
	v_cmp_eq_u32_e32 vcc, v203, v200
	s_nop 1
	v_cndmask_b32_e64 v44, 0, 1.0, vcc
	v_pk_fma_f32 v[40:41], v[42:43], v[40:41], v[44:45] op_sel_hi:[0,1,1] neg_lo:[1,0,0] neg_hi:[1,0,0]
	v_cvt_pk_bf16_f32 v39, v40, v41
	ds_write_b64 v186, v[38:39] offset:3264
	ds_read_b32 v38, v187 offset:184
	v_cmp_eq_u32_e32 vcc, v133, v201
	s_nop 1
	v_cndmask_b32_e64 v40, 0, 1.0, vcc
	v_cmp_eq_u32_e32 vcc, v135, v201
	s_nop 1
	v_cndmask_b32_e64 v41, 0, 1.0, vcc
	v_cmp_eq_u32_e32 vcc, v202, v201
	s_waitcnt lgkmcnt(0)
	v_pk_fma_f32 v[34:35], v[38:39], v[34:35], v[40:41] op_sel_hi:[0,1,1] neg_lo:[1,0,0] neg_hi:[1,0,0]
	v_cvt_pk_bf16_f32 v34, v34, v35
	v_cndmask_b32_e64 v41, 0, 1.0, vcc
	v_cmp_eq_u32_e32 vcc, v203, v201
	s_nop 1
	v_cndmask_b32_e64 v40, 0, 1.0, vcc
	v_pk_fma_f32 v[36:37], v[38:39], v[36:37], v[40:41] op_sel_hi:[0,1,1] neg_lo:[1,0,0] neg_hi:[1,0,0]
	v_cvt_pk_bf16_f32 v35, v36, v37
	ds_write_b64 v186, v[34:35] offset:3808
	ds_read_b128 v[34:37], v1
	ds_read_b128 v[38:41], v1 offset:64
	ds_read_b128 v[42:45], v1 offset:128
	ds_read_b128 v[46:49], v1 offset:192
	v_mov_b32_e32 v106, v189
	s_waitcnt vmcnt(15)
	s_waitcnt vmcnt(14)
	s_waitcnt vmcnt(13)
	s_waitcnt vmcnt(12)
	s_waitcnt vmcnt(11)
	s_waitcnt vmcnt(10)
	s_waitcnt vmcnt(9)
	s_waitcnt vmcnt(8)
	ds_read_b32 v82, v187
	v_add_u32_e32 v107, 1, v106
	v_cmp_eq_u32_e32 vcc, v106, v132
	v_add_u32_e32 v108, 3, v106
	v_add_u32_e32 v109, 2, v106
	v_cndmask_b32_e64 v84, 0, 1.0, vcc
	v_cmp_eq_u32_e32 vcc, v107, v132
	s_nop 1
	v_cndmask_b32_e64 v85, 0, 1.0, vcc
	v_cmp_eq_u32_e32 vcc, v108, v132
	s_waitcnt lgkmcnt(0)
	v_pk_fma_f32 v[94:95], v[82:83], v[118:119], v[84:85] op_sel_hi:[0,1,1] neg_lo:[1,0,0] neg_hi:[1,0,0]
	v_cvt_pk_bf16_f32 v94, v94, v95
	v_cndmask_b32_e64 v97, 0, 1.0, vcc
	v_cmp_eq_u32_e32 vcc, v109, v132
	s_nop 1
	v_cndmask_b32_e64 v96, 0, 1.0, vcc
	v_pk_fma_f32 v[82:83], v[82:83], v[120:121], v[96:97] op_sel_hi:[0,1,1] neg_lo:[1,0,0] neg_hi:[1,0,0]
	v_cvt_pk_bf16_f32 v95, v82, v83
	ds_write_b64 v186, v[94:95]
	ds_read_b32 v82, v187 offset:8
	v_cmp_eq_u32_e32 vcc, v106, v193
	s_nop 1
	v_cndmask_b32_e64 v94, 0, 1.0, vcc
	v_cmp_eq_u32_e32 vcc, v107, v193
	s_nop 1
	v_cndmask_b32_e64 v95, 0, 1.0, vcc
	v_cmp_eq_u32_e32 vcc, v108, v193
	s_waitcnt lgkmcnt(0)
	v_pk_fma_f32 v[94:95], v[82:83], v[110:111], v[94:95] op_sel_hi:[0,1,1] neg_lo:[1,0,0] neg_hi:[1,0,0]
	v_cvt_pk_bf16_f32 v94, v94, v95
	v_cndmask_b32_e64 v85, 0, 1.0, vcc
	v_pk_fma_f32 v[82:83], v[82:83], v[112:113], v[84:85] op_sel_hi:[0,1,1] neg_lo:[1,0,0] neg_hi:[1,0,0]
	v_cvt_pk_bf16_f32 v95, v82, v83
	ds_write_b64 v186, v[94:95] offset:544
	ds_read_b32 v82, v187 offset:16
	v_cmp_eq_u32_e32 vcc, v106, v192
	s_nop 1
	v_cndmask_b32_e64 v84, 0, 1.0, vcc
	v_cmp_eq_u32_e32 vcc, v107, v192
	s_nop 1
	v_cndmask_b32_e64 v85, 0, 1.0, vcc
	v_cmp_eq_u32_e32 vcc, v108, v192
	s_waitcnt lgkmcnt(0)
	v_pk_fma_f32 v[84:85], v[82:83], v[98:99], v[84:85] op_sel_hi:[0,1,1] neg_lo:[1,0,0] neg_hi:[1,0,0]
	v_cvt_pk_bf16_f32 v84, v84, v85
	v_cndmask_b32_e64 v95, 0, 1.0, vcc
	v_cmp_eq_u32_e32 vcc, v109, v192
	s_nop 1
	v_cndmask_b32_e64 v94, 0, 1.0, vcc
	v_pk_fma_f32 v[82:83], v[82:83], v[100:101], v[94:95] op_sel_hi:[0,1,1] neg_lo:[1,0,0] neg_hi:[1,0,0]
	v_cvt_pk_bf16_f32 v85, v82, v83
	ds_write_b64 v186, v[84:85] offset:1088
	ds_read_b32 v82, v187 offset:24
	v_cmp_eq_u32_e32 vcc, v106, v190
	s_nop 1
	v_cndmask_b32_e64 v84, 0, 1.0, vcc
	v_cmp_eq_u32_e32 vcc, v107, v190
	s_nop 1
	v_cndmask_b32_e64 v85, 0, 1.0, vcc
	v_cmp_eq_u32_e32 vcc, v108, v190
	s_waitcnt lgkmcnt(0)
	v_pk_fma_f32 v[84:85], v[82:83], v[86:87], v[84:85] op_sel_hi:[0,1,1] neg_lo:[1,0,0] neg_hi:[1,0,0]
	v_cvt_pk_bf16_f32 v84, v84, v85
	v_cndmask_b32_e64 v87, 0, 1.0, vcc
	v_cmp_eq_u32_e32 vcc, v109, v190
	s_nop 1
	v_cndmask_b32_e64 v86, 0, 1.0, vcc
	v_pk_fma_f32 v[82:83], v[82:83], v[88:89], v[86:87] op_sel_hi:[0,1,1] neg_lo:[1,0,0] neg_hi:[1,0,0]
	v_cvt_pk_bf16_f32 v85, v82, v83
	ds_write_b64 v186, v[84:85] offset:1632
	ds_read_b32 v82, v187 offset:32
	v_cmp_eq_u32_e32 vcc, v106, v149
	s_nop 1
	v_cndmask_b32_e64 v84, 0, 1.0, vcc
	v_cmp_eq_u32_e32 vcc, v107, v149
	s_nop 1
	v_cndmask_b32_e64 v85, 0, 1.0, vcc
	v_cmp_eq_u32_e32 vcc, v108, v149
	s_waitcnt lgkmcnt(0)
	v_pk_fma_f32 v[62:63], v[82:83], v[62:63], v[84:85] op_sel_hi:[0,1,1] neg_lo:[1,0,0] neg_hi:[1,0,0]
	v_cvt_pk_bf16_f32 v62, v62, v63
	v_cndmask_b32_e64 v85, 0, 1.0, vcc
	v_cmp_eq_u32_e32 vcc, v109, v149
	s_nop 1
	v_cndmask_b32_e64 v84, 0, 1.0, vcc
	v_pk_fma_f32 v[64:65], v[82:83], v[64:65], v[84:85] op_sel_hi:[0,1,1] neg_lo:[1,0,0] neg_hi:[1,0,0]
	v_cvt_pk_bf16_f32 v63, v64, v65
	ds_write_b64 v186, v[62:63] offset:2176
	ds_read_b32 v62, v187 offset:40
	v_cmp_eq_u32_e32 vcc, v106, v148
	s_nop 1
	v_cndmask_b32_e64 v64, 0, 1.0, vcc
	v_cmp_eq_u32_e32 vcc, v107, v148
	s_nop 1
	v_cndmask_b32_e64 v65, 0, 1.0, vcc
	v_cmp_eq_u32_e32 vcc, v108, v148
	s_waitcnt lgkmcnt(0)
	v_pk_fma_f32 v[58:59], v[62:63], v[58:59], v[64:65] op_sel_hi:[0,1,1] neg_lo:[1,0,0] neg_hi:[1,0,0]
	v_cvt_pk_bf16_f32 v58, v58, v59
	v_cndmask_b32_e64 v65, 0, 1.0, vcc
	v_cmp_eq_u32_e32 vcc, v109, v148
	s_nop 1
	v_cndmask_b32_e64 v64, 0, 1.0, vcc
	v_pk_fma_f32 v[60:61], v[62:63], v[60:61], v[64:65] op_sel_hi:[0,1,1] neg_lo:[1,0,0] neg_hi:[1,0,0]
	v_cvt_pk_bf16_f32 v59, v60, v61
	ds_write_b64 v186, v[58:59] offset:2720
	ds_read_b32 v58, v187 offset:48
	v_cmp_eq_u32_e32 vcc, v106, v147
	s_nop 1
	v_cndmask_b32_e64 v60, 0, 1.0, vcc
	v_cmp_eq_u32_e32 vcc, v107, v147
	s_nop 1
	v_cndmask_b32_e64 v61, 0, 1.0, vcc
	v_cmp_eq_u32_e32 vcc, v108, v147
	s_waitcnt lgkmcnt(0)
	v_pk_fma_f32 v[54:55], v[58:59], v[54:55], v[60:61] op_sel_hi:[0,1,1] neg_lo:[1,0,0] neg_hi:[1,0,0]
	v_cvt_pk_bf16_f32 v54, v54, v55
	v_cndmask_b32_e64 v61, 0, 1.0, vcc
	v_cmp_eq_u32_e32 vcc, v109, v147
	s_nop 1
	v_cndmask_b32_e64 v60, 0, 1.0, vcc
	v_pk_fma_f32 v[56:57], v[58:59], v[56:57], v[60:61] op_sel_hi:[0,1,1] neg_lo:[1,0,0] neg_hi:[1,0,0]
	v_cvt_pk_bf16_f32 v55, v56, v57
	ds_write_b64 v186, v[54:55] offset:3264
	ds_read_b32 v54, v187 offset:56
	v_cmp_eq_u32_e32 vcc, v106, v146
	s_nop 1
	v_cndmask_b32_e64 v56, 0, 1.0, vcc
	v_cmp_eq_u32_e32 vcc, v107, v146
	s_nop 1
	v_cndmask_b32_e64 v57, 0, 1.0, vcc
	v_cmp_eq_u32_e32 vcc, v108, v146
	s_waitcnt lgkmcnt(0)
	v_pk_fma_f32 v[50:51], v[54:55], v[50:51], v[56:57] op_sel_hi:[0,1,1] neg_lo:[1,0,0] neg_hi:[1,0,0]
	v_cvt_pk_bf16_f32 v50, v50, v51
	v_cndmask_b32_e64 v57, 0, 1.0, vcc
	v_cmp_eq_u32_e32 vcc, v109, v146
	s_nop 1
	v_cndmask_b32_e64 v56, 0, 1.0, vcc
	v_pk_fma_f32 v[52:53], v[54:55], v[52:53], v[56:57] op_sel_hi:[0,1,1] neg_lo:[1,0,0] neg_hi:[1,0,0]
	v_cvt_pk_bf16_f32 v51, v52, v53
	ds_write_b64 v186, v[50:51] offset:3808
	ds_read_b128 v[50:53], v1
	ds_read_b128 v[54:57], v1 offset:64
	ds_read_b128 v[58:61], v1 offset:128
	ds_read_b128 v[62:65], v1 offset:192
	v_lshl_add_u64 v[82:83], v[168:169], 0, s[8:9]
	v_lshl_add_u64 v[84:85], v[170:171], 0, s[8:9]
	v_lshl_add_u64 v[86:87], v[172:173], 0, s[8:9]
	v_lshl_add_u64 v[88:89], v[174:175], 0, s[8:9]
	v_lshl_add_u64 v[94:95], v[176:177], 0, s[8:9]
	v_lshl_add_u64 v[96:97], v[178:179], 0, s[8:9]
	v_lshl_add_u64 v[122:123], v[180:181], 0, s[8:9]
	v_lshl_add_u64 v[124:125], v[182:183], 0, s[8:9]
	global_load_dwordx4 v[134:137], v[82:83], off nt
	global_load_dwordx4 v[118:121], v[84:85], off nt
	global_load_dwordx4 v[110:113], v[86:87], off nt
	global_load_dwordx4 v[106:109], v[88:89], off nt
	global_load_dwordx4 v[98:101], v[94:95], off nt
	s_nop 0
	global_load_dwordx4 v[94:97], v[96:97], off nt
	s_nop 0
	global_load_dwordx4 v[86:89], v[122:123], off nt
	global_load_dwordx4 v[82:85], v[124:125], off nt
	v_mov_b32_e32 v132, v189
	s_waitcnt vmcnt(15)
	s_waitcnt vmcnt(14)
	s_waitcnt vmcnt(13)
	s_waitcnt vmcnt(12)
	s_waitcnt vmcnt(11)
	s_waitcnt vmcnt(10)
	s_waitcnt vmcnt(9)
	s_waitcnt vmcnt(8)
	ds_read_b32 v122, v187 offset:64
	v_add_u32_e32 v133, 1, v132
	v_cmp_eq_u32_e32 vcc, v132, v138
	v_add_u32_e32 v146, 3, v132
	v_add_u32_e32 v147, 2, v132
	v_cndmask_b32_e64 v124, 0, 1.0, vcc
	v_cmp_eq_u32_e32 vcc, v133, v138
	s_nop 1
	v_cndmask_b32_e64 v125, 0, 1.0, vcc
	v_cmp_eq_u32_e32 vcc, v146, v138
	s_waitcnt lgkmcnt(0)
	v_pk_fma_f32 v[124:125], v[122:123], v[126:127], v[124:125] op_sel_hi:[0,1,1] neg_lo:[1,0,0] neg_hi:[1,0,0]
	v_cvt_pk_bf16_f32 v124, v124, v125
	v_cndmask_b32_e64 v127, 0, 1.0, vcc
	v_cmp_eq_u32_e32 vcc, v147, v138
	s_nop 1
	v_cndmask_b32_e64 v126, 0, 1.0, vcc
	v_pk_fma_f32 v[122:123], v[122:123], v[128:129], v[126:127] op_sel_hi:[0,1,1] neg_lo:[1,0,0] neg_hi:[1,0,0]
	v_cvt_pk_bf16_f32 v125, v122, v123
	ds_write_b64 v186, v[124:125]
	ds_read_b32 v122, v187 offset:72
	v_cmp_eq_u32_e32 vcc, v132, v139
	s_nop 1
	v_cndmask_b32_e64 v124, 0, 1.0, vcc
	v_cmp_eq_u32_e32 vcc, v133, v139
	s_nop 1
	v_cndmask_b32_e64 v125, 0, 1.0, vcc
	v_cmp_eq_u32_e32 vcc, v146, v139
	s_waitcnt lgkmcnt(0)
	v_pk_fma_f32 v[114:115], v[122:123], v[114:115], v[124:125] op_sel_hi:[0,1,1] neg_lo:[1,0,0] neg_hi:[1,0,0]
	v_cvt_pk_bf16_f32 v114, v114, v115
	v_cndmask_b32_e64 v125, 0, 1.0, vcc
	v_cmp_eq_u32_e32 vcc, v147, v139
	s_nop 1
	v_cndmask_b32_e64 v124, 0, 1.0, vcc
	v_pk_fma_f32 v[116:117], v[122:123], v[116:117], v[124:125] op_sel_hi:[0,1,1] neg_lo:[1,0,0] neg_hi:[1,0,0]
	v_cvt_pk_bf16_f32 v115, v116, v117
	ds_write_b64 v186, v[114:115] offset:544
	ds_read_b32 v114, v187 offset:80
	v_cmp_eq_u32_e32 vcc, v132, v140
	s_nop 1
	v_cndmask_b32_e64 v116, 0, 1.0, vcc
	v_cmp_eq_u32_e32 vcc, v133, v140
	s_nop 1
	v_cndmask_b32_e64 v117, 0, 1.0, vcc
	v_cmp_eq_u32_e32 vcc, v146, v140
	s_waitcnt lgkmcnt(0)
	v_pk_fma_f32 v[102:103], v[114:115], v[102:103], v[116:117] op_sel_hi:[0,1,1] neg_lo:[1,0,0] neg_hi:[1,0,0]
	v_cvt_pk_bf16_f32 v102, v102, v103
	v_cndmask_b32_e64 v117, 0, 1.0, vcc
	v_cmp_eq_u32_e32 vcc, v147, v140
	s_nop 1
	v_cndmask_b32_e64 v116, 0, 1.0, vcc
	v_pk_fma_f32 v[104:105], v[114:115], v[104:105], v[116:117] op_sel_hi:[0,1,1] neg_lo:[1,0,0] neg_hi:[1,0,0]
	v_cvt_pk_bf16_f32 v103, v104, v105
	ds_write_b64 v186, v[102:103] offset:1088
	ds_read_b32 v102, v187 offset:88
	v_cmp_eq_u32_e32 vcc, v132, v141
	s_nop 1
	v_cndmask_b32_e64 v104, 0, 1.0, vcc
	v_cmp_eq_u32_e32 vcc, v133, v141
	s_nop 1
	v_cndmask_b32_e64 v105, 0, 1.0, vcc
	v_cmp_eq_u32_e32 vcc, v146, v141
	s_waitcnt lgkmcnt(0)
	v_pk_fma_f32 v[90:91], v[102:103], v[90:91], v[104:105] op_sel_hi:[0,1,1] neg_lo:[1,0,0] neg_hi:[1,0,0]
	v_cvt_pk_bf16_f32 v90, v90, v91
	v_cndmask_b32_e64 v105, 0, 1.0, vcc
	v_cmp_eq_u32_e32 vcc, v147, v141
	s_nop 1
	v_cndmask_b32_e64 v104, 0, 1.0, vcc
	v_pk_fma_f32 v[92:93], v[102:103], v[92:93], v[104:105] op_sel_hi:[0,1,1] neg_lo:[1,0,0] neg_hi:[1,0,0]
	v_cvt_pk_bf16_f32 v91, v92, v93
	ds_write_b64 v186, v[90:91] offset:1632
	ds_read_b32 v90, v187 offset:96
	v_cmp_eq_u32_e32 vcc, v132, v142
	s_nop 1
	v_cndmask_b32_e64 v92, 0, 1.0, vcc
	v_cmp_eq_u32_e32 vcc, v133, v142
	s_nop 1
	v_cndmask_b32_e64 v93, 0, 1.0, vcc
	v_cmp_eq_u32_e32 vcc, v146, v142
	s_waitcnt lgkmcnt(0)
	v_pk_fma_f32 v[78:79], v[90:91], v[78:79], v[92:93] op_sel_hi:[0,1,1] neg_lo:[1,0,0] neg_hi:[1,0,0]
	v_cvt_pk_bf16_f32 v78, v78, v79
	v_cndmask_b32_e64 v93, 0, 1.0, vcc
	v_cmp_eq_u32_e32 vcc, v147, v142
	s_nop 1
	v_cndmask_b32_e64 v92, 0, 1.0, vcc
	v_pk_fma_f32 v[80:81], v[90:91], v[80:81], v[92:93] op_sel_hi:[0,1,1] neg_lo:[1,0,0] neg_hi:[1,0,0]
	v_cvt_pk_bf16_f32 v79, v80, v81
	ds_write_b64 v186, v[78:79] offset:2176
	ds_read_b32 v78, v187 offset:104
	v_cmp_eq_u32_e32 vcc, v132, v143
	s_nop 1
	v_cndmask_b32_e64 v80, 0, 1.0, vcc
	v_cmp_eq_u32_e32 vcc, v133, v143
	s_nop 1
	v_cndmask_b32_e64 v81, 0, 1.0, vcc
	v_cmp_eq_u32_e32 vcc, v146, v143
	s_waitcnt lgkmcnt(0)
	v_pk_fma_f32 v[74:75], v[78:79], v[74:75], v[80:81] op_sel_hi:[0,1,1] neg_lo:[1,0,0] neg_hi:[1,0,0]
	v_cvt_pk_bf16_f32 v74, v74, v75
	v_cndmask_b32_e64 v81, 0, 1.0, vcc
	v_cmp_eq_u32_e32 vcc, v147, v143
	s_nop 1
	v_cndmask_b32_e64 v80, 0, 1.0, vcc
	v_pk_fma_f32 v[76:77], v[78:79], v[76:77], v[80:81] op_sel_hi:[0,1,1] neg_lo:[1,0,0] neg_hi:[1,0,0]
	v_cvt_pk_bf16_f32 v75, v76, v77
	ds_write_b64 v186, v[74:75] offset:2720
	ds_read_b32 v74, v187 offset:112
	v_cmp_eq_u32_e32 vcc, v132, v144
	s_nop 1
	v_cndmask_b32_e64 v76, 0, 1.0, vcc
	v_cmp_eq_u32_e32 vcc, v133, v144
	s_nop 1
	v_cndmask_b32_e64 v77, 0, 1.0, vcc
	v_cmp_eq_u32_e32 vcc, v146, v144
	s_waitcnt lgkmcnt(0)
	v_pk_fma_f32 v[70:71], v[74:75], v[70:71], v[76:77] op_sel_hi:[0,1,1] neg_lo:[1,0,0] neg_hi:[1,0,0]
	v_cvt_pk_bf16_f32 v70, v70, v71
	v_cndmask_b32_e64 v77, 0, 1.0, vcc
	v_cmp_eq_u32_e32 vcc, v147, v144
	s_nop 1
	v_cndmask_b32_e64 v76, 0, 1.0, vcc
	v_pk_fma_f32 v[72:73], v[74:75], v[72:73], v[76:77] op_sel_hi:[0,1,1] neg_lo:[1,0,0] neg_hi:[1,0,0]
	v_cvt_pk_bf16_f32 v71, v72, v73
	ds_write_b64 v186, v[70:71] offset:3264
	ds_read_b32 v70, v187 offset:120
	v_cmp_eq_u32_e32 vcc, v132, v145
	s_nop 1
	v_cndmask_b32_e64 v72, 0, 1.0, vcc
	v_cmp_eq_u32_e32 vcc, v133, v145
	s_nop 1
	v_cndmask_b32_e64 v73, 0, 1.0, vcc
	v_cmp_eq_u32_e32 vcc, v146, v145
	s_waitcnt lgkmcnt(0)
	v_pk_fma_f32 v[66:67], v[70:71], v[66:67], v[72:73] op_sel_hi:[0,1,1] neg_lo:[1,0,0] neg_hi:[1,0,0]
	v_cvt_pk_bf16_f32 v66, v66, v67
	v_cndmask_b32_e64 v73, 0, 1.0, vcc
	v_cmp_eq_u32_e32 vcc, v147, v145
	s_nop 1
	v_cndmask_b32_e64 v72, 0, 1.0, vcc
	v_pk_fma_f32 v[68:69], v[70:71], v[68:69], v[72:73] op_sel_hi:[0,1,1] neg_lo:[1,0,0] neg_hi:[1,0,0]
	v_cvt_pk_bf16_f32 v67, v68, v69
	ds_write_b64 v186, v[66:67] offset:3808
	ds_read_b128 v[66:69], v1
	ds_read_b128 v[70:73], v1 offset:64
	ds_read_b128 v[74:77], v1 offset:128
	ds_read_b128 v[78:81], v1 offset:192
	v_lshl_add_u64 v[90:91], v[130:131], 0, s[0:1]
	v_add_co_u32_e32 v92, vcc, s7, v90
	s_nop 1
	v_addc_co_u32_e32 v93, vcc, 0, v91, vcc
	global_load_dwordx4 v[146:149], v[90:91], off nt
	global_load_dwordx4 v[142:145], v[92:93], off nt
	v_add_co_u32_e32 v92, vcc, s36, v90
	s_nop 1
	v_addc_co_u32_e32 v93, vcc, 0, v91, vcc
	v_add_co_u32_e32 v102, vcc, s37, v90
	s_nop 1
	v_addc_co_u32_e32 v103, vcc, 0, v91, vcc
	global_load_dwordx4 v[138:141], v[92:93], off nt
	global_load_dwordx4 v[130:133], v[102:103], off nt
	v_add_co_u32_e32 v92, vcc, s38, v90
	s_nop 1
	v_addc_co_u32_e32 v93, vcc, 0, v91, vcc
	v_add_co_u32_e32 v102, vcc, s39, v90
	s_nop 1
	v_addc_co_u32_e32 v103, vcc, 0, v91, vcc
	global_load_dwordx4 v[126:129], v[92:93], off nt
	global_load_dwordx4 v[122:125], v[102:103], off nt
	v_add_co_u32_e32 v92, vcc, s41, v90
	s_nop 1
	v_addc_co_u32_e32 v93, vcc, 0, v91, vcc
	v_add_co_u32_e32 v90, vcc, s42, v90
	s_nop 1
	v_addc_co_u32_e32 v91, vcc, 0, v91, vcc
	global_load_dwordx4 v[114:117], v[92:93], off nt
	global_load_dwordx4 v[102:105], v[90:91], off nt
	s_waitcnt vmcnt(15)
	s_waitcnt vmcnt(14)
	s_waitcnt vmcnt(13)
	s_waitcnt vmcnt(12)
	s_waitcnt vmcnt(11)
	s_waitcnt vmcnt(10)
	s_waitcnt vmcnt(9)
	s_waitcnt vmcnt(8)
	ds_read_b32 v90, v187 offset:128
	v_add_u32_e32 v190, 1, v189
	v_cmp_eq_u32_e32 vcc, v189, v194
	v_add_u32_e32 v192, 3, v189
	v_add_u32_e32 v193, 2, v189
	v_cndmask_b32_e64 v92, 0, 1.0, vcc
	v_cmp_eq_u32_e32 vcc, v190, v194
	s_nop 1
	v_cndmask_b32_e64 v93, 0, 1.0, vcc
	v_cmp_eq_u32_e32 vcc, v192, v194
	s_waitcnt lgkmcnt(0)
	v_pk_fma_f32 v[92:93], v[90:91], v[134:135], v[92:93] op_sel_hi:[0,1,1] neg_lo:[1,0,0] neg_hi:[1,0,0]
	v_cvt_pk_bf16_f32 v92, v92, v93
	v_cndmask_b32_e64 v135, 0, 1.0, vcc
	v_cmp_eq_u32_e32 vcc, v193, v194
	s_nop 1
	v_cndmask_b32_e64 v134, 0, 1.0, vcc
	v_pk_fma_f32 v[90:91], v[90:91], v[136:137], v[134:135] op_sel_hi:[0,1,1] neg_lo:[1,0,0] neg_hi:[1,0,0]
	v_cvt_pk_bf16_f32 v93, v90, v91
	ds_write_b64 v186, v[92:93]
	ds_read_b32 v90, v187 offset:136
	v_cmp_eq_u32_e32 vcc, v189, v195
	s_nop 1
	v_cndmask_b32_e64 v92, 0, 1.0, vcc
	v_cmp_eq_u32_e32 vcc, v190, v195
	s_nop 1
	v_cndmask_b32_e64 v93, 0, 1.0, vcc
	v_cmp_eq_u32_e32 vcc, v192, v195
	s_waitcnt lgkmcnt(0)
	v_pk_fma_f32 v[92:93], v[90:91], v[118:119], v[92:93] op_sel_hi:[0,1,1] neg_lo:[1,0,0] neg_hi:[1,0,0]
	v_cvt_pk_bf16_f32 v92, v92, v93
	v_cndmask_b32_e64 v119, 0, 1.0, vcc
	v_cmp_eq_u32_e32 vcc, v193, v195
	s_nop 1
	v_cndmask_b32_e64 v118, 0, 1.0, vcc
	v_pk_fma_f32 v[90:91], v[90:91], v[120:121], v[118:119] op_sel_hi:[0,1,1] neg_lo:[1,0,0] neg_hi:[1,0,0]
	v_cvt_pk_bf16_f32 v93, v90, v91
	ds_write_b64 v186, v[92:93] offset:544
	ds_read_b32 v90, v187 offset:144
	v_cmp_eq_u32_e32 vcc, v189, v196
	s_nop 1
	v_cndmask_b32_e64 v92, 0, 1.0, vcc
	v_cmp_eq_u32_e32 vcc, v190, v196
	s_nop 1
	v_cndmask_b32_e64 v93, 0, 1.0, vcc
	v_cmp_eq_u32_e32 vcc, v192, v196
	s_waitcnt lgkmcnt(0)
	v_pk_fma_f32 v[92:93], v[90:91], v[110:111], v[92:93] op_sel_hi:[0,1,1] neg_lo:[1,0,0] neg_hi:[1,0,0]
	v_cvt_pk_bf16_f32 v92, v92, v93
	v_cndmask_b32_e64 v111, 0, 1.0, vcc
	v_cmp_eq_u32_e32 vcc, v193, v196
	s_nop 1
	v_cndmask_b32_e64 v110, 0, 1.0, vcc
	v_pk_fma_f32 v[90:91], v[90:91], v[112:113], v[110:111] op_sel_hi:[0,1,1] neg_lo:[1,0,0] neg_hi:[1,0,0]
	v_cvt_pk_bf16_f32 v93, v90, v91
	ds_write_b64 v186, v[92:93] offset:1088
	ds_read_b32 v90, v187 offset:152
	v_cmp_eq_u32_e32 vcc, v189, v197
	s_nop 1
	v_cndmask_b32_e64 v92, 0, 1.0, vcc
	v_cmp_eq_u32_e32 vcc, v190, v197
	s_nop 1
	v_cndmask_b32_e64 v93, 0, 1.0, vcc
	v_cmp_eq_u32_e32 vcc, v192, v197
	s_waitcnt lgkmcnt(0)
	v_pk_fma_f32 v[92:93], v[90:91], v[106:107], v[92:93] op_sel_hi:[0,1,1] neg_lo:[1,0,0] neg_hi:[1,0,0]
	v_cvt_pk_bf16_f32 v92, v92, v93
	v_cndmask_b32_e64 v107, 0, 1.0, vcc
	v_cmp_eq_u32_e32 vcc, v193, v197
	s_nop 1
	v_cndmask_b32_e64 v106, 0, 1.0, vcc
	v_pk_fma_f32 v[90:91], v[90:91], v[108:109], v[106:107] op_sel_hi:[0,1,1] neg_lo:[1,0,0] neg_hi:[1,0,0]
	v_cvt_pk_bf16_f32 v93, v90, v91
	ds_write_b64 v186, v[92:93] offset:1632
	ds_read_b32 v90, v187 offset:160
	v_cmp_eq_u32_e32 vcc, v189, v198
	s_nop 1
	v_cndmask_b32_e64 v92, 0, 1.0, vcc
	v_cmp_eq_u32_e32 vcc, v190, v198
	s_nop 1
	v_cndmask_b32_e64 v93, 0, 1.0, vcc
	v_cmp_eq_u32_e32 vcc, v192, v198
	s_waitcnt lgkmcnt(0)
	v_pk_fma_f32 v[92:93], v[90:91], v[98:99], v[92:93] op_sel_hi:[0,1,1] neg_lo:[1,0,0] neg_hi:[1,0,0]
	v_cvt_pk_bf16_f32 v92, v92, v93
	v_cndmask_b32_e64 v99, 0, 1.0, vcc
	v_cmp_eq_u32_e32 vcc, v193, v198
	s_nop 1
	v_cndmask_b32_e64 v98, 0, 1.0, vcc
	v_pk_fma_f32 v[90:91], v[90:91], v[100:101], v[98:99] op_sel_hi:[0,1,1] neg_lo:[1,0,0] neg_hi:[1,0,0]
	v_cvt_pk_bf16_f32 v93, v90, v91
	ds_write_b64 v186, v[92:93] offset:2176
	ds_read_b32 v90, v187 offset:168
	v_cmp_eq_u32_e32 vcc, v189, v199
	s_nop 1
	v_cndmask_b32_e64 v92, 0, 1.0, vcc
	v_cmp_eq_u32_e32 vcc, v190, v199
	s_nop 1
	v_cndmask_b32_e64 v93, 0, 1.0, vcc
	v_cmp_eq_u32_e32 vcc, v192, v199
	s_waitcnt lgkmcnt(0)
	v_pk_fma_f32 v[92:93], v[90:91], v[94:95], v[92:93] op_sel_hi:[0,1,1] neg_lo:[1,0,0] neg_hi:[1,0,0]
	v_cvt_pk_bf16_f32 v92, v92, v93
	v_cndmask_b32_e64 v95, 0, 1.0, vcc
	v_cmp_eq_u32_e32 vcc, v193, v199
	s_nop 1
	v_cndmask_b32_e64 v94, 0, 1.0, vcc
	v_pk_fma_f32 v[90:91], v[90:91], v[96:97], v[94:95] op_sel_hi:[0,1,1] neg_lo:[1,0,0] neg_hi:[1,0,0]
	v_cvt_pk_bf16_f32 v93, v90, v91
	ds_write_b64 v186, v[92:93] offset:2720
	ds_read_b32 v90, v187 offset:176
	v_cmp_eq_u32_e32 vcc, v189, v200
	s_nop 1
	v_cndmask_b32_e64 v92, 0, 1.0, vcc
	v_cmp_eq_u32_e32 vcc, v190, v200
	s_nop 1
	v_cndmask_b32_e64 v93, 0, 1.0, vcc
	v_cmp_eq_u32_e32 vcc, v192, v200
	s_waitcnt lgkmcnt(0)
	v_pk_fma_f32 v[86:87], v[90:91], v[86:87], v[92:93] op_sel_hi:[0,1,1] neg_lo:[1,0,0] neg_hi:[1,0,0]
	v_cvt_pk_bf16_f32 v86, v86, v87
	v_cndmask_b32_e64 v93, 0, 1.0, vcc
	v_cmp_eq_u32_e32 vcc, v193, v200
	s_nop 1
	v_cndmask_b32_e64 v92, 0, 1.0, vcc
	v_pk_fma_f32 v[88:89], v[90:91], v[88:89], v[92:93] op_sel_hi:[0,1,1] neg_lo:[1,0,0] neg_hi:[1,0,0]
	v_cvt_pk_bf16_f32 v87, v88, v89
	ds_write_b64 v186, v[86:87] offset:3264
	ds_read_b32 v86, v187 offset:184
	v_cmp_eq_u32_e32 vcc, v189, v201
	s_nop 1
	v_cndmask_b32_e64 v88, 0, 1.0, vcc
	v_cmp_eq_u32_e32 vcc, v190, v201
	s_nop 1
	v_cndmask_b32_e64 v89, 0, 1.0, vcc
	v_cmp_eq_u32_e32 vcc, v192, v201
	s_waitcnt lgkmcnt(0)
	v_pk_fma_f32 v[82:83], v[86:87], v[82:83], v[88:89] op_sel_hi:[0,1,1] neg_lo:[1,0,0] neg_hi:[1,0,0]
	v_cvt_pk_bf16_f32 v82, v82, v83
	v_cndmask_b32_e64 v89, 0, 1.0, vcc
	v_cmp_eq_u32_e32 vcc, v193, v201
	s_nop 1
	v_cndmask_b32_e64 v88, 0, 1.0, vcc
	v_pk_fma_f32 v[84:85], v[86:87], v[84:85], v[88:89] op_sel_hi:[0,1,1] neg_lo:[1,0,0] neg_hi:[1,0,0]
	v_cvt_pk_bf16_f32 v83, v84, v85
	ds_write_b64 v186, v[82:83] offset:3808
	ds_read_b128 v[82:85], v1
	ds_read_b128 v[86:89], v1 offset:64
	ds_read_b128 v[90:93], v1 offset:128
	ds_read_b128 v[94:97], v1 offset:192
	v_lshl_add_u64 v[98:99], v[150:151], 0, s[0:1]
	v_lshl_add_u64 v[192:193], v[164:165], 0, s[0:1]
	v_lshl_add_u64 v[196:197], v[166:167], 0, s[0:1]
	v_lshl_add_u64 v[100:101], v[152:153], 0, s[0:1]
	v_lshl_add_u64 v[106:107], v[156:157], 0, s[0:1]
	v_lshl_add_u64 v[108:109], v[158:159], 0, s[0:1]
	v_lshl_add_u64 v[110:111], v[160:161], 0, s[0:1]
	v_lshl_add_u64 v[112:113], v[162:163], 0, s[0:1]
	global_load_dwordx4 v[118:121], v[98:99], off nt
	global_load_dwordx4 v[134:137], v[100:101], off nt
	global_load_dwordx4 v[150:153], v[106:107], off nt
	global_load_dwordx4 v[156:159], v[108:109], off nt
	global_load_dwordx4 v[160:163], v[110:111], off nt
	global_load_dwordx4 v[164:167], v[112:113], off nt
	s_nop 0
	global_load_dwordx4 v[192:195], v[192:193], off nt
	s_nop 0
	global_load_dwordx4 v[196:199], v[196:197], off nt
	v_mov_b32_e32 v98, v188
	s_waitcnt vmcnt(15)
	s_waitcnt vmcnt(14)
	s_waitcnt vmcnt(13)
	s_waitcnt vmcnt(12)
	s_waitcnt vmcnt(11)
	s_waitcnt vmcnt(10)
	s_waitcnt vmcnt(9)
	s_waitcnt vmcnt(8)
	ds_read_b32 v98, v187
	s_waitcnt lgkmcnt(0)
	v_pk_fma_f32 v[100:101], v[98:99], v[146:147], 0 op_sel_hi:[0,1,0] neg_lo:[1,0,0] neg_hi:[1,0,0]
	v_pk_fma_f32 v[98:99], v[98:99], v[148:149], 0 op_sel_hi:[0,1,0] neg_lo:[1,0,0] neg_hi:[1,0,0]
	v_cvt_pk_bf16_f32 v100, v100, v101
	v_cvt_pk_bf16_f32 v101, v98, v99
	ds_write_b64 v186, v[100:101]
	ds_read_b32 v98, v187 offset:8
	s_waitcnt lgkmcnt(0)
	v_pk_fma_f32 v[100:101], v[98:99], v[142:143], 0 op_sel_hi:[0,1,0] neg_lo:[1,0,0] neg_hi:[1,0,0]
	v_pk_fma_f32 v[98:99], v[98:99], v[144:145], 0 op_sel_hi:[0,1,0] neg_lo:[1,0,0] neg_hi:[1,0,0]
	v_cvt_pk_bf16_f32 v100, v100, v101
	v_cvt_pk_bf16_f32 v101, v98, v99
	ds_write_b64 v186, v[100:101] offset:544
	ds_read_b32 v98, v187 offset:16
	s_waitcnt lgkmcnt(0)
	v_pk_fma_f32 v[100:101], v[98:99], v[138:139], 0 op_sel_hi:[0,1,0] neg_lo:[1,0,0] neg_hi:[1,0,0]
	v_pk_fma_f32 v[98:99], v[98:99], v[140:141], 0 op_sel_hi:[0,1,0] neg_lo:[1,0,0] neg_hi:[1,0,0]
	v_cvt_pk_bf16_f32 v100, v100, v101
	v_cvt_pk_bf16_f32 v101, v98, v99
	ds_write_b64 v186, v[100:101] offset:1088
	ds_read_b32 v98, v187 offset:24
	s_waitcnt lgkmcnt(0)
	v_pk_fma_f32 v[100:101], v[98:99], v[130:131], 0 op_sel_hi:[0,1,0] neg_lo:[1,0,0] neg_hi:[1,0,0]
	v_pk_fma_f32 v[98:99], v[98:99], v[132:133], 0 op_sel_hi:[0,1,0] neg_lo:[1,0,0] neg_hi:[1,0,0]
	v_cvt_pk_bf16_f32 v100, v100, v101
	v_cvt_pk_bf16_f32 v101, v98, v99
	ds_write_b64 v186, v[100:101] offset:1632
	ds_read_b32 v98, v187 offset:32
	s_waitcnt lgkmcnt(0)
	v_pk_fma_f32 v[100:101], v[98:99], v[126:127], 0 op_sel_hi:[0,1,0] neg_lo:[1,0,0] neg_hi:[1,0,0]
	v_pk_fma_f32 v[98:99], v[98:99], v[128:129], 0 op_sel_hi:[0,1,0] neg_lo:[1,0,0] neg_hi:[1,0,0]
	v_cvt_pk_bf16_f32 v100, v100, v101
	v_cvt_pk_bf16_f32 v101, v98, v99
	ds_write_b64 v186, v[100:101] offset:2176
	ds_read_b32 v98, v187 offset:40
	s_waitcnt lgkmcnt(0)
	v_pk_fma_f32 v[100:101], v[98:99], v[122:123], 0 op_sel_hi:[0,1,0] neg_lo:[1,0,0] neg_hi:[1,0,0]
	v_pk_fma_f32 v[98:99], v[98:99], v[124:125], 0 op_sel_hi:[0,1,0] neg_lo:[1,0,0] neg_hi:[1,0,0]
	v_cvt_pk_bf16_f32 v100, v100, v101
	v_cvt_pk_bf16_f32 v101, v98, v99
	ds_write_b64 v186, v[100:101] offset:2720
	ds_read_b32 v98, v187 offset:48
	s_waitcnt lgkmcnt(0)
	v_pk_fma_f32 v[100:101], v[98:99], v[114:115], 0 op_sel_hi:[0,1,0] neg_lo:[1,0,0] neg_hi:[1,0,0]
	v_pk_fma_f32 v[98:99], v[98:99], v[116:117], 0 op_sel_hi:[0,1,0] neg_lo:[1,0,0] neg_hi:[1,0,0]
	v_cvt_pk_bf16_f32 v100, v100, v101
	v_cvt_pk_bf16_f32 v101, v98, v99
	ds_write_b64 v186, v[100:101] offset:3264
	ds_read_b32 v98, v187 offset:56
	s_waitcnt lgkmcnt(0)
	v_pk_fma_f32 v[100:101], v[98:99], v[102:103], 0 op_sel_hi:[0,1,0] neg_lo:[1,0,0] neg_hi:[1,0,0]
	v_pk_fma_f32 v[98:99], v[98:99], v[104:105], 0 op_sel_hi:[0,1,0] neg_lo:[1,0,0] neg_hi:[1,0,0]
	v_cvt_pk_bf16_f32 v100, v100, v101
	v_cvt_pk_bf16_f32 v101, v98, v99
	ds_write_b64 v186, v[100:101] offset:3808
	ds_read_b128 v[98:101], v1
	ds_read_b128 v[102:105], v1 offset:64
	ds_read_b128 v[106:109], v1 offset:128
	ds_read_b128 v[110:113], v1 offset:192
	v_lshl_add_u64 v[114:115], v[168:169], 0, s[0:1]
	v_lshl_add_u64 v[126:127], v[176:177], 0, s[0:1]
	v_lshl_add_u64 v[176:177], v[180:181], 0, s[0:1]
	v_lshl_add_u64 v[180:181], v[182:183], 0, s[0:1]
	v_lshl_add_u64 v[116:117], v[170:171], 0, s[0:1]
	v_lshl_add_u64 v[122:123], v[172:173], 0, s[0:1]
	v_lshl_add_u64 v[124:125], v[174:175], 0, s[0:1]
	v_lshl_add_u64 v[128:129], v[178:179], 0, s[0:1]
	global_load_dwordx4 v[130:133], v[114:115], off nt
	global_load_dwordx4 v[138:141], v[116:117], off nt
	global_load_dwordx4 v[142:145], v[122:123], off nt
	global_load_dwordx4 v[146:149], v[124:125], off nt
	global_load_dwordx4 v[168:171], v[126:127], off nt
	global_load_dwordx4 v[172:175], v[128:129], off nt
	s_nop 0
	global_load_dwordx4 v[176:179], v[176:177], off nt
	s_nop 0
	global_load_dwordx4 v[180:183], v[180:181], off nt
	v_mov_b32_e32 v114, v188
	s_waitcnt vmcnt(15)
	s_waitcnt vmcnt(14)
	s_waitcnt vmcnt(13)
	s_waitcnt vmcnt(12)
	s_waitcnt vmcnt(11)
	s_waitcnt vmcnt(10)
	s_waitcnt vmcnt(9)
	s_waitcnt vmcnt(8)
	ds_read_b32 v114, v187 offset:64
	s_waitcnt lgkmcnt(0)
	v_pk_fma_f32 v[116:117], v[114:115], v[118:119], 0 op_sel_hi:[0,1,0] neg_lo:[1,0,0] neg_hi:[1,0,0]
	v_pk_fma_f32 v[114:115], v[114:115], v[120:121], 0 op_sel_hi:[0,1,0] neg_lo:[1,0,0] neg_hi:[1,0,0]
	v_cvt_pk_bf16_f32 v116, v116, v117
	v_cvt_pk_bf16_f32 v117, v114, v115
	ds_write_b64 v186, v[116:117]
	ds_read_b32 v114, v187 offset:72
	s_waitcnt lgkmcnt(0)
	v_pk_fma_f32 v[116:117], v[114:115], v[134:135], 0 op_sel_hi:[0,1,0] neg_lo:[1,0,0] neg_hi:[1,0,0]
	v_pk_fma_f32 v[114:115], v[114:115], v[136:137], 0 op_sel_hi:[0,1,0] neg_lo:[1,0,0] neg_hi:[1,0,0]
	v_cvt_pk_bf16_f32 v116, v116, v117
	v_cvt_pk_bf16_f32 v117, v114, v115
	ds_write_b64 v186, v[116:117] offset:544
	ds_read_b32 v114, v187 offset:80
	s_waitcnt lgkmcnt(0)
	v_pk_fma_f32 v[116:117], v[114:115], v[150:151], 0 op_sel_hi:[0,1,0] neg_lo:[1,0,0] neg_hi:[1,0,0]
	v_pk_fma_f32 v[114:115], v[114:115], v[152:153], 0 op_sel_hi:[0,1,0] neg_lo:[1,0,0] neg_hi:[1,0,0]
	v_cvt_pk_bf16_f32 v116, v116, v117
	v_cvt_pk_bf16_f32 v117, v114, v115
	ds_write_b64 v186, v[116:117] offset:1088
	ds_read_b32 v114, v187 offset:88
	s_waitcnt lgkmcnt(0)
	v_pk_fma_f32 v[116:117], v[114:115], v[156:157], 0 op_sel_hi:[0,1,0] neg_lo:[1,0,0] neg_hi:[1,0,0]
	v_pk_fma_f32 v[114:115], v[114:115], v[158:159], 0 op_sel_hi:[0,1,0] neg_lo:[1,0,0] neg_hi:[1,0,0]
	v_cvt_pk_bf16_f32 v116, v116, v117
	v_cvt_pk_bf16_f32 v117, v114, v115
	ds_write_b64 v186, v[116:117] offset:1632
	ds_read_b32 v114, v187 offset:96
	s_waitcnt lgkmcnt(0)
	v_pk_fma_f32 v[116:117], v[114:115], v[160:161], 0 op_sel_hi:[0,1,0] neg_lo:[1,0,0] neg_hi:[1,0,0]
	v_pk_fma_f32 v[114:115], v[114:115], v[162:163], 0 op_sel_hi:[0,1,0] neg_lo:[1,0,0] neg_hi:[1,0,0]
	v_cvt_pk_bf16_f32 v116, v116, v117
	v_cvt_pk_bf16_f32 v117, v114, v115
	ds_write_b64 v186, v[116:117] offset:2176
	ds_read_b32 v114, v187 offset:104
	s_waitcnt lgkmcnt(0)
	v_pk_fma_f32 v[116:117], v[114:115], v[164:165], 0 op_sel_hi:[0,1,0] neg_lo:[1,0,0] neg_hi:[1,0,0]
	v_pk_fma_f32 v[114:115], v[114:115], v[166:167], 0 op_sel_hi:[0,1,0] neg_lo:[1,0,0] neg_hi:[1,0,0]
	v_cvt_pk_bf16_f32 v116, v116, v117
	v_cvt_pk_bf16_f32 v117, v114, v115
	ds_write_b64 v186, v[116:117] offset:2720
	ds_read_b32 v114, v187 offset:112
	s_waitcnt lgkmcnt(0)
	v_pk_fma_f32 v[116:117], v[114:115], v[192:193], 0 op_sel_hi:[0,1,0] neg_lo:[1,0,0] neg_hi:[1,0,0]
	v_pk_fma_f32 v[114:115], v[114:115], v[194:195], 0 op_sel_hi:[0,1,0] neg_lo:[1,0,0] neg_hi:[1,0,0]
	v_cvt_pk_bf16_f32 v116, v116, v117
	v_cvt_pk_bf16_f32 v117, v114, v115
	ds_write_b64 v186, v[116:117] offset:3264
	ds_read_b32 v114, v187 offset:120
	s_waitcnt lgkmcnt(0)
	v_pk_fma_f32 v[116:117], v[114:115], v[196:197], 0 op_sel_hi:[0,1,0] neg_lo:[1,0,0] neg_hi:[1,0,0]
	v_pk_fma_f32 v[114:115], v[114:115], v[198:199], 0 op_sel_hi:[0,1,0] neg_lo:[1,0,0] neg_hi:[1,0,0]
	v_cvt_pk_bf16_f32 v116, v116, v117
	v_cvt_pk_bf16_f32 v117, v114, v115
	ds_write_b64 v186, v[116:117] offset:3808
	ds_read_b128 v[114:117], v1
	ds_read_b128 v[118:121], v1 offset:64
	ds_read_b128 v[122:125], v1 offset:128
	ds_read_b128 v[126:129], v1 offset:192
	s_waitcnt vmcnt(7)
	s_waitcnt vmcnt(6)
	s_waitcnt vmcnt(5)
	s_waitcnt vmcnt(4)
	s_waitcnt vmcnt(3)
	s_waitcnt vmcnt(2)
	s_waitcnt vmcnt(1)
	s_waitcnt vmcnt(0)
	ds_read_b32 v134, v187 offset:128
	s_waitcnt lgkmcnt(0)
	v_pk_fma_f32 v[130:131], v[134:135], v[130:131], 0 op_sel_hi:[0,1,0] neg_lo:[1,0,0] neg_hi:[1,0,0]
	v_pk_fma_f32 v[132:133], v[134:135], v[132:133], 0 op_sel_hi:[0,1,0] neg_lo:[1,0,0] neg_hi:[1,0,0]
	v_cvt_pk_bf16_f32 v130, v130, v131
	v_cvt_pk_bf16_f32 v131, v132, v133
	ds_write_b64 v186, v[130:131]
	ds_read_b32 v130, v187 offset:136
	s_waitcnt lgkmcnt(0)
	v_pk_fma_f32 v[132:133], v[130:131], v[138:139], 0 op_sel_hi:[0,1,0] neg_lo:[1,0,0] neg_hi:[1,0,0]
	v_pk_fma_f32 v[130:131], v[130:131], v[140:141], 0 op_sel_hi:[0,1,0] neg_lo:[1,0,0] neg_hi:[1,0,0]
	v_cvt_pk_bf16_f32 v132, v132, v133
	v_cvt_pk_bf16_f32 v133, v130, v131
	ds_write_b64 v186, v[132:133] offset:544
	ds_read_b32 v130, v187 offset:144
	s_waitcnt lgkmcnt(0)
	v_pk_fma_f32 v[132:133], v[130:131], v[142:143], 0 op_sel_hi:[0,1,0] neg_lo:[1,0,0] neg_hi:[1,0,0]
	v_pk_fma_f32 v[130:131], v[130:131], v[144:145], 0 op_sel_hi:[0,1,0] neg_lo:[1,0,0] neg_hi:[1,0,0]
	v_cvt_pk_bf16_f32 v132, v132, v133
	v_cvt_pk_bf16_f32 v133, v130, v131
	ds_write_b64 v186, v[132:133] offset:1088
	ds_read_b32 v130, v187 offset:152
	s_waitcnt lgkmcnt(0)
	v_pk_fma_f32 v[132:133], v[130:131], v[146:147], 0 op_sel_hi:[0,1,0] neg_lo:[1,0,0] neg_hi:[1,0,0]
	v_pk_fma_f32 v[130:131], v[130:131], v[148:149], 0 op_sel_hi:[0,1,0] neg_lo:[1,0,0] neg_hi:[1,0,0]
	v_cvt_pk_bf16_f32 v132, v132, v133
	v_cvt_pk_bf16_f32 v133, v130, v131
	ds_write_b64 v186, v[132:133] offset:1632
	ds_read_b32 v130, v187 offset:160
	s_waitcnt lgkmcnt(0)
	v_pk_fma_f32 v[132:133], v[130:131], v[168:169], 0 op_sel_hi:[0,1,0] neg_lo:[1,0,0] neg_hi:[1,0,0]
	v_pk_fma_f32 v[130:131], v[130:131], v[170:171], 0 op_sel_hi:[0,1,0] neg_lo:[1,0,0] neg_hi:[1,0,0]
	v_cvt_pk_bf16_f32 v132, v132, v133
	v_cvt_pk_bf16_f32 v133, v130, v131
	ds_write_b64 v186, v[132:133] offset:2176
	ds_read_b32 v130, v187 offset:168
	s_waitcnt lgkmcnt(0)
	v_pk_fma_f32 v[132:133], v[130:131], v[172:173], 0 op_sel_hi:[0,1,0] neg_lo:[1,0,0] neg_hi:[1,0,0]
	v_pk_fma_f32 v[130:131], v[130:131], v[174:175], 0 op_sel_hi:[0,1,0] neg_lo:[1,0,0] neg_hi:[1,0,0]
	v_cvt_pk_bf16_f32 v132, v132, v133
	v_cvt_pk_bf16_f32 v133, v130, v131
	ds_write_b64 v186, v[132:133] offset:2720
	ds_read_b32 v130, v187 offset:176
	s_waitcnt lgkmcnt(0)
	v_pk_fma_f32 v[132:133], v[130:131], v[176:177], 0 op_sel_hi:[0,1,0] neg_lo:[1,0,0] neg_hi:[1,0,0]
	v_pk_fma_f32 v[130:131], v[130:131], v[178:179], 0 op_sel_hi:[0,1,0] neg_lo:[1,0,0] neg_hi:[1,0,0]
	v_cvt_pk_bf16_f32 v132, v132, v133
	v_cvt_pk_bf16_f32 v133, v130, v131
	ds_write_b64 v186, v[132:133] offset:3264
	ds_read_b32 v130, v187 offset:184
	s_waitcnt lgkmcnt(0)
	v_pk_fma_f32 v[132:133], v[130:131], v[180:181], 0 op_sel_hi:[0,1,0] neg_lo:[1,0,0] neg_hi:[1,0,0]
	v_pk_fma_f32 v[130:131], v[130:131], v[182:183], 0 op_sel_hi:[0,1,0] neg_lo:[1,0,0] neg_hi:[1,0,0]
	v_cvt_pk_bf16_f32 v132, v132, v133
	v_cvt_pk_bf16_f32 v133, v130, v131
	ds_write_b64 v186, v[132:133] offset:3808
	ds_read_b128 v[130:133], v1
	ds_read_b128 v[134:137], v1 offset:64
	ds_read_b128 v[138:141], v1 offset:128
	ds_read_b128 v[142:145], v1 offset:192
	s_ashr_i32 s7, s6, 31
	s_lshl_b64 s[0:1], s[6:7], 2
	s_add_u32 s0, s4, s0
	s_addc_u32 s1, s5, s1
	v_lshlrev_b32_e32 v1, 4, v0
	s_add_i32 s20, s34, 1
	s_add_i32 s34, s34, -1
	v_or_b32_e32 v153, s10, v206
	s_xor_b32 s26, s3, 2
	s_lshl_b64 s[10:11], s[10:11], 3
	s_and_b32 s20, s20, 3
	s_and_b32 s27, s34, 3
	s_add_u32 s10, s14, s10
	s_addc_u32 s11, s15, s11
	s_lshl_b32 s42, s35, 2
	s_add_i32 s41, s42, 0x26a20
	s_add_i32 s42, s42, 0x26a00
	v_lshlrev_b32_e32 v190, 3, v206
	s_cmp_eq_u32 s35, 3
	v_lshlrev_b32_e32 v150, 3, v0
	v_and_b32_e32 v151, 1, v0
	v_lshl_add_u64 v[0:1], v[154:155], 3, s[14:15]
	v_lshl_add_u64 v[192:193], s[10:11], 0, v[190:191]
	s_cselect_b64 s[10:11], -1, 0
	s_lshl_b32 s14, s3, 2
	s_add_u32 s24, s16, s14
	v_or_b32_e32 v155, 0x20000, v150
	v_add_u32_e32 v156, 0x20880, v150
	v_lshlrev_b32_e32 v150, 1, v153
	s_addc_u32 s25, s17, 0
	s_lshl_b32 s43, s3, 9
	v_lshl_add_u32 v212, s26, 9, v150
	s_lshl_b32 s15, s26, 8
	s_add_i32 s26, s43, 0x200
	v_mov_b32_e32 v152, 0x880
	v_cmp_lt_u32_e64 s[0:1], 15, v206
	v_cmp_eq_u32_e32 vcc, 1, v151
	s_and_b32 s45, s26, 0x600
	s_add_i32 s26, s43, 0x500
	v_cndmask_b32_e32 v211, 0, v152, vcc
	s_and_b32 s56, s26, 0x700
	s_add_i32 s26, s43, 0x540
	v_lshl_add_u32 v213, s20, 9, v150
	v_lshl_add_u32 v214, s27, 9, v150
	s_and_b32 s57, s26, 0x740
	s_add_i32 s26, s43, 0x580
	s_and_b32 s58, s26, 0x780
	s_add_i32 s26, s43, 0x5c0
	s_and_b32 s59, s26, 0x7c0
	s_add_i32 s26, s43, 0x600
	s_and_b32 s60, s26, 0x600
	s_add_i32 s26, s43, 0x640
	s_and_b32 s61, s26, 0x640
	s_add_i32 s26, s43, 0x680
	s_and_b32 s62, s26, 0x680
	s_add_i32 s26, s43, 0x6c0
	s_and_b32 s63, s26, 0x6c0
	s_add_i32 s26, s43, 0x700
	s_and_b32 s64, s26, 0x700
	s_add_i32 s26, s43, 0x740
	s_and_b32 s65, s26, 0x740
	s_add_i32 s26, s43, 0x780
	s_lshl_b32 s14, s27, 8
	s_lshl_b32 s20, s20, 8
	s_add_i32 s27, s43, 0x240
	s_add_i32 s28, s43, 0x280
	s_add_i32 s29, s43, 0x2c0
	s_add_i32 s30, s43, 0x300
	s_add_i32 s31, s43, 0x340
	s_add_i32 s34, s43, 0x380
	s_add_i32 s35, s43, 0x3c0
	s_add_i32 s36, s43, 0x440
	s_add_i32 s37, s43, 0x480
	s_add_i32 s38, s43, 0x4c0
	s_and_b32 s66, s26, 0x780
	s_add_i32 s26, s43, 0x7c0
	s_mul_hi_i32 s23, s18, 0x65
	s_mul_i32 s22, s18, 0x65
	v_cmp_eq_u32_e64 s[4:5], 1, v185
	v_cmp_eq_u32_e64 s[6:7], 2, v185
	v_cmp_eq_u32_e64 s[8:9], 63, v206
	s_xor_b32 s44, s43, 0x400
	s_and_b32 s46, s27, 0x640
	s_and_b32 s47, s28, 0x680
	s_waitcnt lgkmcnt(0)
	v_mov_b32_e32 v146, 0x20000
	s_and_b32 s48, s29, 0x6c0
	s_and_b32 s49, s30, 0x700
	s_and_b32 s50, s31, 0x740
	s_and_b32 s51, s34, 0x780
	s_and_b32 s52, s35, 0x7c0
	s_and_b32 s53, s36, 0x640
	s_and_b32 s54, s37, 0x680
	s_and_b32 s55, s38, 0x6c0
	s_and_b32 s67, s26, 0x7c0
	s_and_b64 s[26:27], s[10:11], s[12:13]
	v_lshl_add_u32 v215, v154, 1, v146
	v_mov_b32_e32 v216, 1
	s_lshl_b32 s28, s14, 3
	s_lshl_b32 s30, s15, 3
	s_lshl_b32 s34, s20, 3
	s_movk_i32 s68, 0x7fff
	s_mov_b32 s69, 0
	v_and_b32_e32 v220, 24, v206
	v_lshlrev_b32_e32 v220, 2, v220
	v_and_b32_e32 v221, 2, v206
	v_lshl_or_b32 v220, v221, 3, v220
	v_and_b32_e32 v221, 32, v206
	v_lshrrev_b32_e32 v221, 2, v221
	v_or_b32_e32 v220, v220, v221
	v_and_b32_e32 v221, 4, v206
	v_or_b32_e32 v220, v220, v221
	v_and_b32_e32 v221, 1, v206
	v_lshl_or_b32 v220, v221, 1, v220
	v_mov_b32_e32 v220, v254
	s_lshr_b32 s76, s19, 8
	s_add_i32 s76, s76, 0x20000
	v_add_u32_e32 v220, s76, v220
	v_add_u32_e32 v225, s45, v220
	v_add_u32_e32 v226, s44, v220
	v_add_u32_e32 v227, s60, v220
	v_add_u32_e32 v228, s43, v220
	v_and_b32_e32 v221, 1, v206
	v_mul_u32_u24_e32 v221, 0x880, v221
	v_lshrrev_b32_e32 v220, 4, v206
	v_lshl_add_u32 v221, v220, 5, v221
	v_and_b32_e32 v220, 2, v206
	v_lshl_add_u32 v221, v220, 3, v221
	v_add_u32_e32 v222, 0x20000, v221
	v_cmp_ne_u32_e32 vcc, 0, v220
	v_mov_b32_e32 v220, 0x44444444
	v_mov_b32_e32 v221, 0xeeeeeeee
	s_nop 1
	v_cndmask_b32_e32 v223, v220, v221, vcc
	v_cmp_lt_u32_e64 s[74:75], 47, v206
	v_mov_b32_e32 v224, v184
	s_lshr_b32 s78, s19, 15
	s_lshl_b32 s79, s78, 11
	v_add_u32_e32 v255, s79, v224
	ds_read_b128 v[166:169], v224 offset:0
	ds_read_b128 v[170:173], v224 offset:1024
	ds_read_b128 v[174:177], v224 offset:2048
	ds_read_b128 v[178:181], v224 offset:3072
	ds_read_b128 v[182:185], v224 offset:4096
	ds_read_b128 v[186:189], v224 offset:5120
	s_mov_b32 s20, 0
